# P3 low-rank stage loads batched under one wait, P11 tail loads hoisted, swiglu constants folded, scan compute waves prio
# speedup vs baseline: 1.0040x; 1.0040x over previous
; #define LAS __attribute__((address_space(3)))
; __device__ __forceinline__ unsigned cvt_pk_bf16(float lo, float hi) { unsigned r; asm volatile("v_cvt_pk_bf16_f32 %0, %1, %2" : "=v"(r) : "v"(lo), "v"(hi)); return r; }
; __device__ __forceinline__ f32x4 ld_bf4(const bf16_t* p) { const u32x2 w = *(const u32x2*)p; return (f32x4){__builtin_bit_cast(float, w.x << 16), __builtin_bit_cast(float, w.x & 0xffff0000u), __builtin_bit_cast(float, w.y << 16), __builtin_bit_cast(float, w.y & 0xffff0000u)}; }
; __device__ __forceinline__ f32x4 sig4(f32x4 x) { return (f32x4){sigmoidf_(x.x), sigmoidf_(x.y), sigmoidf_(x.z), sigmoidf_(x.w)}; }
; __device__ __forceinline__ f32x4 qshift4(const bf16_t* P, const float* mu, int gr, bool hp, bool hn, int col) {
;     const bf16_t* pr = P + (size_t)gr * P_PAD + Q0 + col;
;     const f32x4 c = ld_bf4(pr); const f32x4 z = (f32x4){0.f, 0.f, 0.f, 0.f};
;     const f32x4 pv = hp ? ld_bf4(pr - P_PAD) : z, nx = hn ? ld_bf4(pr + P_PAD) : z;
;     const f32x4 m0 = *(const f32x4*)(mu + col), m1 = *(const f32x4*)(mu + P_RWKV + col);
;     return c + m0 * (pv - c) + m1 * (nx - c);
; }
; __device__ __forceinline__ void p3_inputs(Frame& F) {
;     ...
;         for (int i = F.tid; i < 16 * (LOWW / 4); i += NTHR) { const int tk = i / (LOWW / 4), c4 = (i % (LOWW / 4)) * 4, col = c4 < 256 ? 2048 + c4 : 3328 + (c4 - 256);
;             f32x4 qv = qshift4(P, mu, row0 + tk, row0 + tk > s0, row0 + tk + 1 < s1, col);
;             if (c4 < 128) qv = (f32x4){1.0f - 2.0f * __builtin_amdgcn_rcpf(1.0f + __expf(2.0f * qv.x)), 1.0f - 2.0f * __builtin_amdgcn_rcpf(1.0f + __expf(2.0f * qv.y)), 1.0f - 2.0f * __builtin_amdgcn_rcpf(1.0f + __expf(2.0f * qv.z)), 1.0f - 2.0f * __builtin_amdgcn_rcpf(1.0f + __expf(2.0f * qv.w))};
;             else if (c4 >= 256) qv = sig4(qv);
;             u32x2 w; w.x = pg8::cvt_pk_bf16(qv.x, qv.y); w.y = pg8::cvt_pk_bf16(qv.z, qv.w); *(LAS u32x2*)(low + tk * LOWP + c4) = w; }
.LBB0_397:
	s_mov_b32 s2, 0x4ec4ec4f
	s_waitcnt lgkmcnt(1)
	v_mul_hi_u32 v4, v2, s2
	v_lshrrev_b32_e32 v11, 5, v4
	s_movk_i32 s2, 0x1a0
	v_mul_lo_u32 v4, v11, s2
	s_movk_i32 s2, 0xff98
	v_sub_u32_e32 v6, v10, v4
	s_waitcnt lgkmcnt(0)
	v_mad_u64_u32 v[4:5], s[2:3], v11, s2, v[2:3]
	v_cmp_gt_u32_e32 vcc, 64, v4
	v_add_u32_e32 v16, s10, v11
	v_mov_b32_e32 v12, 0
	v_cndmask_b32_e32 v5, v221, v222, vcc
	v_add_u32_e32 v140, v5, v6
	v_mad_i64_i32 v[6:7], s[2:3], v16, s61, v[144:145]
	v_lshl_add_u64 v[8:9], v[140:141], 1, v[6:7]
	v_add_co_u32_e32 v6, vcc, 0x1000, v8
	v_mov_b32_e32 v5, 0
	s_nop 0
	v_addc_co_u32_e32 v7, vcc, 0, v9, vcc
	global_load_dwordx2 v[6:7], v[6:7], off offset:2048
	v_cmp_lt_i32_e64 s[98:99], s11, v16
	v_lshl_add_u64 v[8:9], v[8:9], 0, s[42:43]
	v_mov_b32_e32 v14, 0
	v_mov_b32_e32 v13, 0
	v_mov_b32_e32 v15, 0
	s_and_saveexec_b64 s[2:3], s[98:99]
	v_add_co_u32_e32 v12, vcc, 0xffffd000, v8
	s_nop 1
	v_addc_co_u32_e32 v13, vcc, -1, v9, vcc
	global_load_dwordx2 v[92:93], v[12:13], off offset:-1152
	s_or_b64 exec, exec, s[2:3]
	v_add_u32_e32 v16, 1, v16
	v_cmp_gt_i32_e64 s[100:101], s33, v16
	v_mov_b32_e32 v17, 0
	v_mov_b32_e32 v16, 0
	v_mov_b32_e32 v18, 0
	s_and_saveexec_b64 s[2:3], s[100:101]
	v_add_co_u32_e32 v8, vcc, 0x3000, v8
	s_nop 1
	v_addc_co_u32_e32 v9, vcc, 0, v9, vcc
	global_load_dwordx2 v[94:95], v[8:9], off offset:1152
	s_or_b64 exec, exec, s[2:3]
	v_lshlrev_b64 v[8:9], 2, v[140:141]
	v_lshl_add_u64 v[20:21], s[54:55], 0, v[8:9]
	global_load_dwordx4 v[20:23], v[20:21], off
	v_lshl_add_u64 v[8:9], s[18:19], 0, v[8:9]
	global_load_dwordx4 v[24:27], v[8:9], off
	s_waitcnt vmcnt(0)
	s_and_saveexec_b64 s[2:3], s[98:99]
	v_lshlrev_b32_e32 v12, 16, v92
	v_and_b32_e32 v14, 0xffff0000, v92
	v_lshlrev_b32_e32 v13, 16, v93
	v_and_b32_e32 v15, 0xffff0000, v93
	s_or_b64 exec, exec, s[2:3]
	s_and_saveexec_b64 s[2:3], s[100:101]
	v_lshlrev_b32_e32 v5, 16, v94
	v_and_b32_e32 v17, 0xffff0000, v94
	v_lshlrev_b32_e32 v16, 16, v95
	v_and_b32_e32 v18, 0xffff0000, v95
	s_or_b64 exec, exec, s[2:3]
	s_waitcnt vmcnt(2)
	v_lshlrev_b32_e32 v8, 16, v6
	v_and_b32_e32 v9, 0xffff0000, v6
	v_lshlrev_b32_e32 v6, 16, v7
	v_and_b32_e32 v7, 0xffff0000, v7
	v_sub_f32_e32 v29, v14, v9
	v_sub_f32_e32 v28, v12, v8
	v_sub_f32_e32 v15, v15, v7
	v_sub_f32_e32 v14, v13, v6
	v_sub_f32_e32 v13, v17, v9
	v_sub_f32_e32 v12, v5, v8
	v_sub_f32_e32 v17, v18, v7
	v_sub_f32_e32 v16, v16, v6
	v_cmp_lt_u32_e32 vcc, 31, v4
	s_waitcnt vmcnt(1)
	v_pk_fma_f32 v[6:7], v[14:15], v[22:23], v[6:7]
	v_pk_fma_f32 v[8:9], v[28:29], v[20:21], v[8:9]
	s_waitcnt vmcnt(0)
	v_pk_fma_f32 v[6:7], v[16:17], v[26:27], v[6:7]
	v_pk_fma_f32 v[8:9], v[12:13], v[24:25], v[8:9]
	s_and_saveexec_b64 s[2:3], vcc
	s_xor_b64 s[2:3], exec, s[2:3]
	s_cbranch_execz .LBB0_405
	v_cmp_lt_u32_e32 vcc, 63, v4
	s_and_saveexec_b64 s[8:9], vcc
	s_cbranch_execz .LBB0_404
	v_mul_f32_e32 v4, 0xbfb8aa3b, v8
	v_exp_f32_e32 v4, v4
	v_mul_f32_e32 v5, 0xbfb8aa3b, v9
	v_exp_f32_e32 v5, v5
	v_add_f32_e32 v4, 1.0, v4
	v_rcp_f32_e32 v8, v4
	v_mul_f32_e32 v4, 0xbfb8aa3b, v6
	v_exp_f32_e32 v4, v4
	v_mul_f32_e32 v6, 0xbfb8aa3b, v7
	v_exp_f32_e32 v7, v6
	v_add_f32_e32 v5, 1.0, v5
	v_add_f32_e32 v4, 1.0, v4
	v_rcp_f32_e32 v6, v4
	v_add_f32_e32 v4, 1.0, v7
	v_rcp_f32_e32 v9, v5
	v_rcp_f32_e32 v7, v4

; #define LAS __attribute__((address_space(3)))
; #define P4_RDSET(P, base_, boff_, vo_, vt_, voff_) do { P##w = lds_rd128<(boff_)>(base_); P##a = lds_rd128<(boff_) + SB * 256>(base_); P##b = lds_rd128<(boff_) + 2 * SB * 256>(base_); \
;                     P##k = lds_rd128<(boff_) + 3 * SB * 256>(base_); P##r = lds_rd128<(boff_) + 4 * SB * 256>(base_); P##vo = lds_rd32<(voff_)>(vo_); P##vt = lds_rd32<(voff_)>(vt_); } while (0)
; __device__ __forceinline__ void p4_scan(Frame& F) {
;     ...
;             const int g = F.lane >> 4, kap = F.lane & 15, rown = 8 * F.wave + 2 * g + (kap & 1), roth = rown ^ 1;
;             f32x2 s0 = {0.f, 0.f}, s1 = {0.f, 0.f}, s2 = {0.f, 0.f}, s3 = {0.f, 0.f};
;             asm volatile("s_waitcnt lgkmcnt(0)" ::: "memory"); __builtin_amdgcn_s_barrier(); asm volatile("" ::: "memory");
;             for (int blk = 0; blk < NBLK; ++blk) {
;                 const LAS unsigned char* sb = F.lds + (blk & 1) * SLOT_BYTES;
;                 LAS float* yb = (LAS float*)(F.lds + YB_OFF + (blk & 1) * YB_BYTES);
;                 const unsigned aK = (unsigned)(size_t)(sb) + kap * 16, aVo = (unsigned)(size_t)(sb) + 5 * (SB * 256) + rown * 4, aVt = (unsigned)(size_t)(sb) + 5 * (SB * 256) + roth * 4;
;                 f32x4 cw, ca, cb, ck, cr; float cvo, cvt;
;     ...
;                 P4_RDSET(c, aK, 0, aVo, aVt, 0);
;                 asm volatile("s_waitcnt lgkmcnt(0)" : P4_TIE(c));
.LBB0_487:
	s_mov_b64 s[2:3], -1
	s_and_b64 vcc, exec, s[30:31]
	s_waitcnt vmcnt(0)
	s_barrier
	s_cbranch_vccz .LBB0_491
	s_waitcnt lgkmcnt(0)
	s_barrier
	s_setprio 3
	v_mov_b32_e32 v70, 0
	s_mov_b32 s2, 0
	v_mov_b32_e32 v71, v70
	v_mov_b32_e32 v72, v70
	v_mov_b32_e32 v73, v70
	v_mov_b32_e32 v74, v70
	v_mov_b32_e32 v75, v70
	v_mov_b32_e32 v76, v70
	v_mov_b32_e32 v77, v70
.LBB0_489:
	s_and_b32 s3, s2, 1
	s_mul_i32 s22, s3, 0xb000
	v_lshl_add_u32 v78, s3, 12, v155
	s_add_i32 s3, s22, 0
	v_add_u32_e32 v79, s3, v91
	s_add_i32 s3, s3, 0xa000
	v_add_u32_e32 v80, s3, v99
	v_add_u32_e32 v81, s3, v103
	ds_read_b128 v[82:85], v79 offset:0
	ds_read_b128 v[86:89], v79 offset:0x2000
	ds_read_b128 v[114:117], v79 offset:0x4000
	ds_read_b128 v[118:121], v79 offset:0x6000
	ds_read_b128 v[122:125], v79 offset:0x8000
	ds_read_b32 v126, v80 offset:0
	ds_read_b32 v127, v81 offset:0
	s_add_i32 s2, s2, 1
	s_waitcnt lgkmcnt(0)
	ds_read_b128 v[162:165], v79 offset:0x100
	ds_read_b128 v[166:169], v79 offset:0x2100
	ds_read_b128 v[170:173], v79 offset:0x4100
	ds_read_b128 v[174:177], v79 offset:0x6100
	ds_read_b128 v[178:181], v79 offset:0x8100
	ds_read_b32 v182, v80 offset:0x80
	ds_read_b32 v183, v81 offset:0x80
	v_pk_mul_f32 v[250:251], v[70:71], v[86:87] op_sel_hi:[1,0]
	v_pk_fma_f32 v[250:251], v[72:73], v[86:87], v[250:251] op_sel:[0,1,0] op_sel_hi:[1,1,1]
	v_pk_fma_f32 v[250:251], v[74:75], v[88:89], v[250:251] op_sel_hi:[1,0,1]
	v_pk_fma_f32 v[250:251], v[76:77], v[88:89], v[250:251] op_sel:[0,1,0] op_sel_hi:[1,1,1]
	v_pk_mul_f32 v[184:185], v[126:127], v[118:119] op_sel_hi:[1,0]
	v_pk_mul_f32 v[186:187], v[126:127], v[118:119] op_sel:[0,1] op_sel_hi:[1,1]
	v_add_f32_dpp v252, v251, v250 quad_perm:[1,0,3,2] row_mask:0xf bank_mask:0xf bound_ctrl:1
	s_nop 0
	v_pk_mul_f32 v[188:189], v[126:127], v[120:121] op_sel_hi:[1,0]
	v_add_f32_dpp v252, v252, v252 quad_perm:[2,3,0,1] row_mask:0xf bank_mask:0xf bound_ctrl:1
	s_nop 0
	v_pk_mul_f32 v[190:191], v[126:127], v[120:121] op_sel:[0,1] op_sel_hi:[1,1]
	v_add_f32_dpp v252, v252, v252 row_ror:4 row_mask:0xf bank_mask:0xf bound_ctrl:1
	s_nop 0
	v_pk_fma_f32 v[184:185], v[70:71], v[82:83], v[184:185] op_sel_hi:[1,0,1]
	v_add_f32_dpp v252, v252, v252 row_ror:8 row_mask:0xf bank_mask:0xf bound_ctrl:1
	s_nop 0
	v_pk_fma_f32 v[186:187], v[72:73], v[82:83], v[186:187] op_sel:[0,1,0] op_sel_hi:[1,1,1]
	v_mov_b32_dpp v253, v252 quad_perm:[1,0,3,2] row_mask:0xf bank_mask:0xf bound_ctrl:1
	v_pk_fma_f32 v[188:189], v[74:75], v[84:85], v[188:189] op_sel_hi:[1,0,1]
	v_pk_fma_f32 v[190:191], v[76:77], v[84:85], v[190:191] op_sel:[0,1,0] op_sel_hi:[1,1,1]
	v_pk_fma_f32 v[70:71], v[252:253], v[114:115], v[184:185] op_sel_hi:[1,0,1]
	v_pk_fma_f32 v[72:73], v[252:253], v[114:115], v[186:187] op_sel:[0,1,0] op_sel_hi:[1,1,1]
	v_pk_fma_f32 v[74:75], v[252:253], v[116:117], v[188:189] op_sel_hi:[1,0,1]
	v_pk_fma_f32 v[76:77], v[252:253], v[116:117], v[190:191] op_sel:[0,1,0] op_sel_hi:[1,1,1]
	v_pk_mul_f32 v[192:193], v[70:71], v[122:123] op_sel_hi:[1,0]
	v_pk_fma_f32 v[192:193], v[72:73], v[122:123], v[192:193] op_sel:[0,1,0] op_sel_hi:[1,1,1]
	v_pk_fma_f32 v[192:193], v[74:75], v[124:125], v[192:193] op_sel_hi:[1,0,1]
	v_pk_fma_f32 v[192:193], v[76:77], v[124:125], v[192:193] op_sel:[0,1,0] op_sel_hi:[1,1,1]

	s_cmpk_lg_i32 s2, 0x88
	s_waitcnt lgkmcnt(0)
	s_nop 0
	ds_read_b128 v[82:85], v79 offset:0x200
	ds_read_b128 v[86:89], v79 offset:0x2200
	ds_read_b128 v[114:117], v79 offset:0x4200
	ds_read_b128 v[118:121], v79 offset:0x6200
	ds_read_b128 v[122:125], v79 offset:0x8200
	ds_read_b32 v126, v80 offset:0x100
	ds_read_b32 v127, v81 offset:0x100
	v_pk_mul_f32 v[250:251], v[70:71], v[166:167] op_sel_hi:[1,0]
	v_pk_fma_f32 v[250:251], v[72:73], v[166:167], v[250:251] op_sel:[0,1,0] op_sel_hi:[1,1,1]
	v_pk_fma_f32 v[250:251], v[74:75], v[168:169], v[250:251] op_sel_hi:[1,0,1]
	v_pk_fma_f32 v[250:251], v[76:77], v[168:169], v[250:251] op_sel:[0,1,0] op_sel_hi:[1,1,1]
	v_pk_mul_f32 v[184:185], v[182:183], v[174:175] op_sel_hi:[1,0]
	v_pk_mul_f32 v[186:187], v[182:183], v[174:175] op_sel:[0,1] op_sel_hi:[1,1]
	v_add_f32_dpp v252, v251, v250 quad_perm:[1,0,3,2] row_mask:0xf bank_mask:0xf bound_ctrl:1
	v_add_f32_dpp v92, v193, v192 quad_perm:[1,0,3,2] row_mask:0xf bank_mask:0xf bound_ctrl:1
	v_pk_mul_f32 v[188:189], v[182:183], v[176:177] op_sel_hi:[1,0]
	v_add_f32_dpp v252, v252, v252 quad_perm:[2,3,0,1] row_mask:0xf bank_mask:0xf bound_ctrl:1
	v_add_f32_dpp v92, v92, v92 quad_perm:[2,3,0,1] row_mask:0xf bank_mask:0xf bound_ctrl:1
	v_pk_mul_f32 v[190:191], v[182:183], v[176:177] op_sel:[0,1] op_sel_hi:[1,1]
	v_add_f32_dpp v252, v252, v252 row_ror:4 row_mask:0xf bank_mask:0xf bound_ctrl:1
	v_add_f32_dpp v92, v92, v92 row_ror:4 row_mask:0xf bank_mask:0xf bound_ctrl:1
	v_pk_fma_f32 v[184:185], v[70:71], v[162:163], v[184:185] op_sel_hi:[1,0,1]
	v_add_f32_dpp v252, v252, v252 row_ror:8 row_mask:0xf bank_mask:0xf bound_ctrl:1
	v_add_f32_dpp v92, v92, v92 row_ror:8 row_mask:0xf bank_mask:0xf bound_ctrl:1
	v_pk_fma_f32 v[186:187], v[72:73], v[162:163], v[186:187] op_sel:[0,1,0] op_sel_hi:[1,1,1]
	v_mov_b32_dpp v253, v252 quad_perm:[1,0,3,2] row_mask:0xf bank_mask:0xf bound_ctrl:1
	v_pk_fma_f32 v[188:189], v[74:75], v[164:165], v[188:189] op_sel_hi:[1,0,1]
	v_pk_fma_f32 v[190:191], v[76:77], v[164:165], v[190:191] op_sel:[0,1,0] op_sel_hi:[1,1,1]
	v_pk_fma_f32 v[70:71], v[252:253], v[170:171], v[184:185] op_sel_hi:[1,0,1]
	v_pk_fma_f32 v[72:73], v[252:253], v[170:171], v[186:187] op_sel:[0,1,0] op_sel_hi:[1,1,1]
	v_pk_fma_f32 v[74:75], v[252:253], v[172:173], v[188:189] op_sel_hi:[1,0,1]
	v_pk_fma_f32 v[76:77], v[252:253], v[172:173], v[190:191] op_sel:[0,1,0] op_sel_hi:[1,1,1]
	v_pk_mul_f32 v[194:195], v[70:71], v[178:179] op_sel_hi:[1,0]
	v_pk_fma_f32 v[194:195], v[72:73], v[178:179], v[194:195] op_sel:[0,1,0] op_sel_hi:[1,1,1]
	v_pk_fma_f32 v[194:195], v[74:75], v[180:181], v[194:195] op_sel_hi:[1,0,1]
	v_pk_fma_f32 v[194:195], v[76:77], v[180:181], v[194:195] op_sel:[0,1,0] op_sel_hi:[1,1,1]

	s_waitcnt lgkmcnt(0)
	v_cndmask_b32_e64 v92, 0, v92, s[4:5]
	ds_read_b128 v[162:165], v79 offset:0x300
	ds_read_b128 v[166:169], v79 offset:0x2300
	ds_read_b128 v[170:173], v79 offset:0x4300
	ds_read_b128 v[174:177], v79 offset:0x6300
	ds_read_b128 v[178:181], v79 offset:0x8300
	ds_read_b32 v182, v80 offset:0x180
	ds_read_b32 v183, v81 offset:0x180
	v_pk_mul_f32 v[250:251], v[70:71], v[86:87] op_sel_hi:[1,0]
	v_pk_fma_f32 v[250:251], v[72:73], v[86:87], v[250:251] op_sel:[0,1,0] op_sel_hi:[1,1,1]
	v_pk_fma_f32 v[250:251], v[74:75], v[88:89], v[250:251] op_sel_hi:[1,0,1]
	v_pk_fma_f32 v[250:251], v[76:77], v[88:89], v[250:251] op_sel:[0,1,0] op_sel_hi:[1,1,1]
	v_pk_mul_f32 v[184:185], v[126:127], v[118:119] op_sel_hi:[1,0]
	v_pk_mul_f32 v[186:187], v[126:127], v[118:119] op_sel:[0,1] op_sel_hi:[1,1]
	v_add_f32_dpp v252, v251, v250 quad_perm:[1,0,3,2] row_mask:0xf bank_mask:0xf bound_ctrl:1
	v_add_f32_dpp v161, v195, v194 quad_perm:[1,0,3,2] row_mask:0xf bank_mask:0xf bound_ctrl:1
	v_pk_mul_f32 v[188:189], v[126:127], v[120:121] op_sel_hi:[1,0]
	v_add_f32_dpp v252, v252, v252 quad_perm:[2,3,0,1] row_mask:0xf bank_mask:0xf bound_ctrl:1
	v_add_f32_dpp v161, v161, v161 quad_perm:[2,3,0,1] row_mask:0xf bank_mask:0xf bound_ctrl:1
	v_pk_mul_f32 v[190:191], v[126:127], v[120:121] op_sel:[0,1] op_sel_hi:[1,1]
	v_add_f32_dpp v252, v252, v252 row_ror:4 row_mask:0xf bank_mask:0xf bound_ctrl:1
	v_add_f32_dpp v161, v161, v161 row_ror:4 row_mask:0xf bank_mask:0xf bound_ctrl:1
	v_pk_fma_f32 v[184:185], v[70:71], v[82:83], v[184:185] op_sel_hi:[1,0,1]
	v_add_f32_dpp v252, v252, v252 row_ror:8 row_mask:0xf bank_mask:0xf bound_ctrl:1
	v_add_f32_dpp v161, v161, v161 row_ror:8 row_mask:0xf bank_mask:0xf bound_ctrl:1
	v_pk_fma_f32 v[186:187], v[72:73], v[82:83], v[186:187] op_sel:[0,1,0] op_sel_hi:[1,1,1]
	v_mov_b32_dpp v253, v252 quad_perm:[1,0,3,2] row_mask:0xf bank_mask:0xf bound_ctrl:1
	v_pk_fma_f32 v[188:189], v[74:75], v[84:85], v[188:189] op_sel_hi:[1,0,1]
	v_pk_fma_f32 v[190:191], v[76:77], v[84:85], v[190:191] op_sel:[0,1,0] op_sel_hi:[1,1,1]
	v_pk_fma_f32 v[70:71], v[252:253], v[114:115], v[184:185] op_sel_hi:[1,0,1]
	v_pk_fma_f32 v[72:73], v[252:253], v[114:115], v[186:187] op_sel:[0,1,0] op_sel_hi:[1,1,1]
	v_pk_fma_f32 v[74:75], v[252:253], v[116:117], v[188:189] op_sel_hi:[1,0,1]
	v_pk_fma_f32 v[76:77], v[252:253], v[116:117], v[190:191] op_sel:[0,1,0] op_sel_hi:[1,1,1]
	v_pk_mul_f32 v[192:193], v[70:71], v[122:123] op_sel_hi:[1,0]
	v_pk_fma_f32 v[192:193], v[72:73], v[122:123], v[192:193] op_sel:[0,1,0] op_sel_hi:[1,1,1]
	v_pk_fma_f32 v[192:193], v[74:75], v[124:125], v[192:193] op_sel_hi:[1,0,1]
	v_pk_fma_f32 v[192:193], v[76:77], v[124:125], v[192:193] op_sel:[0,1,0] op_sel_hi:[1,1,1]

	s_waitcnt lgkmcnt(0)
	v_cndmask_b32_e64 v92, v92, v161, s[6:7]
	ds_read_b128 v[82:85], v79 offset:0x400
	ds_read_b128 v[86:89], v79 offset:0x2400
	ds_read_b128 v[114:117], v79 offset:0x4400
	ds_read_b128 v[118:121], v79 offset:0x6400
	ds_read_b128 v[122:125], v79 offset:0x8400
	ds_read_b32 v126, v80 offset:0x200
	ds_read_b32 v127, v81 offset:0x200
	v_pk_mul_f32 v[250:251], v[70:71], v[166:167] op_sel_hi:[1,0]
	v_pk_fma_f32 v[250:251], v[72:73], v[166:167], v[250:251] op_sel:[0,1,0] op_sel_hi:[1,1,1]
	v_pk_fma_f32 v[250:251], v[74:75], v[168:169], v[250:251] op_sel_hi:[1,0,1]
	v_pk_fma_f32 v[250:251], v[76:77], v[168:169], v[250:251] op_sel:[0,1,0] op_sel_hi:[1,1,1]
	v_pk_mul_f32 v[184:185], v[182:183], v[174:175] op_sel_hi:[1,0]
	v_pk_mul_f32 v[186:187], v[182:183], v[174:175] op_sel:[0,1] op_sel_hi:[1,1]
	v_add_f32_dpp v252, v251, v250 quad_perm:[1,0,3,2] row_mask:0xf bank_mask:0xf bound_ctrl:1
	v_add_f32_dpp v161, v193, v192 quad_perm:[1,0,3,2] row_mask:0xf bank_mask:0xf bound_ctrl:1
	v_pk_mul_f32 v[188:189], v[182:183], v[176:177] op_sel_hi:[1,0]
	v_add_f32_dpp v252, v252, v252 quad_perm:[2,3,0,1] row_mask:0xf bank_mask:0xf bound_ctrl:1
	v_add_f32_dpp v161, v161, v161 quad_perm:[2,3,0,1] row_mask:0xf bank_mask:0xf bound_ctrl:1
	v_pk_mul_f32 v[190:191], v[182:183], v[176:177] op_sel:[0,1] op_sel_hi:[1,1]
	v_add_f32_dpp v252, v252, v252 row_ror:4 row_mask:0xf bank_mask:0xf bound_ctrl:1
	v_add_f32_dpp v161, v161, v161 row_ror:4 row_mask:0xf bank_mask:0xf bound_ctrl:1
	v_pk_fma_f32 v[184:185], v[70:71], v[162:163], v[184:185] op_sel_hi:[1,0,1]
	v_add_f32_dpp v252, v252, v252 row_ror:8 row_mask:0xf bank_mask:0xf bound_ctrl:1
	v_add_f32_dpp v161, v161, v161 row_ror:8 row_mask:0xf bank_mask:0xf bound_ctrl:1
	v_pk_fma_f32 v[186:187], v[72:73], v[162:163], v[186:187] op_sel:[0,1,0] op_sel_hi:[1,1,1]
	v_mov_b32_dpp v253, v252 quad_perm:[1,0,3,2] row_mask:0xf bank_mask:0xf bound_ctrl:1
	v_pk_fma_f32 v[188:189], v[74:75], v[164:165], v[188:189] op_sel_hi:[1,0,1]
	v_pk_fma_f32 v[190:191], v[76:77], v[164:165], v[190:191] op_sel:[0,1,0] op_sel_hi:[1,1,1]
	v_pk_fma_f32 v[70:71], v[252:253], v[170:171], v[184:185] op_sel_hi:[1,0,1]
	v_pk_fma_f32 v[72:73], v[252:253], v[170:171], v[186:187] op_sel:[0,1,0] op_sel_hi:[1,1,1]
	v_pk_fma_f32 v[74:75], v[252:253], v[172:173], v[188:189] op_sel_hi:[1,0,1]
	v_pk_fma_f32 v[76:77], v[252:253], v[172:173], v[190:191] op_sel:[0,1,0] op_sel_hi:[1,1,1]
	v_pk_mul_f32 v[194:195], v[70:71], v[178:179] op_sel_hi:[1,0]
	v_pk_fma_f32 v[194:195], v[72:73], v[178:179], v[194:195] op_sel:[0,1,0] op_sel_hi:[1,1,1]
	v_pk_fma_f32 v[194:195], v[74:75], v[180:181], v[194:195] op_sel_hi:[1,0,1]
	v_pk_fma_f32 v[194:195], v[76:77], v[180:181], v[194:195] op_sel:[0,1,0] op_sel_hi:[1,1,1]

	s_waitcnt lgkmcnt(0)
	v_cndmask_b32_e64 v92, v92, v161, s[8:9]
	ds_read_b128 v[162:165], v79 offset:0x500
	ds_read_b128 v[166:169], v79 offset:0x2500
	ds_read_b128 v[170:173], v79 offset:0x4500
	ds_read_b128 v[174:177], v79 offset:0x6500
	ds_read_b128 v[178:181], v79 offset:0x8500
	ds_read_b32 v182, v80 offset:0x280
	ds_read_b32 v183, v81 offset:0x280
	v_pk_mul_f32 v[250:251], v[70:71], v[86:87] op_sel_hi:[1,0]
	v_pk_fma_f32 v[250:251], v[72:73], v[86:87], v[250:251] op_sel:[0,1,0] op_sel_hi:[1,1,1]
	v_pk_fma_f32 v[250:251], v[74:75], v[88:89], v[250:251] op_sel_hi:[1,0,1]
	v_pk_fma_f32 v[250:251], v[76:77], v[88:89], v[250:251] op_sel:[0,1,0] op_sel_hi:[1,1,1]
	v_pk_mul_f32 v[184:185], v[126:127], v[118:119] op_sel_hi:[1,0]
	v_pk_mul_f32 v[186:187], v[126:127], v[118:119] op_sel:[0,1] op_sel_hi:[1,1]
	v_add_f32_dpp v252, v251, v250 quad_perm:[1,0,3,2] row_mask:0xf bank_mask:0xf bound_ctrl:1
	v_add_f32_dpp v161, v195, v194 quad_perm:[1,0,3,2] row_mask:0xf bank_mask:0xf bound_ctrl:1
	v_pk_mul_f32 v[188:189], v[126:127], v[120:121] op_sel_hi:[1,0]
	v_add_f32_dpp v252, v252, v252 quad_perm:[2,3,0,1] row_mask:0xf bank_mask:0xf bound_ctrl:1
	v_add_f32_dpp v161, v161, v161 quad_perm:[2,3,0,1] row_mask:0xf bank_mask:0xf bound_ctrl:1
	v_pk_mul_f32 v[190:191], v[126:127], v[120:121] op_sel:[0,1] op_sel_hi:[1,1]
	v_add_f32_dpp v252, v252, v252 row_ror:4 row_mask:0xf bank_mask:0xf bound_ctrl:1
	v_add_f32_dpp v161, v161, v161 row_ror:4 row_mask:0xf bank_mask:0xf bound_ctrl:1
	v_pk_fma_f32 v[184:185], v[70:71], v[82:83], v[184:185] op_sel_hi:[1,0,1]
	v_add_f32_dpp v252, v252, v252 row_ror:8 row_mask:0xf bank_mask:0xf bound_ctrl:1
	v_add_f32_dpp v161, v161, v161 row_ror:8 row_mask:0xf bank_mask:0xf bound_ctrl:1
	v_pk_fma_f32 v[186:187], v[72:73], v[82:83], v[186:187] op_sel:[0,1,0] op_sel_hi:[1,1,1]
	v_mov_b32_dpp v253, v252 quad_perm:[1,0,3,2] row_mask:0xf bank_mask:0xf bound_ctrl:1
	v_pk_fma_f32 v[188:189], v[74:75], v[84:85], v[188:189] op_sel_hi:[1,0,1]
	v_pk_fma_f32 v[190:191], v[76:77], v[84:85], v[190:191] op_sel:[0,1,0] op_sel_hi:[1,1,1]
	v_pk_fma_f32 v[70:71], v[252:253], v[114:115], v[184:185] op_sel_hi:[1,0,1]
	v_pk_fma_f32 v[72:73], v[252:253], v[114:115], v[186:187] op_sel:[0,1,0] op_sel_hi:[1,1,1]
	v_pk_fma_f32 v[74:75], v[252:253], v[116:117], v[188:189] op_sel_hi:[1,0,1]
	v_pk_fma_f32 v[76:77], v[252:253], v[116:117], v[190:191] op_sel:[0,1,0] op_sel_hi:[1,1,1]
	v_pk_mul_f32 v[192:193], v[70:71], v[122:123] op_sel_hi:[1,0]
	v_pk_fma_f32 v[192:193], v[72:73], v[122:123], v[192:193] op_sel:[0,1,0] op_sel_hi:[1,1,1]
	v_pk_fma_f32 v[192:193], v[74:75], v[124:125], v[192:193] op_sel_hi:[1,0,1]
	v_pk_fma_f32 v[192:193], v[76:77], v[124:125], v[192:193] op_sel:[0,1,0] op_sel_hi:[1,1,1]

	s_waitcnt lgkmcnt(0)
	v_cndmask_b32_e64 v92, v92, v161, s[10:11]
	ds_read_b128 v[82:85], v79 offset:0x600
	ds_read_b128 v[86:89], v79 offset:0x2600
	ds_read_b128 v[114:117], v79 offset:0x4600
	ds_read_b128 v[118:121], v79 offset:0x6600
	ds_read_b128 v[122:125], v79 offset:0x8600
	ds_read_b32 v126, v80 offset:0x300
	ds_read_b32 v127, v81 offset:0x300
	v_pk_mul_f32 v[250:251], v[70:71], v[166:167] op_sel_hi:[1,0]
	v_pk_fma_f32 v[250:251], v[72:73], v[166:167], v[250:251] op_sel:[0,1,0] op_sel_hi:[1,1,1]
	v_pk_fma_f32 v[250:251], v[74:75], v[168:169], v[250:251] op_sel_hi:[1,0,1]
	v_pk_fma_f32 v[250:251], v[76:77], v[168:169], v[250:251] op_sel:[0,1,0] op_sel_hi:[1,1,1]
	v_pk_mul_f32 v[184:185], v[182:183], v[174:175] op_sel_hi:[1,0]
	v_pk_mul_f32 v[186:187], v[182:183], v[174:175] op_sel:[0,1] op_sel_hi:[1,1]
	v_add_f32_dpp v252, v251, v250 quad_perm:[1,0,3,2] row_mask:0xf bank_mask:0xf bound_ctrl:1
	v_add_f32_dpp v161, v193, v192 quad_perm:[1,0,3,2] row_mask:0xf bank_mask:0xf bound_ctrl:1
	v_pk_mul_f32 v[188:189], v[182:183], v[176:177] op_sel_hi:[1,0]
	v_add_f32_dpp v252, v252, v252 quad_perm:[2,3,0,1] row_mask:0xf bank_mask:0xf bound_ctrl:1
	v_add_f32_dpp v161, v161, v161 quad_perm:[2,3,0,1] row_mask:0xf bank_mask:0xf bound_ctrl:1
	v_pk_mul_f32 v[190:191], v[182:183], v[176:177] op_sel:[0,1] op_sel_hi:[1,1]
	v_add_f32_dpp v252, v252, v252 row_ror:4 row_mask:0xf bank_mask:0xf bound_ctrl:1
	v_add_f32_dpp v161, v161, v161 row_ror:4 row_mask:0xf bank_mask:0xf bound_ctrl:1
	v_pk_fma_f32 v[184:185], v[70:71], v[162:163], v[184:185] op_sel_hi:[1,0,1]
	v_add_f32_dpp v252, v252, v252 row_ror:8 row_mask:0xf bank_mask:0xf bound_ctrl:1
	v_add_f32_dpp v161, v161, v161 row_ror:8 row_mask:0xf bank_mask:0xf bound_ctrl:1
	v_pk_fma_f32 v[186:187], v[72:73], v[162:163], v[186:187] op_sel:[0,1,0] op_sel_hi:[1,1,1]
	v_mov_b32_dpp v253, v252 quad_perm:[1,0,3,2] row_mask:0xf bank_mask:0xf bound_ctrl:1
	v_pk_fma_f32 v[188:189], v[74:75], v[164:165], v[188:189] op_sel_hi:[1,0,1]
	v_pk_fma_f32 v[190:191], v[76:77], v[164:165], v[190:191] op_sel:[0,1,0] op_sel_hi:[1,1,1]
	v_pk_fma_f32 v[70:71], v[252:253], v[170:171], v[184:185] op_sel_hi:[1,0,1]
	v_pk_fma_f32 v[72:73], v[252:253], v[170:171], v[186:187] op_sel:[0,1,0] op_sel_hi:[1,1,1]
	v_pk_fma_f32 v[74:75], v[252:253], v[172:173], v[188:189] op_sel_hi:[1,0,1]
	v_pk_fma_f32 v[76:77], v[252:253], v[172:173], v[190:191] op_sel:[0,1,0] op_sel_hi:[1,1,1]
	v_pk_mul_f32 v[194:195], v[70:71], v[178:179] op_sel_hi:[1,0]
	v_pk_fma_f32 v[194:195], v[72:73], v[178:179], v[194:195] op_sel:[0,1,0] op_sel_hi:[1,1,1]
	v_pk_fma_f32 v[194:195], v[74:75], v[180:181], v[194:195] op_sel_hi:[1,0,1]
	v_pk_fma_f32 v[194:195], v[76:77], v[180:181], v[194:195] op_sel:[0,1,0] op_sel_hi:[1,1,1]

	s_waitcnt lgkmcnt(0)
	v_cndmask_b32_e64 v92, v92, v161, s[12:13]
	ds_read_b128 v[162:165], v79 offset:0x700
	ds_read_b128 v[166:169], v79 offset:0x2700
	ds_read_b128 v[170:173], v79 offset:0x4700
	ds_read_b128 v[174:177], v79 offset:0x6700
	ds_read_b128 v[178:181], v79 offset:0x8700
	ds_read_b32 v182, v80 offset:0x380
	ds_read_b32 v183, v81 offset:0x380
	v_pk_mul_f32 v[250:251], v[70:71], v[86:87] op_sel_hi:[1,0]
	v_pk_fma_f32 v[250:251], v[72:73], v[86:87], v[250:251] op_sel:[0,1,0] op_sel_hi:[1,1,1]
	v_pk_fma_f32 v[250:251], v[74:75], v[88:89], v[250:251] op_sel_hi:[1,0,1]
	v_pk_fma_f32 v[250:251], v[76:77], v[88:89], v[250:251] op_sel:[0,1,0] op_sel_hi:[1,1,1]
	v_pk_mul_f32 v[184:185], v[126:127], v[118:119] op_sel_hi:[1,0]
	v_pk_mul_f32 v[186:187], v[126:127], v[118:119] op_sel:[0,1] op_sel_hi:[1,1]
	v_add_f32_dpp v252, v251, v250 quad_perm:[1,0,3,2] row_mask:0xf bank_mask:0xf bound_ctrl:1
	v_add_f32_dpp v161, v195, v194 quad_perm:[1,0,3,2] row_mask:0xf bank_mask:0xf bound_ctrl:1
	v_pk_mul_f32 v[188:189], v[126:127], v[120:121] op_sel_hi:[1,0]
	v_add_f32_dpp v252, v252, v252 quad_perm:[2,3,0,1] row_mask:0xf bank_mask:0xf bound_ctrl:1
	v_add_f32_dpp v161, v161, v161 quad_perm:[2,3,0,1] row_mask:0xf bank_mask:0xf bound_ctrl:1
	v_pk_mul_f32 v[190:191], v[126:127], v[120:121] op_sel:[0,1] op_sel_hi:[1,1]
	v_add_f32_dpp v252, v252, v252 row_ror:4 row_mask:0xf bank_mask:0xf bound_ctrl:1
	v_add_f32_dpp v161, v161, v161 row_ror:4 row_mask:0xf bank_mask:0xf bound_ctrl:1
	v_pk_fma_f32 v[184:185], v[70:71], v[82:83], v[184:185] op_sel_hi:[1,0,1]
	v_add_f32_dpp v252, v252, v252 row_ror:8 row_mask:0xf bank_mask:0xf bound_ctrl:1
	v_add_f32_dpp v161, v161, v161 row_ror:8 row_mask:0xf bank_mask:0xf bound_ctrl:1
	v_pk_fma_f32 v[186:187], v[72:73], v[82:83], v[186:187] op_sel:[0,1,0] op_sel_hi:[1,1,1]
	v_mov_b32_dpp v253, v252 quad_perm:[1,0,3,2] row_mask:0xf bank_mask:0xf bound_ctrl:1
	v_pk_fma_f32 v[188:189], v[74:75], v[84:85], v[188:189] op_sel_hi:[1,0,1]
	v_pk_fma_f32 v[190:191], v[76:77], v[84:85], v[190:191] op_sel:[0,1,0] op_sel_hi:[1,1,1]
	v_pk_fma_f32 v[70:71], v[252:253], v[114:115], v[184:185] op_sel_hi:[1,0,1]
	v_pk_fma_f32 v[72:73], v[252:253], v[114:115], v[186:187] op_sel:[0,1,0] op_sel_hi:[1,1,1]
	v_pk_fma_f32 v[74:75], v[252:253], v[116:117], v[188:189] op_sel_hi:[1,0,1]
	v_pk_fma_f32 v[76:77], v[252:253], v[116:117], v[190:191] op_sel:[0,1,0] op_sel_hi:[1,1,1]
	v_pk_mul_f32 v[192:193], v[70:71], v[122:123] op_sel_hi:[1,0]
	v_pk_fma_f32 v[192:193], v[72:73], v[122:123], v[192:193] op_sel:[0,1,0] op_sel_hi:[1,1,1]
	v_pk_fma_f32 v[192:193], v[74:75], v[124:125], v[192:193] op_sel_hi:[1,0,1]
	v_pk_fma_f32 v[192:193], v[76:77], v[124:125], v[192:193] op_sel:[0,1,0] op_sel_hi:[1,1,1]

	s_waitcnt lgkmcnt(0)
	v_cndmask_b32_e64 v92, v92, v161, s[14:15]
	ds_read_b128 v[82:85], v79 offset:0x800
	ds_read_b128 v[86:89], v79 offset:0x2800
	ds_read_b128 v[114:117], v79 offset:0x4800
	ds_read_b128 v[118:121], v79 offset:0x6800
	ds_read_b128 v[122:125], v79 offset:0x8800
	ds_read_b32 v126, v80 offset:0x400
	ds_read_b32 v127, v81 offset:0x400
	v_pk_mul_f32 v[250:251], v[70:71], v[166:167] op_sel_hi:[1,0]
	v_pk_fma_f32 v[250:251], v[72:73], v[166:167], v[250:251] op_sel:[0,1,0] op_sel_hi:[1,1,1]
	v_pk_fma_f32 v[250:251], v[74:75], v[168:169], v[250:251] op_sel_hi:[1,0,1]
	v_pk_fma_f32 v[250:251], v[76:77], v[168:169], v[250:251] op_sel:[0,1,0] op_sel_hi:[1,1,1]
	v_pk_mul_f32 v[184:185], v[182:183], v[174:175] op_sel_hi:[1,0]
	v_pk_mul_f32 v[186:187], v[182:183], v[174:175] op_sel:[0,1] op_sel_hi:[1,1]
	v_add_f32_dpp v252, v251, v250 quad_perm:[1,0,3,2] row_mask:0xf bank_mask:0xf bound_ctrl:1
	v_add_f32_dpp v161, v193, v192 quad_perm:[1,0,3,2] row_mask:0xf bank_mask:0xf bound_ctrl:1
	v_pk_mul_f32 v[188:189], v[182:183], v[176:177] op_sel_hi:[1,0]
	v_add_f32_dpp v252, v252, v252 quad_perm:[2,3,0,1] row_mask:0xf bank_mask:0xf bound_ctrl:1
	v_add_f32_dpp v161, v161, v161 quad_perm:[2,3,0,1] row_mask:0xf bank_mask:0xf bound_ctrl:1
	v_pk_mul_f32 v[190:191], v[182:183], v[176:177] op_sel:[0,1] op_sel_hi:[1,1]
	v_add_f32_dpp v252, v252, v252 row_ror:4 row_mask:0xf bank_mask:0xf bound_ctrl:1
	v_add_f32_dpp v161, v161, v161 row_ror:4 row_mask:0xf bank_mask:0xf bound_ctrl:1
	v_pk_fma_f32 v[184:185], v[70:71], v[162:163], v[184:185] op_sel_hi:[1,0,1]
	v_add_f32_dpp v252, v252, v252 row_ror:8 row_mask:0xf bank_mask:0xf bound_ctrl:1
	v_add_f32_dpp v161, v161, v161 row_ror:8 row_mask:0xf bank_mask:0xf bound_ctrl:1
	v_pk_fma_f32 v[186:187], v[72:73], v[162:163], v[186:187] op_sel:[0,1,0] op_sel_hi:[1,1,1]
	v_mov_b32_dpp v253, v252 quad_perm:[1,0,3,2] row_mask:0xf bank_mask:0xf bound_ctrl:1
	v_pk_fma_f32 v[188:189], v[74:75], v[164:165], v[188:189] op_sel_hi:[1,0,1]
	v_pk_fma_f32 v[190:191], v[76:77], v[164:165], v[190:191] op_sel:[0,1,0] op_sel_hi:[1,1,1]
	v_pk_fma_f32 v[70:71], v[252:253], v[170:171], v[184:185] op_sel_hi:[1,0,1]
	v_pk_fma_f32 v[72:73], v[252:253], v[170:171], v[186:187] op_sel:[0,1,0] op_sel_hi:[1,1,1]
	v_pk_fma_f32 v[74:75], v[252:253], v[172:173], v[188:189] op_sel_hi:[1,0,1]
	v_pk_fma_f32 v[76:77], v[252:253], v[172:173], v[190:191] op_sel:[0,1,0] op_sel_hi:[1,1,1]
	v_pk_mul_f32 v[194:195], v[70:71], v[178:179] op_sel_hi:[1,0]
	v_pk_fma_f32 v[194:195], v[72:73], v[178:179], v[194:195] op_sel:[0,1,0] op_sel_hi:[1,1,1]
	v_pk_fma_f32 v[194:195], v[74:75], v[180:181], v[194:195] op_sel_hi:[1,0,1]
	v_pk_fma_f32 v[194:195], v[76:77], v[180:181], v[194:195] op_sel:[0,1,0] op_sel_hi:[1,1,1]

	s_waitcnt lgkmcnt(0)
	v_cndmask_b32_e64 v92, v92, v161, s[16:17]
	ds_read_b128 v[162:165], v79 offset:0x900
	ds_read_b128 v[166:169], v79 offset:0x2900
	ds_read_b128 v[170:173], v79 offset:0x4900
	ds_read_b128 v[174:177], v79 offset:0x6900
	ds_read_b128 v[178:181], v79 offset:0x8900
	ds_read_b32 v182, v80 offset:0x480
	ds_read_b32 v183, v81 offset:0x480
	v_pk_mul_f32 v[250:251], v[70:71], v[86:87] op_sel_hi:[1,0]
	v_pk_fma_f32 v[250:251], v[72:73], v[86:87], v[250:251] op_sel:[0,1,0] op_sel_hi:[1,1,1]
	v_pk_fma_f32 v[250:251], v[74:75], v[88:89], v[250:251] op_sel_hi:[1,0,1]
	v_pk_fma_f32 v[250:251], v[76:77], v[88:89], v[250:251] op_sel:[0,1,0] op_sel_hi:[1,1,1]
	v_pk_mul_f32 v[184:185], v[126:127], v[118:119] op_sel_hi:[1,0]
	v_pk_mul_f32 v[186:187], v[126:127], v[118:119] op_sel:[0,1] op_sel_hi:[1,1]
	v_add_f32_dpp v252, v251, v250 quad_perm:[1,0,3,2] row_mask:0xf bank_mask:0xf bound_ctrl:1
	v_add_f32_dpp v161, v195, v194 quad_perm:[1,0,3,2] row_mask:0xf bank_mask:0xf bound_ctrl:1
	v_pk_mul_f32 v[188:189], v[126:127], v[120:121] op_sel_hi:[1,0]
	v_add_f32_dpp v252, v252, v252 quad_perm:[2,3,0,1] row_mask:0xf bank_mask:0xf bound_ctrl:1
	v_add_f32_dpp v161, v161, v161 quad_perm:[2,3,0,1] row_mask:0xf bank_mask:0xf bound_ctrl:1
	v_pk_mul_f32 v[190:191], v[126:127], v[120:121] op_sel:[0,1] op_sel_hi:[1,1]
	v_add_f32_dpp v252, v252, v252 row_ror:4 row_mask:0xf bank_mask:0xf bound_ctrl:1
	v_add_f32_dpp v161, v161, v161 row_ror:4 row_mask:0xf bank_mask:0xf bound_ctrl:1
	v_pk_fma_f32 v[184:185], v[70:71], v[82:83], v[184:185] op_sel_hi:[1,0,1]
	v_add_f32_dpp v252, v252, v252 row_ror:8 row_mask:0xf bank_mask:0xf bound_ctrl:1
	v_add_f32_dpp v161, v161, v161 row_ror:8 row_mask:0xf bank_mask:0xf bound_ctrl:1
	v_pk_fma_f32 v[186:187], v[72:73], v[82:83], v[186:187] op_sel:[0,1,0] op_sel_hi:[1,1,1]
	v_mov_b32_dpp v253, v252 quad_perm:[1,0,3,2] row_mask:0xf bank_mask:0xf bound_ctrl:1
	v_pk_fma_f32 v[188:189], v[74:75], v[84:85], v[188:189] op_sel_hi:[1,0,1]
	v_pk_fma_f32 v[190:191], v[76:77], v[84:85], v[190:191] op_sel:[0,1,0] op_sel_hi:[1,1,1]
	v_pk_fma_f32 v[70:71], v[252:253], v[114:115], v[184:185] op_sel_hi:[1,0,1]
	v_pk_fma_f32 v[72:73], v[252:253], v[114:115], v[186:187] op_sel:[0,1,0] op_sel_hi:[1,1,1]
	v_pk_fma_f32 v[74:75], v[252:253], v[116:117], v[188:189] op_sel_hi:[1,0,1]
	v_pk_fma_f32 v[76:77], v[252:253], v[116:117], v[190:191] op_sel:[0,1,0] op_sel_hi:[1,1,1]
	v_pk_mul_f32 v[192:193], v[70:71], v[122:123] op_sel_hi:[1,0]
	v_pk_fma_f32 v[192:193], v[72:73], v[122:123], v[192:193] op_sel:[0,1,0] op_sel_hi:[1,1,1]
	v_pk_fma_f32 v[192:193], v[74:75], v[124:125], v[192:193] op_sel_hi:[1,0,1]
	v_pk_fma_f32 v[192:193], v[76:77], v[124:125], v[192:193] op_sel:[0,1,0] op_sel_hi:[1,1,1]

	s_nop 0
	v_cndmask_b32_e64 v82, v92, v161, s[18:19]
	ds_write_b32 v78, v82
	s_waitcnt lgkmcnt(0)
	s_nop 0
	ds_read_b128 v[82:85], v79 offset:0xa00
	ds_read_b128 v[86:89], v79 offset:0x2a00
	ds_read_b128 v[114:117], v79 offset:0x4a00
	ds_read_b128 v[118:121], v79 offset:0x6a00
	ds_read_b128 v[122:125], v79 offset:0x8a00
	ds_read_b32 v126, v80 offset:0x500
	ds_read_b32 v127, v81 offset:0x500
	v_pk_mul_f32 v[250:251], v[70:71], v[166:167] op_sel_hi:[1,0]
	v_pk_fma_f32 v[250:251], v[72:73], v[166:167], v[250:251] op_sel:[0,1,0] op_sel_hi:[1,1,1]
	v_pk_fma_f32 v[250:251], v[74:75], v[168:169], v[250:251] op_sel_hi:[1,0,1]
	v_pk_fma_f32 v[250:251], v[76:77], v[168:169], v[250:251] op_sel:[0,1,0] op_sel_hi:[1,1,1]
	v_pk_mul_f32 v[184:185], v[182:183], v[174:175] op_sel_hi:[1,0]
	v_pk_mul_f32 v[186:187], v[182:183], v[174:175] op_sel:[0,1] op_sel_hi:[1,1]
	v_add_f32_dpp v252, v251, v250 quad_perm:[1,0,3,2] row_mask:0xf bank_mask:0xf bound_ctrl:1
	v_add_f32_dpp v92, v193, v192 quad_perm:[1,0,3,2] row_mask:0xf bank_mask:0xf bound_ctrl:1
	v_pk_mul_f32 v[188:189], v[182:183], v[176:177] op_sel_hi:[1,0]
	v_add_f32_dpp v252, v252, v252 quad_perm:[2,3,0,1] row_mask:0xf bank_mask:0xf bound_ctrl:1
	v_add_f32_dpp v92, v92, v92 quad_perm:[2,3,0,1] row_mask:0xf bank_mask:0xf bound_ctrl:1
	v_pk_mul_f32 v[190:191], v[182:183], v[176:177] op_sel:[0,1] op_sel_hi:[1,1]
	v_add_f32_dpp v252, v252, v252 row_ror:4 row_mask:0xf bank_mask:0xf bound_ctrl:1
	v_add_f32_dpp v92, v92, v92 row_ror:4 row_mask:0xf bank_mask:0xf bound_ctrl:1
	v_pk_fma_f32 v[184:185], v[70:71], v[162:163], v[184:185] op_sel_hi:[1,0,1]
	v_add_f32_dpp v252, v252, v252 row_ror:8 row_mask:0xf bank_mask:0xf bound_ctrl:1
	v_add_f32_dpp v92, v92, v92 row_ror:8 row_mask:0xf bank_mask:0xf bound_ctrl:1
	v_pk_fma_f32 v[186:187], v[72:73], v[162:163], v[186:187] op_sel:[0,1,0] op_sel_hi:[1,1,1]
	v_mov_b32_dpp v253, v252 quad_perm:[1,0,3,2] row_mask:0xf bank_mask:0xf bound_ctrl:1
	v_pk_fma_f32 v[188:189], v[74:75], v[164:165], v[188:189] op_sel_hi:[1,0,1]
	v_pk_fma_f32 v[190:191], v[76:77], v[164:165], v[190:191] op_sel:[0,1,0] op_sel_hi:[1,1,1]
	v_pk_fma_f32 v[70:71], v[252:253], v[170:171], v[184:185] op_sel_hi:[1,0,1]
	v_pk_fma_f32 v[72:73], v[252:253], v[170:171], v[186:187] op_sel:[0,1,0] op_sel_hi:[1,1,1]
	v_pk_fma_f32 v[74:75], v[252:253], v[172:173], v[188:189] op_sel_hi:[1,0,1]
	v_pk_fma_f32 v[76:77], v[252:253], v[172:173], v[190:191] op_sel:[0,1,0] op_sel_hi:[1,1,1]
	v_pk_mul_f32 v[194:195], v[70:71], v[178:179] op_sel_hi:[1,0]
	v_pk_fma_f32 v[194:195], v[72:73], v[178:179], v[194:195] op_sel:[0,1,0] op_sel_hi:[1,1,1]
	v_pk_fma_f32 v[194:195], v[74:75], v[180:181], v[194:195] op_sel_hi:[1,0,1]
	v_pk_fma_f32 v[194:195], v[76:77], v[180:181], v[194:195] op_sel:[0,1,0] op_sel_hi:[1,1,1]

	s_waitcnt lgkmcnt(0)
	v_cndmask_b32_e64 v92, 0, v92, s[4:5]
	ds_read_b128 v[162:165], v79 offset:0xb00
	ds_read_b128 v[166:169], v79 offset:0x2b00
	ds_read_b128 v[170:173], v79 offset:0x4b00
	ds_read_b128 v[174:177], v79 offset:0x6b00
	ds_read_b128 v[178:181], v79 offset:0x8b00
	ds_read_b32 v182, v80 offset:0x580
	ds_read_b32 v183, v81 offset:0x580
	v_pk_mul_f32 v[250:251], v[70:71], v[86:87] op_sel_hi:[1,0]
	v_pk_fma_f32 v[250:251], v[72:73], v[86:87], v[250:251] op_sel:[0,1,0] op_sel_hi:[1,1,1]
	v_pk_fma_f32 v[250:251], v[74:75], v[88:89], v[250:251] op_sel_hi:[1,0,1]
	v_pk_fma_f32 v[250:251], v[76:77], v[88:89], v[250:251] op_sel:[0,1,0] op_sel_hi:[1,1,1]
	v_pk_mul_f32 v[184:185], v[126:127], v[118:119] op_sel_hi:[1,0]
	v_pk_mul_f32 v[186:187], v[126:127], v[118:119] op_sel:[0,1] op_sel_hi:[1,1]
	v_add_f32_dpp v252, v251, v250 quad_perm:[1,0,3,2] row_mask:0xf bank_mask:0xf bound_ctrl:1
	v_add_f32_dpp v161, v195, v194 quad_perm:[1,0,3,2] row_mask:0xf bank_mask:0xf bound_ctrl:1
	v_pk_mul_f32 v[188:189], v[126:127], v[120:121] op_sel_hi:[1,0]
	v_add_f32_dpp v252, v252, v252 quad_perm:[2,3,0,1] row_mask:0xf bank_mask:0xf bound_ctrl:1
	v_add_f32_dpp v161, v161, v161 quad_perm:[2,3,0,1] row_mask:0xf bank_mask:0xf bound_ctrl:1
	v_pk_mul_f32 v[190:191], v[126:127], v[120:121] op_sel:[0,1] op_sel_hi:[1,1]
	v_add_f32_dpp v252, v252, v252 row_ror:4 row_mask:0xf bank_mask:0xf bound_ctrl:1
	v_add_f32_dpp v161, v161, v161 row_ror:4 row_mask:0xf bank_mask:0xf bound_ctrl:1
	v_pk_fma_f32 v[184:185], v[70:71], v[82:83], v[184:185] op_sel_hi:[1,0,1]
	v_add_f32_dpp v252, v252, v252 row_ror:8 row_mask:0xf bank_mask:0xf bound_ctrl:1
	v_add_f32_dpp v161, v161, v161 row_ror:8 row_mask:0xf bank_mask:0xf bound_ctrl:1
	v_pk_fma_f32 v[186:187], v[72:73], v[82:83], v[186:187] op_sel:[0,1,0] op_sel_hi:[1,1,1]
	v_mov_b32_dpp v253, v252 quad_perm:[1,0,3,2] row_mask:0xf bank_mask:0xf bound_ctrl:1
	v_pk_fma_f32 v[188:189], v[74:75], v[84:85], v[188:189] op_sel_hi:[1,0,1]
	v_pk_fma_f32 v[190:191], v[76:77], v[84:85], v[190:191] op_sel:[0,1,0] op_sel_hi:[1,1,1]
	v_pk_fma_f32 v[70:71], v[252:253], v[114:115], v[184:185] op_sel_hi:[1,0,1]
	v_pk_fma_f32 v[72:73], v[252:253], v[114:115], v[186:187] op_sel:[0,1,0] op_sel_hi:[1,1,1]
	v_pk_fma_f32 v[74:75], v[252:253], v[116:117], v[188:189] op_sel_hi:[1,0,1]
	v_pk_fma_f32 v[76:77], v[252:253], v[116:117], v[190:191] op_sel:[0,1,0] op_sel_hi:[1,1,1]
	v_pk_mul_f32 v[192:193], v[70:71], v[122:123] op_sel_hi:[1,0]
	v_pk_fma_f32 v[192:193], v[72:73], v[122:123], v[192:193] op_sel:[0,1,0] op_sel_hi:[1,1,1]
	v_pk_fma_f32 v[192:193], v[74:75], v[124:125], v[192:193] op_sel_hi:[1,0,1]
	v_pk_fma_f32 v[192:193], v[76:77], v[124:125], v[192:193] op_sel:[0,1,0] op_sel_hi:[1,1,1]

	s_waitcnt lgkmcnt(0)
	v_cndmask_b32_e64 v92, v92, v161, s[6:7]
	ds_read_b128 v[82:85], v79 offset:0xc00
	ds_read_b128 v[86:89], v79 offset:0x2c00
	ds_read_b128 v[114:117], v79 offset:0x4c00
	ds_read_b128 v[118:121], v79 offset:0x6c00
	ds_read_b128 v[122:125], v79 offset:0x8c00
	ds_read_b32 v126, v80 offset:0x600
	ds_read_b32 v127, v81 offset:0x600
	v_pk_mul_f32 v[250:251], v[70:71], v[166:167] op_sel_hi:[1,0]
	v_pk_fma_f32 v[250:251], v[72:73], v[166:167], v[250:251] op_sel:[0,1,0] op_sel_hi:[1,1,1]
	v_pk_fma_f32 v[250:251], v[74:75], v[168:169], v[250:251] op_sel_hi:[1,0,1]
	v_pk_fma_f32 v[250:251], v[76:77], v[168:169], v[250:251] op_sel:[0,1,0] op_sel_hi:[1,1,1]
	v_pk_mul_f32 v[184:185], v[182:183], v[174:175] op_sel_hi:[1,0]
	v_pk_mul_f32 v[186:187], v[182:183], v[174:175] op_sel:[0,1] op_sel_hi:[1,1]
	v_add_f32_dpp v252, v251, v250 quad_perm:[1,0,3,2] row_mask:0xf bank_mask:0xf bound_ctrl:1
	v_add_f32_dpp v161, v193, v192 quad_perm:[1,0,3,2] row_mask:0xf bank_mask:0xf bound_ctrl:1
	v_pk_mul_f32 v[188:189], v[182:183], v[176:177] op_sel_hi:[1,0]
	v_add_f32_dpp v252, v252, v252 quad_perm:[2,3,0,1] row_mask:0xf bank_mask:0xf bound_ctrl:1
	v_add_f32_dpp v161, v161, v161 quad_perm:[2,3,0,1] row_mask:0xf bank_mask:0xf bound_ctrl:1
	v_pk_mul_f32 v[190:191], v[182:183], v[176:177] op_sel:[0,1] op_sel_hi:[1,1]
	v_add_f32_dpp v252, v252, v252 row_ror:4 row_mask:0xf bank_mask:0xf bound_ctrl:1
	v_add_f32_dpp v161, v161, v161 row_ror:4 row_mask:0xf bank_mask:0xf bound_ctrl:1
	v_pk_fma_f32 v[184:185], v[70:71], v[162:163], v[184:185] op_sel_hi:[1,0,1]
	v_add_f32_dpp v252, v252, v252 row_ror:8 row_mask:0xf bank_mask:0xf bound_ctrl:1
	v_add_f32_dpp v161, v161, v161 row_ror:8 row_mask:0xf bank_mask:0xf bound_ctrl:1
	v_pk_fma_f32 v[186:187], v[72:73], v[162:163], v[186:187] op_sel:[0,1,0] op_sel_hi:[1,1,1]
	v_mov_b32_dpp v253, v252 quad_perm:[1,0,3,2] row_mask:0xf bank_mask:0xf bound_ctrl:1
	v_pk_fma_f32 v[188:189], v[74:75], v[164:165], v[188:189] op_sel_hi:[1,0,1]
	v_pk_fma_f32 v[190:191], v[76:77], v[164:165], v[190:191] op_sel:[0,1,0] op_sel_hi:[1,1,1]
	v_pk_fma_f32 v[70:71], v[252:253], v[170:171], v[184:185] op_sel_hi:[1,0,1]
	v_pk_fma_f32 v[72:73], v[252:253], v[170:171], v[186:187] op_sel:[0,1,0] op_sel_hi:[1,1,1]
	v_pk_fma_f32 v[74:75], v[252:253], v[172:173], v[188:189] op_sel_hi:[1,0,1]
	v_pk_fma_f32 v[76:77], v[252:253], v[172:173], v[190:191] op_sel:[0,1,0] op_sel_hi:[1,1,1]
	v_pk_mul_f32 v[194:195], v[70:71], v[178:179] op_sel_hi:[1,0]
	v_pk_fma_f32 v[194:195], v[72:73], v[178:179], v[194:195] op_sel:[0,1,0] op_sel_hi:[1,1,1]
	v_pk_fma_f32 v[194:195], v[74:75], v[180:181], v[194:195] op_sel_hi:[1,0,1]
	v_pk_fma_f32 v[194:195], v[76:77], v[180:181], v[194:195] op_sel:[0,1,0] op_sel_hi:[1,1,1]

	s_waitcnt lgkmcnt(0)
	v_cndmask_b32_e64 v92, v92, v161, s[8:9]
	ds_read_b128 v[162:165], v79 offset:0xd00
	ds_read_b128 v[166:169], v79 offset:0x2d00
	ds_read_b128 v[170:173], v79 offset:0x4d00
	ds_read_b128 v[174:177], v79 offset:0x6d00
	ds_read_b128 v[178:181], v79 offset:0x8d00
	ds_read_b32 v182, v80 offset:0x680
	ds_read_b32 v183, v81 offset:0x680
	v_pk_mul_f32 v[250:251], v[70:71], v[86:87] op_sel_hi:[1,0]
	v_pk_fma_f32 v[250:251], v[72:73], v[86:87], v[250:251] op_sel:[0,1,0] op_sel_hi:[1,1,1]
	v_pk_fma_f32 v[250:251], v[74:75], v[88:89], v[250:251] op_sel_hi:[1,0,1]
	v_pk_fma_f32 v[250:251], v[76:77], v[88:89], v[250:251] op_sel:[0,1,0] op_sel_hi:[1,1,1]
	v_pk_mul_f32 v[184:185], v[126:127], v[118:119] op_sel_hi:[1,0]
	v_pk_mul_f32 v[186:187], v[126:127], v[118:119] op_sel:[0,1] op_sel_hi:[1,1]
	v_add_f32_dpp v252, v251, v250 quad_perm:[1,0,3,2] row_mask:0xf bank_mask:0xf bound_ctrl:1
	v_add_f32_dpp v161, v195, v194 quad_perm:[1,0,3,2] row_mask:0xf bank_mask:0xf bound_ctrl:1
	v_pk_mul_f32 v[188:189], v[126:127], v[120:121] op_sel_hi:[1,0]
	v_add_f32_dpp v252, v252, v252 quad_perm:[2,3,0,1] row_mask:0xf bank_mask:0xf bound_ctrl:1
	v_add_f32_dpp v161, v161, v161 quad_perm:[2,3,0,1] row_mask:0xf bank_mask:0xf bound_ctrl:1
	v_pk_mul_f32 v[190:191], v[126:127], v[120:121] op_sel:[0,1] op_sel_hi:[1,1]
	v_add_f32_dpp v252, v252, v252 row_ror:4 row_mask:0xf bank_mask:0xf bound_ctrl:1
	v_add_f32_dpp v161, v161, v161 row_ror:4 row_mask:0xf bank_mask:0xf bound_ctrl:1
	v_pk_fma_f32 v[184:185], v[70:71], v[82:83], v[184:185] op_sel_hi:[1,0,1]
	v_add_f32_dpp v252, v252, v252 row_ror:8 row_mask:0xf bank_mask:0xf bound_ctrl:1
	v_add_f32_dpp v161, v161, v161 row_ror:8 row_mask:0xf bank_mask:0xf bound_ctrl:1
	v_pk_fma_f32 v[186:187], v[72:73], v[82:83], v[186:187] op_sel:[0,1,0] op_sel_hi:[1,1,1]
	v_mov_b32_dpp v253, v252 quad_perm:[1,0,3,2] row_mask:0xf bank_mask:0xf bound_ctrl:1
	v_pk_fma_f32 v[188:189], v[74:75], v[84:85], v[188:189] op_sel_hi:[1,0,1]
	v_pk_fma_f32 v[190:191], v[76:77], v[84:85], v[190:191] op_sel:[0,1,0] op_sel_hi:[1,1,1]
	v_pk_fma_f32 v[70:71], v[252:253], v[114:115], v[184:185] op_sel_hi:[1,0,1]
	v_pk_fma_f32 v[72:73], v[252:253], v[114:115], v[186:187] op_sel:[0,1,0] op_sel_hi:[1,1,1]
	v_pk_fma_f32 v[74:75], v[252:253], v[116:117], v[188:189] op_sel_hi:[1,0,1]
	v_pk_fma_f32 v[76:77], v[252:253], v[116:117], v[190:191] op_sel:[0,1,0] op_sel_hi:[1,1,1]
	v_pk_mul_f32 v[192:193], v[70:71], v[122:123] op_sel_hi:[1,0]
	v_pk_fma_f32 v[192:193], v[72:73], v[122:123], v[192:193] op_sel:[0,1,0] op_sel_hi:[1,1,1]
	v_pk_fma_f32 v[192:193], v[74:75], v[124:125], v[192:193] op_sel_hi:[1,0,1]
	v_pk_fma_f32 v[192:193], v[76:77], v[124:125], v[192:193] op_sel:[0,1,0] op_sel_hi:[1,1,1]

	s_waitcnt lgkmcnt(0)
	v_cndmask_b32_e64 v92, v92, v161, s[10:11]
	ds_read_b128 v[82:85], v79 offset:0xe00
	ds_read_b128 v[86:89], v79 offset:0x2e00
	ds_read_b128 v[114:117], v79 offset:0x4e00
	ds_read_b128 v[118:121], v79 offset:0x6e00
	ds_read_b128 v[122:125], v79 offset:0x8e00
	ds_read_b32 v126, v80 offset:0x700
	ds_read_b32 v127, v81 offset:0x700
	v_pk_mul_f32 v[250:251], v[70:71], v[166:167] op_sel_hi:[1,0]
	v_pk_fma_f32 v[250:251], v[72:73], v[166:167], v[250:251] op_sel:[0,1,0] op_sel_hi:[1,1,1]
	v_pk_fma_f32 v[250:251], v[74:75], v[168:169], v[250:251] op_sel_hi:[1,0,1]
	v_pk_fma_f32 v[250:251], v[76:77], v[168:169], v[250:251] op_sel:[0,1,0] op_sel_hi:[1,1,1]
	v_pk_mul_f32 v[184:185], v[182:183], v[174:175] op_sel_hi:[1,0]
	v_pk_mul_f32 v[186:187], v[182:183], v[174:175] op_sel:[0,1] op_sel_hi:[1,1]
	v_add_f32_dpp v252, v251, v250 quad_perm:[1,0,3,2] row_mask:0xf bank_mask:0xf bound_ctrl:1
	v_add_f32_dpp v161, v193, v192 quad_perm:[1,0,3,2] row_mask:0xf bank_mask:0xf bound_ctrl:1
	v_pk_mul_f32 v[188:189], v[182:183], v[176:177] op_sel_hi:[1,0]
	v_add_f32_dpp v252, v252, v252 quad_perm:[2,3,0,1] row_mask:0xf bank_mask:0xf bound_ctrl:1
	v_add_f32_dpp v161, v161, v161 quad_perm:[2,3,0,1] row_mask:0xf bank_mask:0xf bound_ctrl:1
	v_pk_mul_f32 v[190:191], v[182:183], v[176:177] op_sel:[0,1] op_sel_hi:[1,1]
	v_add_f32_dpp v252, v252, v252 row_ror:4 row_mask:0xf bank_mask:0xf bound_ctrl:1
	v_add_f32_dpp v161, v161, v161 row_ror:4 row_mask:0xf bank_mask:0xf bound_ctrl:1
	v_pk_fma_f32 v[184:185], v[70:71], v[162:163], v[184:185] op_sel_hi:[1,0,1]
	v_add_f32_dpp v252, v252, v252 row_ror:8 row_mask:0xf bank_mask:0xf bound_ctrl:1
	v_add_f32_dpp v161, v161, v161 row_ror:8 row_mask:0xf bank_mask:0xf bound_ctrl:1
	v_pk_fma_f32 v[186:187], v[72:73], v[162:163], v[186:187] op_sel:[0,1,0] op_sel_hi:[1,1,1]
	v_mov_b32_dpp v253, v252 quad_perm:[1,0,3,2] row_mask:0xf bank_mask:0xf bound_ctrl:1
	v_pk_fma_f32 v[188:189], v[74:75], v[164:165], v[188:189] op_sel_hi:[1,0,1]
	v_pk_fma_f32 v[190:191], v[76:77], v[164:165], v[190:191] op_sel:[0,1,0] op_sel_hi:[1,1,1]
	v_pk_fma_f32 v[70:71], v[252:253], v[170:171], v[184:185] op_sel_hi:[1,0,1]
	v_pk_fma_f32 v[72:73], v[252:253], v[170:171], v[186:187] op_sel:[0,1,0] op_sel_hi:[1,1,1]
	v_pk_fma_f32 v[74:75], v[252:253], v[172:173], v[188:189] op_sel_hi:[1,0,1]
	v_pk_fma_f32 v[76:77], v[252:253], v[172:173], v[190:191] op_sel:[0,1,0] op_sel_hi:[1,1,1]
	v_pk_mul_f32 v[194:195], v[70:71], v[178:179] op_sel_hi:[1,0]
	v_pk_fma_f32 v[194:195], v[72:73], v[178:179], v[194:195] op_sel:[0,1,0] op_sel_hi:[1,1,1]
	v_pk_fma_f32 v[194:195], v[74:75], v[180:181], v[194:195] op_sel_hi:[1,0,1]
	v_pk_fma_f32 v[194:195], v[76:77], v[180:181], v[194:195] op_sel:[0,1,0] op_sel_hi:[1,1,1]

	s_waitcnt lgkmcnt(0)
	v_cndmask_b32_e64 v92, v92, v161, s[12:13]
	ds_read_b128 v[162:165], v79 offset:0xf00
	ds_read_b128 v[166:169], v79 offset:0x2f00
	ds_read_b128 v[170:173], v79 offset:0x4f00
	ds_read_b128 v[174:177], v79 offset:0x6f00
	ds_read_b128 v[178:181], v79 offset:0x8f00
	ds_read_b32 v182, v80 offset:0x780
	ds_read_b32 v183, v81 offset:0x780
	v_pk_mul_f32 v[250:251], v[70:71], v[86:87] op_sel_hi:[1,0]
	v_pk_fma_f32 v[250:251], v[72:73], v[86:87], v[250:251] op_sel:[0,1,0] op_sel_hi:[1,1,1]
	v_pk_fma_f32 v[250:251], v[74:75], v[88:89], v[250:251] op_sel_hi:[1,0,1]
	v_pk_fma_f32 v[250:251], v[76:77], v[88:89], v[250:251] op_sel:[0,1,0] op_sel_hi:[1,1,1]
	v_pk_mul_f32 v[184:185], v[126:127], v[118:119] op_sel_hi:[1,0]
	v_pk_mul_f32 v[186:187], v[126:127], v[118:119] op_sel:[0,1] op_sel_hi:[1,1]
	v_add_f32_dpp v252, v251, v250 quad_perm:[1,0,3,2] row_mask:0xf bank_mask:0xf bound_ctrl:1
	v_add_f32_dpp v161, v195, v194 quad_perm:[1,0,3,2] row_mask:0xf bank_mask:0xf bound_ctrl:1
	v_pk_mul_f32 v[188:189], v[126:127], v[120:121] op_sel_hi:[1,0]
	v_add_f32_dpp v252, v252, v252 quad_perm:[2,3,0,1] row_mask:0xf bank_mask:0xf bound_ctrl:1
	v_add_f32_dpp v161, v161, v161 quad_perm:[2,3,0,1] row_mask:0xf bank_mask:0xf bound_ctrl:1
	v_pk_mul_f32 v[190:191], v[126:127], v[120:121] op_sel:[0,1] op_sel_hi:[1,1]
	v_add_f32_dpp v252, v252, v252 row_ror:4 row_mask:0xf bank_mask:0xf bound_ctrl:1
	v_add_f32_dpp v161, v161, v161 row_ror:4 row_mask:0xf bank_mask:0xf bound_ctrl:1
	v_pk_fma_f32 v[184:185], v[70:71], v[82:83], v[184:185] op_sel_hi:[1,0,1]
	v_add_f32_dpp v252, v252, v252 row_ror:8 row_mask:0xf bank_mask:0xf bound_ctrl:1
	v_add_f32_dpp v161, v161, v161 row_ror:8 row_mask:0xf bank_mask:0xf bound_ctrl:1
	v_pk_fma_f32 v[186:187], v[72:73], v[82:83], v[186:187] op_sel:[0,1,0] op_sel_hi:[1,1,1]
	v_mov_b32_dpp v253, v252 quad_perm:[1,0,3,2] row_mask:0xf bank_mask:0xf bound_ctrl:1
	v_pk_fma_f32 v[188:189], v[74:75], v[84:85], v[188:189] op_sel_hi:[1,0,1]
	v_pk_fma_f32 v[190:191], v[76:77], v[84:85], v[190:191] op_sel:[0,1,0] op_sel_hi:[1,1,1]
	v_pk_fma_f32 v[70:71], v[252:253], v[114:115], v[184:185] op_sel_hi:[1,0,1]
	v_pk_fma_f32 v[72:73], v[252:253], v[114:115], v[186:187] op_sel:[0,1,0] op_sel_hi:[1,1,1]
	v_pk_fma_f32 v[74:75], v[252:253], v[116:117], v[188:189] op_sel_hi:[1,0,1]
	v_pk_fma_f32 v[76:77], v[252:253], v[116:117], v[190:191] op_sel:[0,1,0] op_sel_hi:[1,1,1]
	v_pk_mul_f32 v[192:193], v[70:71], v[122:123] op_sel_hi:[1,0]
	v_pk_fma_f32 v[192:193], v[72:73], v[122:123], v[192:193] op_sel:[0,1,0] op_sel_hi:[1,1,1]
	v_pk_fma_f32 v[192:193], v[74:75], v[124:125], v[192:193] op_sel_hi:[1,0,1]
	v_pk_fma_f32 v[192:193], v[76:77], v[124:125], v[192:193] op_sel:[0,1,0] op_sel_hi:[1,1,1]

	s_waitcnt lgkmcnt(0)
	v_cndmask_b32_e64 v92, v92, v161, s[14:15]
	ds_read_b128 v[82:85], v79 offset:0x1000
	ds_read_b128 v[86:89], v79 offset:0x3000
	ds_read_b128 v[114:117], v79 offset:0x5000
	ds_read_b128 v[118:121], v79 offset:0x7000
	ds_read_b128 v[122:125], v79 offset:0x9000
	ds_read_b32 v126, v80 offset:0x800
	ds_read_b32 v127, v81 offset:0x800
	v_pk_mul_f32 v[250:251], v[70:71], v[166:167] op_sel_hi:[1,0]
	v_pk_fma_f32 v[250:251], v[72:73], v[166:167], v[250:251] op_sel:[0,1,0] op_sel_hi:[1,1,1]
	v_pk_fma_f32 v[250:251], v[74:75], v[168:169], v[250:251] op_sel_hi:[1,0,1]
	v_pk_fma_f32 v[250:251], v[76:77], v[168:169], v[250:251] op_sel:[0,1,0] op_sel_hi:[1,1,1]
	v_pk_mul_f32 v[184:185], v[182:183], v[174:175] op_sel_hi:[1,0]
	v_pk_mul_f32 v[186:187], v[182:183], v[174:175] op_sel:[0,1] op_sel_hi:[1,1]
	v_add_f32_dpp v252, v251, v250 quad_perm:[1,0,3,2] row_mask:0xf bank_mask:0xf bound_ctrl:1
	v_add_f32_dpp v161, v193, v192 quad_perm:[1,0,3,2] row_mask:0xf bank_mask:0xf bound_ctrl:1
	v_pk_mul_f32 v[188:189], v[182:183], v[176:177] op_sel_hi:[1,0]
	v_add_f32_dpp v252, v252, v252 quad_perm:[2,3,0,1] row_mask:0xf bank_mask:0xf bound_ctrl:1
	v_add_f32_dpp v161, v161, v161 quad_perm:[2,3,0,1] row_mask:0xf bank_mask:0xf bound_ctrl:1
	v_pk_mul_f32 v[190:191], v[182:183], v[176:177] op_sel:[0,1] op_sel_hi:[1,1]
	v_add_f32_dpp v252, v252, v252 row_ror:4 row_mask:0xf bank_mask:0xf bound_ctrl:1
	v_add_f32_dpp v161, v161, v161 row_ror:4 row_mask:0xf bank_mask:0xf bound_ctrl:1
	v_pk_fma_f32 v[184:185], v[70:71], v[162:163], v[184:185] op_sel_hi:[1,0,1]
	v_add_f32_dpp v252, v252, v252 row_ror:8 row_mask:0xf bank_mask:0xf bound_ctrl:1
	v_add_f32_dpp v161, v161, v161 row_ror:8 row_mask:0xf bank_mask:0xf bound_ctrl:1
	v_pk_fma_f32 v[186:187], v[72:73], v[162:163], v[186:187] op_sel:[0,1,0] op_sel_hi:[1,1,1]
	v_mov_b32_dpp v253, v252 quad_perm:[1,0,3,2] row_mask:0xf bank_mask:0xf bound_ctrl:1
	v_pk_fma_f32 v[188:189], v[74:75], v[164:165], v[188:189] op_sel_hi:[1,0,1]
	v_pk_fma_f32 v[190:191], v[76:77], v[164:165], v[190:191] op_sel:[0,1,0] op_sel_hi:[1,1,1]
	v_pk_fma_f32 v[70:71], v[252:253], v[170:171], v[184:185] op_sel_hi:[1,0,1]
	v_pk_fma_f32 v[72:73], v[252:253], v[170:171], v[186:187] op_sel:[0,1,0] op_sel_hi:[1,1,1]
	v_pk_fma_f32 v[74:75], v[252:253], v[172:173], v[188:189] op_sel_hi:[1,0,1]
	v_pk_fma_f32 v[76:77], v[252:253], v[172:173], v[190:191] op_sel:[0,1,0] op_sel_hi:[1,1,1]
	v_pk_mul_f32 v[194:195], v[70:71], v[178:179] op_sel_hi:[1,0]
	v_pk_fma_f32 v[194:195], v[72:73], v[178:179], v[194:195] op_sel:[0,1,0] op_sel_hi:[1,1,1]
	v_pk_fma_f32 v[194:195], v[74:75], v[180:181], v[194:195] op_sel_hi:[1,0,1]
	v_pk_fma_f32 v[194:195], v[76:77], v[180:181], v[194:195] op_sel:[0,1,0] op_sel_hi:[1,1,1]

	s_waitcnt lgkmcnt(0)
	v_cndmask_b32_e64 v92, v92, v161, s[16:17]
	ds_read_b128 v[162:165], v79 offset:0x1100
	ds_read_b128 v[166:169], v79 offset:0x3100
	ds_read_b128 v[170:173], v79 offset:0x5100
	ds_read_b128 v[174:177], v79 offset:0x7100
	ds_read_b128 v[178:181], v79 offset:0x9100
	ds_read_b32 v182, v80 offset:0x880
	ds_read_b32 v183, v81 offset:0x880
	v_pk_mul_f32 v[250:251], v[70:71], v[86:87] op_sel_hi:[1,0]
	v_pk_fma_f32 v[250:251], v[72:73], v[86:87], v[250:251] op_sel:[0,1,0] op_sel_hi:[1,1,1]
	v_pk_fma_f32 v[250:251], v[74:75], v[88:89], v[250:251] op_sel_hi:[1,0,1]
	v_pk_fma_f32 v[250:251], v[76:77], v[88:89], v[250:251] op_sel:[0,1,0] op_sel_hi:[1,1,1]
	v_pk_mul_f32 v[184:185], v[126:127], v[118:119] op_sel_hi:[1,0]
	v_pk_mul_f32 v[186:187], v[126:127], v[118:119] op_sel:[0,1] op_sel_hi:[1,1]
	v_add_f32_dpp v252, v251, v250 quad_perm:[1,0,3,2] row_mask:0xf bank_mask:0xf bound_ctrl:1
	v_add_f32_dpp v161, v195, v194 quad_perm:[1,0,3,2] row_mask:0xf bank_mask:0xf bound_ctrl:1
	v_pk_mul_f32 v[188:189], v[126:127], v[120:121] op_sel_hi:[1,0]
	v_add_f32_dpp v252, v252, v252 quad_perm:[2,3,0,1] row_mask:0xf bank_mask:0xf bound_ctrl:1
	v_add_f32_dpp v161, v161, v161 quad_perm:[2,3,0,1] row_mask:0xf bank_mask:0xf bound_ctrl:1
	v_pk_mul_f32 v[190:191], v[126:127], v[120:121] op_sel:[0,1] op_sel_hi:[1,1]
	v_add_f32_dpp v252, v252, v252 row_ror:4 row_mask:0xf bank_mask:0xf bound_ctrl:1
	v_add_f32_dpp v161, v161, v161 row_ror:4 row_mask:0xf bank_mask:0xf bound_ctrl:1
	v_pk_fma_f32 v[184:185], v[70:71], v[82:83], v[184:185] op_sel_hi:[1,0,1]
	v_add_f32_dpp v252, v252, v252 row_ror:8 row_mask:0xf bank_mask:0xf bound_ctrl:1
	v_add_f32_dpp v161, v161, v161 row_ror:8 row_mask:0xf bank_mask:0xf bound_ctrl:1
	v_pk_fma_f32 v[186:187], v[72:73], v[82:83], v[186:187] op_sel:[0,1,0] op_sel_hi:[1,1,1]
	v_mov_b32_dpp v253, v252 quad_perm:[1,0,3,2] row_mask:0xf bank_mask:0xf bound_ctrl:1
	v_pk_fma_f32 v[188:189], v[74:75], v[84:85], v[188:189] op_sel_hi:[1,0,1]
	v_pk_fma_f32 v[190:191], v[76:77], v[84:85], v[190:191] op_sel:[0,1,0] op_sel_hi:[1,1,1]
	v_pk_fma_f32 v[70:71], v[252:253], v[114:115], v[184:185] op_sel_hi:[1,0,1]
	v_pk_fma_f32 v[72:73], v[252:253], v[114:115], v[186:187] op_sel:[0,1,0] op_sel_hi:[1,1,1]
	v_pk_fma_f32 v[74:75], v[252:253], v[116:117], v[188:189] op_sel_hi:[1,0,1]
	v_pk_fma_f32 v[76:77], v[252:253], v[116:117], v[190:191] op_sel:[0,1,0] op_sel_hi:[1,1,1]
	v_pk_mul_f32 v[192:193], v[70:71], v[122:123] op_sel_hi:[1,0]
	v_pk_fma_f32 v[192:193], v[72:73], v[122:123], v[192:193] op_sel:[0,1,0] op_sel_hi:[1,1,1]
	v_pk_fma_f32 v[192:193], v[74:75], v[124:125], v[192:193] op_sel_hi:[1,0,1]
	v_pk_fma_f32 v[192:193], v[76:77], v[124:125], v[192:193] op_sel:[0,1,0] op_sel_hi:[1,1,1]

	s_nop 0
	v_cndmask_b32_e64 v82, v92, v161, s[18:19]
	ds_write_b32 v78, v82 offset:1024
	s_waitcnt lgkmcnt(0)
	s_nop 0
	ds_read_b128 v[82:85], v79 offset:0x1200
	ds_read_b128 v[86:89], v79 offset:0x3200
	ds_read_b128 v[114:117], v79 offset:0x5200
	ds_read_b128 v[118:121], v79 offset:0x7200
	ds_read_b128 v[122:125], v79 offset:0x9200
	ds_read_b32 v126, v80 offset:0x900
	ds_read_b32 v127, v81 offset:0x900
	v_pk_mul_f32 v[250:251], v[70:71], v[166:167] op_sel_hi:[1,0]
	v_pk_fma_f32 v[250:251], v[72:73], v[166:167], v[250:251] op_sel:[0,1,0] op_sel_hi:[1,1,1]
	v_pk_fma_f32 v[250:251], v[74:75], v[168:169], v[250:251] op_sel_hi:[1,0,1]
	v_pk_fma_f32 v[250:251], v[76:77], v[168:169], v[250:251] op_sel:[0,1,0] op_sel_hi:[1,1,1]
	v_pk_mul_f32 v[184:185], v[182:183], v[174:175] op_sel_hi:[1,0]
	v_pk_mul_f32 v[186:187], v[182:183], v[174:175] op_sel:[0,1] op_sel_hi:[1,1]
	v_add_f32_dpp v252, v251, v250 quad_perm:[1,0,3,2] row_mask:0xf bank_mask:0xf bound_ctrl:1
	v_add_f32_dpp v92, v193, v192 quad_perm:[1,0,3,2] row_mask:0xf bank_mask:0xf bound_ctrl:1
	v_pk_mul_f32 v[188:189], v[182:183], v[176:177] op_sel_hi:[1,0]
	v_add_f32_dpp v252, v252, v252 quad_perm:[2,3,0,1] row_mask:0xf bank_mask:0xf bound_ctrl:1
	v_add_f32_dpp v92, v92, v92 quad_perm:[2,3,0,1] row_mask:0xf bank_mask:0xf bound_ctrl:1
	v_pk_mul_f32 v[190:191], v[182:183], v[176:177] op_sel:[0,1] op_sel_hi:[1,1]
	v_add_f32_dpp v252, v252, v252 row_ror:4 row_mask:0xf bank_mask:0xf bound_ctrl:1
	v_add_f32_dpp v92, v92, v92 row_ror:4 row_mask:0xf bank_mask:0xf bound_ctrl:1
	v_pk_fma_f32 v[184:185], v[70:71], v[162:163], v[184:185] op_sel_hi:[1,0,1]
	v_add_f32_dpp v252, v252, v252 row_ror:8 row_mask:0xf bank_mask:0xf bound_ctrl:1
	v_add_f32_dpp v92, v92, v92 row_ror:8 row_mask:0xf bank_mask:0xf bound_ctrl:1
	v_pk_fma_f32 v[186:187], v[72:73], v[162:163], v[186:187] op_sel:[0,1,0] op_sel_hi:[1,1,1]
	v_mov_b32_dpp v253, v252 quad_perm:[1,0,3,2] row_mask:0xf bank_mask:0xf bound_ctrl:1
	v_pk_fma_f32 v[188:189], v[74:75], v[164:165], v[188:189] op_sel_hi:[1,0,1]
	v_pk_fma_f32 v[190:191], v[76:77], v[164:165], v[190:191] op_sel:[0,1,0] op_sel_hi:[1,1,1]
	v_pk_fma_f32 v[70:71], v[252:253], v[170:171], v[184:185] op_sel_hi:[1,0,1]
	v_pk_fma_f32 v[72:73], v[252:253], v[170:171], v[186:187] op_sel:[0,1,0] op_sel_hi:[1,1,1]
	v_pk_fma_f32 v[74:75], v[252:253], v[172:173], v[188:189] op_sel_hi:[1,0,1]
	v_pk_fma_f32 v[76:77], v[252:253], v[172:173], v[190:191] op_sel:[0,1,0] op_sel_hi:[1,1,1]
	v_pk_mul_f32 v[194:195], v[70:71], v[178:179] op_sel_hi:[1,0]
	v_pk_fma_f32 v[194:195], v[72:73], v[178:179], v[194:195] op_sel:[0,1,0] op_sel_hi:[1,1,1]
	v_pk_fma_f32 v[194:195], v[74:75], v[180:181], v[194:195] op_sel_hi:[1,0,1]
	v_pk_fma_f32 v[194:195], v[76:77], v[180:181], v[194:195] op_sel:[0,1,0] op_sel_hi:[1,1,1]

	s_waitcnt lgkmcnt(0)
	v_cndmask_b32_e64 v92, 0, v92, s[4:5]
	ds_read_b128 v[162:165], v79 offset:0x1300
	ds_read_b128 v[166:169], v79 offset:0x3300
	ds_read_b128 v[170:173], v79 offset:0x5300
	ds_read_b128 v[174:177], v79 offset:0x7300
	ds_read_b128 v[178:181], v79 offset:0x9300
	ds_read_b32 v182, v80 offset:0x980
	ds_read_b32 v183, v81 offset:0x980
	v_pk_mul_f32 v[250:251], v[70:71], v[86:87] op_sel_hi:[1,0]
	v_pk_fma_f32 v[250:251], v[72:73], v[86:87], v[250:251] op_sel:[0,1,0] op_sel_hi:[1,1,1]
	v_pk_fma_f32 v[250:251], v[74:75], v[88:89], v[250:251] op_sel_hi:[1,0,1]
	v_pk_fma_f32 v[250:251], v[76:77], v[88:89], v[250:251] op_sel:[0,1,0] op_sel_hi:[1,1,1]
	v_pk_mul_f32 v[184:185], v[126:127], v[118:119] op_sel_hi:[1,0]
	v_pk_mul_f32 v[186:187], v[126:127], v[118:119] op_sel:[0,1] op_sel_hi:[1,1]
	v_add_f32_dpp v252, v251, v250 quad_perm:[1,0,3,2] row_mask:0xf bank_mask:0xf bound_ctrl:1
	v_add_f32_dpp v161, v195, v194 quad_perm:[1,0,3,2] row_mask:0xf bank_mask:0xf bound_ctrl:1
	v_pk_mul_f32 v[188:189], v[126:127], v[120:121] op_sel_hi:[1,0]
	v_add_f32_dpp v252, v252, v252 quad_perm:[2,3,0,1] row_mask:0xf bank_mask:0xf bound_ctrl:1
	v_add_f32_dpp v161, v161, v161 quad_perm:[2,3,0,1] row_mask:0xf bank_mask:0xf bound_ctrl:1
	v_pk_mul_f32 v[190:191], v[126:127], v[120:121] op_sel:[0,1] op_sel_hi:[1,1]
	v_add_f32_dpp v252, v252, v252 row_ror:4 row_mask:0xf bank_mask:0xf bound_ctrl:1
	v_add_f32_dpp v161, v161, v161 row_ror:4 row_mask:0xf bank_mask:0xf bound_ctrl:1
	v_pk_fma_f32 v[184:185], v[70:71], v[82:83], v[184:185] op_sel_hi:[1,0,1]
	v_add_f32_dpp v252, v252, v252 row_ror:8 row_mask:0xf bank_mask:0xf bound_ctrl:1
	v_add_f32_dpp v161, v161, v161 row_ror:8 row_mask:0xf bank_mask:0xf bound_ctrl:1
	v_pk_fma_f32 v[186:187], v[72:73], v[82:83], v[186:187] op_sel:[0,1,0] op_sel_hi:[1,1,1]
	v_mov_b32_dpp v253, v252 quad_perm:[1,0,3,2] row_mask:0xf bank_mask:0xf bound_ctrl:1
	v_pk_fma_f32 v[188:189], v[74:75], v[84:85], v[188:189] op_sel_hi:[1,0,1]
	v_pk_fma_f32 v[190:191], v[76:77], v[84:85], v[190:191] op_sel:[0,1,0] op_sel_hi:[1,1,1]
	v_pk_fma_f32 v[70:71], v[252:253], v[114:115], v[184:185] op_sel_hi:[1,0,1]
	v_pk_fma_f32 v[72:73], v[252:253], v[114:115], v[186:187] op_sel:[0,1,0] op_sel_hi:[1,1,1]
	v_pk_fma_f32 v[74:75], v[252:253], v[116:117], v[188:189] op_sel_hi:[1,0,1]
	v_pk_fma_f32 v[76:77], v[252:253], v[116:117], v[190:191] op_sel:[0,1,0] op_sel_hi:[1,1,1]
	v_pk_mul_f32 v[192:193], v[70:71], v[122:123] op_sel_hi:[1,0]
	v_pk_fma_f32 v[192:193], v[72:73], v[122:123], v[192:193] op_sel:[0,1,0] op_sel_hi:[1,1,1]
	v_pk_fma_f32 v[192:193], v[74:75], v[124:125], v[192:193] op_sel_hi:[1,0,1]
	v_pk_fma_f32 v[192:193], v[76:77], v[124:125], v[192:193] op_sel:[0,1,0] op_sel_hi:[1,1,1]

	s_waitcnt lgkmcnt(0)
	v_cndmask_b32_e64 v92, v92, v161, s[6:7]
	ds_read_b128 v[82:85], v79 offset:0x1400
	ds_read_b128 v[86:89], v79 offset:0x3400
	ds_read_b128 v[114:117], v79 offset:0x5400
	ds_read_b128 v[118:121], v79 offset:0x7400
	ds_read_b128 v[122:125], v79 offset:0x9400
	ds_read_b32 v126, v80 offset:0xa00
	ds_read_b32 v127, v81 offset:0xa00
	v_pk_mul_f32 v[250:251], v[70:71], v[166:167] op_sel_hi:[1,0]
	v_pk_fma_f32 v[250:251], v[72:73], v[166:167], v[250:251] op_sel:[0,1,0] op_sel_hi:[1,1,1]
	v_pk_fma_f32 v[250:251], v[74:75], v[168:169], v[250:251] op_sel_hi:[1,0,1]
	v_pk_fma_f32 v[250:251], v[76:77], v[168:169], v[250:251] op_sel:[0,1,0] op_sel_hi:[1,1,1]
	v_pk_mul_f32 v[184:185], v[182:183], v[174:175] op_sel_hi:[1,0]
	v_pk_mul_f32 v[186:187], v[182:183], v[174:175] op_sel:[0,1] op_sel_hi:[1,1]
	v_add_f32_dpp v252, v251, v250 quad_perm:[1,0,3,2] row_mask:0xf bank_mask:0xf bound_ctrl:1
	v_add_f32_dpp v161, v193, v192 quad_perm:[1,0,3,2] row_mask:0xf bank_mask:0xf bound_ctrl:1
	v_pk_mul_f32 v[188:189], v[182:183], v[176:177] op_sel_hi:[1,0]
	v_add_f32_dpp v252, v252, v252 quad_perm:[2,3,0,1] row_mask:0xf bank_mask:0xf bound_ctrl:1
	v_add_f32_dpp v161, v161, v161 quad_perm:[2,3,0,1] row_mask:0xf bank_mask:0xf bound_ctrl:1
	v_pk_mul_f32 v[190:191], v[182:183], v[176:177] op_sel:[0,1] op_sel_hi:[1,1]
	v_add_f32_dpp v252, v252, v252 row_ror:4 row_mask:0xf bank_mask:0xf bound_ctrl:1
	v_add_f32_dpp v161, v161, v161 row_ror:4 row_mask:0xf bank_mask:0xf bound_ctrl:1
	v_pk_fma_f32 v[184:185], v[70:71], v[162:163], v[184:185] op_sel_hi:[1,0,1]
	v_add_f32_dpp v252, v252, v252 row_ror:8 row_mask:0xf bank_mask:0xf bound_ctrl:1
	v_add_f32_dpp v161, v161, v161 row_ror:8 row_mask:0xf bank_mask:0xf bound_ctrl:1
	v_pk_fma_f32 v[186:187], v[72:73], v[162:163], v[186:187] op_sel:[0,1,0] op_sel_hi:[1,1,1]
	v_mov_b32_dpp v253, v252 quad_perm:[1,0,3,2] row_mask:0xf bank_mask:0xf bound_ctrl:1
	v_pk_fma_f32 v[188:189], v[74:75], v[164:165], v[188:189] op_sel_hi:[1,0,1]
	v_pk_fma_f32 v[190:191], v[76:77], v[164:165], v[190:191] op_sel:[0,1,0] op_sel_hi:[1,1,1]
	v_pk_fma_f32 v[70:71], v[252:253], v[170:171], v[184:185] op_sel_hi:[1,0,1]
	v_pk_fma_f32 v[72:73], v[252:253], v[170:171], v[186:187] op_sel:[0,1,0] op_sel_hi:[1,1,1]
	v_pk_fma_f32 v[74:75], v[252:253], v[172:173], v[188:189] op_sel_hi:[1,0,1]
	v_pk_fma_f32 v[76:77], v[252:253], v[172:173], v[190:191] op_sel:[0,1,0] op_sel_hi:[1,1,1]
	v_pk_mul_f32 v[194:195], v[70:71], v[178:179] op_sel_hi:[1,0]
	v_pk_fma_f32 v[194:195], v[72:73], v[178:179], v[194:195] op_sel:[0,1,0] op_sel_hi:[1,1,1]
	v_pk_fma_f32 v[194:195], v[74:75], v[180:181], v[194:195] op_sel_hi:[1,0,1]
	v_pk_fma_f32 v[194:195], v[76:77], v[180:181], v[194:195] op_sel:[0,1,0] op_sel_hi:[1,1,1]

	s_waitcnt lgkmcnt(0)
	v_cndmask_b32_e64 v92, v92, v161, s[8:9]
	ds_read_b128 v[162:165], v79 offset:0x1500
	ds_read_b128 v[166:169], v79 offset:0x3500
	ds_read_b128 v[170:173], v79 offset:0x5500
	ds_read_b128 v[174:177], v79 offset:0x7500
	ds_read_b128 v[178:181], v79 offset:0x9500
	ds_read_b32 v182, v80 offset:0xa80
	ds_read_b32 v183, v81 offset:0xa80
	v_pk_mul_f32 v[250:251], v[70:71], v[86:87] op_sel_hi:[1,0]
	v_pk_fma_f32 v[250:251], v[72:73], v[86:87], v[250:251] op_sel:[0,1,0] op_sel_hi:[1,1,1]
	v_pk_fma_f32 v[250:251], v[74:75], v[88:89], v[250:251] op_sel_hi:[1,0,1]
	v_pk_fma_f32 v[250:251], v[76:77], v[88:89], v[250:251] op_sel:[0,1,0] op_sel_hi:[1,1,1]
	v_pk_mul_f32 v[184:185], v[126:127], v[118:119] op_sel_hi:[1,0]
	v_pk_mul_f32 v[186:187], v[126:127], v[118:119] op_sel:[0,1] op_sel_hi:[1,1]
	v_add_f32_dpp v252, v251, v250 quad_perm:[1,0,3,2] row_mask:0xf bank_mask:0xf bound_ctrl:1
	v_add_f32_dpp v161, v195, v194 quad_perm:[1,0,3,2] row_mask:0xf bank_mask:0xf bound_ctrl:1
	v_pk_mul_f32 v[188:189], v[126:127], v[120:121] op_sel_hi:[1,0]
	v_add_f32_dpp v252, v252, v252 quad_perm:[2,3,0,1] row_mask:0xf bank_mask:0xf bound_ctrl:1
	v_add_f32_dpp v161, v161, v161 quad_perm:[2,3,0,1] row_mask:0xf bank_mask:0xf bound_ctrl:1
	v_pk_mul_f32 v[190:191], v[126:127], v[120:121] op_sel:[0,1] op_sel_hi:[1,1]
	v_add_f32_dpp v252, v252, v252 row_ror:4 row_mask:0xf bank_mask:0xf bound_ctrl:1
	v_add_f32_dpp v161, v161, v161 row_ror:4 row_mask:0xf bank_mask:0xf bound_ctrl:1
	v_pk_fma_f32 v[184:185], v[70:71], v[82:83], v[184:185] op_sel_hi:[1,0,1]
	v_add_f32_dpp v252, v252, v252 row_ror:8 row_mask:0xf bank_mask:0xf bound_ctrl:1
	v_add_f32_dpp v161, v161, v161 row_ror:8 row_mask:0xf bank_mask:0xf bound_ctrl:1
	v_pk_fma_f32 v[186:187], v[72:73], v[82:83], v[186:187] op_sel:[0,1,0] op_sel_hi:[1,1,1]
	v_mov_b32_dpp v253, v252 quad_perm:[1,0,3,2] row_mask:0xf bank_mask:0xf bound_ctrl:1
	v_pk_fma_f32 v[188:189], v[74:75], v[84:85], v[188:189] op_sel_hi:[1,0,1]
	v_pk_fma_f32 v[190:191], v[76:77], v[84:85], v[190:191] op_sel:[0,1,0] op_sel_hi:[1,1,1]
	v_pk_fma_f32 v[70:71], v[252:253], v[114:115], v[184:185] op_sel_hi:[1,0,1]
	v_pk_fma_f32 v[72:73], v[252:253], v[114:115], v[186:187] op_sel:[0,1,0] op_sel_hi:[1,1,1]
	v_pk_fma_f32 v[74:75], v[252:253], v[116:117], v[188:189] op_sel_hi:[1,0,1]
	v_pk_fma_f32 v[76:77], v[252:253], v[116:117], v[190:191] op_sel:[0,1,0] op_sel_hi:[1,1,1]
	v_pk_mul_f32 v[192:193], v[70:71], v[122:123] op_sel_hi:[1,0]
	v_pk_fma_f32 v[192:193], v[72:73], v[122:123], v[192:193] op_sel:[0,1,0] op_sel_hi:[1,1,1]
	v_pk_fma_f32 v[192:193], v[74:75], v[124:125], v[192:193] op_sel_hi:[1,0,1]
	v_pk_fma_f32 v[192:193], v[76:77], v[124:125], v[192:193] op_sel:[0,1,0] op_sel_hi:[1,1,1]

	s_waitcnt lgkmcnt(0)
	v_cndmask_b32_e64 v92, v92, v161, s[10:11]
	ds_read_b128 v[82:85], v79 offset:0x1600
	ds_read_b128 v[86:89], v79 offset:0x3600
	ds_read_b128 v[114:117], v79 offset:0x5600
	ds_read_b128 v[118:121], v79 offset:0x7600
	ds_read_b128 v[122:125], v79 offset:0x9600
	ds_read_b32 v126, v80 offset:0xb00
	ds_read_b32 v127, v81 offset:0xb00
	v_pk_mul_f32 v[250:251], v[70:71], v[166:167] op_sel_hi:[1,0]
	v_pk_fma_f32 v[250:251], v[72:73], v[166:167], v[250:251] op_sel:[0,1,0] op_sel_hi:[1,1,1]
	v_pk_fma_f32 v[250:251], v[74:75], v[168:169], v[250:251] op_sel_hi:[1,0,1]
	v_pk_fma_f32 v[250:251], v[76:77], v[168:169], v[250:251] op_sel:[0,1,0] op_sel_hi:[1,1,1]
	v_pk_mul_f32 v[184:185], v[182:183], v[174:175] op_sel_hi:[1,0]
	v_pk_mul_f32 v[186:187], v[182:183], v[174:175] op_sel:[0,1] op_sel_hi:[1,1]
	v_add_f32_dpp v252, v251, v250 quad_perm:[1,0,3,2] row_mask:0xf bank_mask:0xf bound_ctrl:1
	v_add_f32_dpp v161, v193, v192 quad_perm:[1,0,3,2] row_mask:0xf bank_mask:0xf bound_ctrl:1
	v_pk_mul_f32 v[188:189], v[182:183], v[176:177] op_sel_hi:[1,0]
	v_add_f32_dpp v252, v252, v252 quad_perm:[2,3,0,1] row_mask:0xf bank_mask:0xf bound_ctrl:1
	v_add_f32_dpp v161, v161, v161 quad_perm:[2,3,0,1] row_mask:0xf bank_mask:0xf bound_ctrl:1
	v_pk_mul_f32 v[190:191], v[182:183], v[176:177] op_sel:[0,1] op_sel_hi:[1,1]
	v_add_f32_dpp v252, v252, v252 row_ror:4 row_mask:0xf bank_mask:0xf bound_ctrl:1
	v_add_f32_dpp v161, v161, v161 row_ror:4 row_mask:0xf bank_mask:0xf bound_ctrl:1
	v_pk_fma_f32 v[184:185], v[70:71], v[162:163], v[184:185] op_sel_hi:[1,0,1]
	v_add_f32_dpp v252, v252, v252 row_ror:8 row_mask:0xf bank_mask:0xf bound_ctrl:1
	v_add_f32_dpp v161, v161, v161 row_ror:8 row_mask:0xf bank_mask:0xf bound_ctrl:1
	v_pk_fma_f32 v[186:187], v[72:73], v[162:163], v[186:187] op_sel:[0,1,0] op_sel_hi:[1,1,1]
	v_mov_b32_dpp v253, v252 quad_perm:[1,0,3,2] row_mask:0xf bank_mask:0xf bound_ctrl:1
	v_pk_fma_f32 v[188:189], v[74:75], v[164:165], v[188:189] op_sel_hi:[1,0,1]
	v_pk_fma_f32 v[190:191], v[76:77], v[164:165], v[190:191] op_sel:[0,1,0] op_sel_hi:[1,1,1]
	v_pk_fma_f32 v[70:71], v[252:253], v[170:171], v[184:185] op_sel_hi:[1,0,1]
	v_pk_fma_f32 v[72:73], v[252:253], v[170:171], v[186:187] op_sel:[0,1,0] op_sel_hi:[1,1,1]
	v_pk_fma_f32 v[74:75], v[252:253], v[172:173], v[188:189] op_sel_hi:[1,0,1]
	v_pk_fma_f32 v[76:77], v[252:253], v[172:173], v[190:191] op_sel:[0,1,0] op_sel_hi:[1,1,1]
	v_pk_mul_f32 v[194:195], v[70:71], v[178:179] op_sel_hi:[1,0]
	v_pk_fma_f32 v[194:195], v[72:73], v[178:179], v[194:195] op_sel:[0,1,0] op_sel_hi:[1,1,1]
	v_pk_fma_f32 v[194:195], v[74:75], v[180:181], v[194:195] op_sel_hi:[1,0,1]
	v_pk_fma_f32 v[194:195], v[76:77], v[180:181], v[194:195] op_sel:[0,1,0] op_sel_hi:[1,1,1]

	s_waitcnt lgkmcnt(0)
	v_cndmask_b32_e64 v92, v92, v161, s[12:13]
	ds_read_b128 v[162:165], v79 offset:0x1700
	ds_read_b128 v[166:169], v79 offset:0x3700
	ds_read_b128 v[170:173], v79 offset:0x5700
	ds_read_b128 v[174:177], v79 offset:0x7700
	ds_read_b128 v[178:181], v79 offset:0x9700
	ds_read_b32 v182, v80 offset:0xb80
	ds_read_b32 v183, v81 offset:0xb80
	v_pk_mul_f32 v[250:251], v[70:71], v[86:87] op_sel_hi:[1,0]
	v_pk_fma_f32 v[250:251], v[72:73], v[86:87], v[250:251] op_sel:[0,1,0] op_sel_hi:[1,1,1]
	v_pk_fma_f32 v[250:251], v[74:75], v[88:89], v[250:251] op_sel_hi:[1,0,1]
	v_pk_fma_f32 v[250:251], v[76:77], v[88:89], v[250:251] op_sel:[0,1,0] op_sel_hi:[1,1,1]
	v_pk_mul_f32 v[184:185], v[126:127], v[118:119] op_sel_hi:[1,0]
	v_pk_mul_f32 v[186:187], v[126:127], v[118:119] op_sel:[0,1] op_sel_hi:[1,1]
	v_add_f32_dpp v252, v251, v250 quad_perm:[1,0,3,2] row_mask:0xf bank_mask:0xf bound_ctrl:1
	v_add_f32_dpp v161, v195, v194 quad_perm:[1,0,3,2] row_mask:0xf bank_mask:0xf bound_ctrl:1
	v_pk_mul_f32 v[188:189], v[126:127], v[120:121] op_sel_hi:[1,0]
	v_add_f32_dpp v252, v252, v252 quad_perm:[2,3,0,1] row_mask:0xf bank_mask:0xf bound_ctrl:1
	v_add_f32_dpp v161, v161, v161 quad_perm:[2,3,0,1] row_mask:0xf bank_mask:0xf bound_ctrl:1
	v_pk_mul_f32 v[190:191], v[126:127], v[120:121] op_sel:[0,1] op_sel_hi:[1,1]
	v_add_f32_dpp v252, v252, v252 row_ror:4 row_mask:0xf bank_mask:0xf bound_ctrl:1
	v_add_f32_dpp v161, v161, v161 row_ror:4 row_mask:0xf bank_mask:0xf bound_ctrl:1
	v_pk_fma_f32 v[184:185], v[70:71], v[82:83], v[184:185] op_sel_hi:[1,0,1]
	v_add_f32_dpp v252, v252, v252 row_ror:8 row_mask:0xf bank_mask:0xf bound_ctrl:1
	v_add_f32_dpp v161, v161, v161 row_ror:8 row_mask:0xf bank_mask:0xf bound_ctrl:1
	v_pk_fma_f32 v[186:187], v[72:73], v[82:83], v[186:187] op_sel:[0,1,0] op_sel_hi:[1,1,1]
	v_mov_b32_dpp v253, v252 quad_perm:[1,0,3,2] row_mask:0xf bank_mask:0xf bound_ctrl:1
	v_pk_fma_f32 v[188:189], v[74:75], v[84:85], v[188:189] op_sel_hi:[1,0,1]
	v_pk_fma_f32 v[190:191], v[76:77], v[84:85], v[190:191] op_sel:[0,1,0] op_sel_hi:[1,1,1]
	v_pk_fma_f32 v[70:71], v[252:253], v[114:115], v[184:185] op_sel_hi:[1,0,1]
	v_pk_fma_f32 v[72:73], v[252:253], v[114:115], v[186:187] op_sel:[0,1,0] op_sel_hi:[1,1,1]
	v_pk_fma_f32 v[74:75], v[252:253], v[116:117], v[188:189] op_sel_hi:[1,0,1]
	v_pk_fma_f32 v[76:77], v[252:253], v[116:117], v[190:191] op_sel:[0,1,0] op_sel_hi:[1,1,1]
	v_pk_mul_f32 v[192:193], v[70:71], v[122:123] op_sel_hi:[1,0]
	v_pk_fma_f32 v[192:193], v[72:73], v[122:123], v[192:193] op_sel:[0,1,0] op_sel_hi:[1,1,1]
	v_pk_fma_f32 v[192:193], v[74:75], v[124:125], v[192:193] op_sel_hi:[1,0,1]
	v_pk_fma_f32 v[192:193], v[76:77], v[124:125], v[192:193] op_sel:[0,1,0] op_sel_hi:[1,1,1]

	s_waitcnt lgkmcnt(0)
	v_cndmask_b32_e64 v92, v92, v161, s[14:15]
	ds_read_b128 v[82:85], v79 offset:0x1800
	ds_read_b128 v[86:89], v79 offset:0x3800
	ds_read_b128 v[114:117], v79 offset:0x5800
	ds_read_b128 v[118:121], v79 offset:0x7800
	ds_read_b128 v[122:125], v79 offset:0x9800
	ds_read_b32 v126, v80 offset:0xc00
	ds_read_b32 v127, v81 offset:0xc00
	v_pk_mul_f32 v[250:251], v[70:71], v[166:167] op_sel_hi:[1,0]
	v_pk_fma_f32 v[250:251], v[72:73], v[166:167], v[250:251] op_sel:[0,1,0] op_sel_hi:[1,1,1]
	v_pk_fma_f32 v[250:251], v[74:75], v[168:169], v[250:251] op_sel_hi:[1,0,1]
	v_pk_fma_f32 v[250:251], v[76:77], v[168:169], v[250:251] op_sel:[0,1,0] op_sel_hi:[1,1,1]
	v_pk_mul_f32 v[184:185], v[182:183], v[174:175] op_sel_hi:[1,0]
	v_pk_mul_f32 v[186:187], v[182:183], v[174:175] op_sel:[0,1] op_sel_hi:[1,1]
	v_add_f32_dpp v252, v251, v250 quad_perm:[1,0,3,2] row_mask:0xf bank_mask:0xf bound_ctrl:1
	v_add_f32_dpp v161, v193, v192 quad_perm:[1,0,3,2] row_mask:0xf bank_mask:0xf bound_ctrl:1
	v_pk_mul_f32 v[188:189], v[182:183], v[176:177] op_sel_hi:[1,0]
	v_add_f32_dpp v252, v252, v252 quad_perm:[2,3,0,1] row_mask:0xf bank_mask:0xf bound_ctrl:1
	v_add_f32_dpp v161, v161, v161 quad_perm:[2,3,0,1] row_mask:0xf bank_mask:0xf bound_ctrl:1
	v_pk_mul_f32 v[190:191], v[182:183], v[176:177] op_sel:[0,1] op_sel_hi:[1,1]
	v_add_f32_dpp v252, v252, v252 row_ror:4 row_mask:0xf bank_mask:0xf bound_ctrl:1
	v_add_f32_dpp v161, v161, v161 row_ror:4 row_mask:0xf bank_mask:0xf bound_ctrl:1
	v_pk_fma_f32 v[184:185], v[70:71], v[162:163], v[184:185] op_sel_hi:[1,0,1]
	v_add_f32_dpp v252, v252, v252 row_ror:8 row_mask:0xf bank_mask:0xf bound_ctrl:1
	v_add_f32_dpp v161, v161, v161 row_ror:8 row_mask:0xf bank_mask:0xf bound_ctrl:1
	v_pk_fma_f32 v[186:187], v[72:73], v[162:163], v[186:187] op_sel:[0,1,0] op_sel_hi:[1,1,1]
	v_mov_b32_dpp v253, v252 quad_perm:[1,0,3,2] row_mask:0xf bank_mask:0xf bound_ctrl:1
	v_pk_fma_f32 v[188:189], v[74:75], v[164:165], v[188:189] op_sel_hi:[1,0,1]
	v_pk_fma_f32 v[190:191], v[76:77], v[164:165], v[190:191] op_sel:[0,1,0] op_sel_hi:[1,1,1]
	v_pk_fma_f32 v[70:71], v[252:253], v[170:171], v[184:185] op_sel_hi:[1,0,1]
	v_pk_fma_f32 v[72:73], v[252:253], v[170:171], v[186:187] op_sel:[0,1,0] op_sel_hi:[1,1,1]
	v_pk_fma_f32 v[74:75], v[252:253], v[172:173], v[188:189] op_sel_hi:[1,0,1]
	v_pk_fma_f32 v[76:77], v[252:253], v[172:173], v[190:191] op_sel:[0,1,0] op_sel_hi:[1,1,1]
	v_pk_mul_f32 v[194:195], v[70:71], v[178:179] op_sel_hi:[1,0]
	v_pk_fma_f32 v[194:195], v[72:73], v[178:179], v[194:195] op_sel:[0,1,0] op_sel_hi:[1,1,1]
	v_pk_fma_f32 v[194:195], v[74:75], v[180:181], v[194:195] op_sel_hi:[1,0,1]
	v_pk_fma_f32 v[194:195], v[76:77], v[180:181], v[194:195] op_sel:[0,1,0] op_sel_hi:[1,1,1]

	s_waitcnt lgkmcnt(0)
	v_cndmask_b32_e64 v92, v92, v161, s[16:17]
	ds_read_b128 v[162:165], v79 offset:0x1900
	ds_read_b128 v[166:169], v79 offset:0x3900
	ds_read_b128 v[170:173], v79 offset:0x5900
	ds_read_b128 v[174:177], v79 offset:0x7900
	ds_read_b128 v[178:181], v79 offset:0x9900
	ds_read_b32 v182, v80 offset:0xc80
	ds_read_b32 v183, v81 offset:0xc80
	v_pk_mul_f32 v[250:251], v[70:71], v[86:87] op_sel_hi:[1,0]
	v_pk_fma_f32 v[250:251], v[72:73], v[86:87], v[250:251] op_sel:[0,1,0] op_sel_hi:[1,1,1]
	v_pk_fma_f32 v[250:251], v[74:75], v[88:89], v[250:251] op_sel_hi:[1,0,1]
	v_pk_fma_f32 v[250:251], v[76:77], v[88:89], v[250:251] op_sel:[0,1,0] op_sel_hi:[1,1,1]
	v_pk_mul_f32 v[184:185], v[126:127], v[118:119] op_sel_hi:[1,0]
	v_pk_mul_f32 v[186:187], v[126:127], v[118:119] op_sel:[0,1] op_sel_hi:[1,1]
	v_add_f32_dpp v252, v251, v250 quad_perm:[1,0,3,2] row_mask:0xf bank_mask:0xf bound_ctrl:1
	v_add_f32_dpp v161, v195, v194 quad_perm:[1,0,3,2] row_mask:0xf bank_mask:0xf bound_ctrl:1
	v_pk_mul_f32 v[188:189], v[126:127], v[120:121] op_sel_hi:[1,0]
	v_add_f32_dpp v252, v252, v252 quad_perm:[2,3,0,1] row_mask:0xf bank_mask:0xf bound_ctrl:1
	v_add_f32_dpp v161, v161, v161 quad_perm:[2,3,0,1] row_mask:0xf bank_mask:0xf bound_ctrl:1
	v_pk_mul_f32 v[190:191], v[126:127], v[120:121] op_sel:[0,1] op_sel_hi:[1,1]
	v_add_f32_dpp v252, v252, v252 row_ror:4 row_mask:0xf bank_mask:0xf bound_ctrl:1
	v_add_f32_dpp v161, v161, v161 row_ror:4 row_mask:0xf bank_mask:0xf bound_ctrl:1
	v_pk_fma_f32 v[184:185], v[70:71], v[82:83], v[184:185] op_sel_hi:[1,0,1]
	v_add_f32_dpp v252, v252, v252 row_ror:8 row_mask:0xf bank_mask:0xf bound_ctrl:1
	v_add_f32_dpp v161, v161, v161 row_ror:8 row_mask:0xf bank_mask:0xf bound_ctrl:1
	v_pk_fma_f32 v[186:187], v[72:73], v[82:83], v[186:187] op_sel:[0,1,0] op_sel_hi:[1,1,1]
	v_mov_b32_dpp v253, v252 quad_perm:[1,0,3,2] row_mask:0xf bank_mask:0xf bound_ctrl:1
	v_pk_fma_f32 v[188:189], v[74:75], v[84:85], v[188:189] op_sel_hi:[1,0,1]
	v_pk_fma_f32 v[190:191], v[76:77], v[84:85], v[190:191] op_sel:[0,1,0] op_sel_hi:[1,1,1]
	v_pk_fma_f32 v[70:71], v[252:253], v[114:115], v[184:185] op_sel_hi:[1,0,1]
	v_pk_fma_f32 v[72:73], v[252:253], v[114:115], v[186:187] op_sel:[0,1,0] op_sel_hi:[1,1,1]
	v_pk_fma_f32 v[74:75], v[252:253], v[116:117], v[188:189] op_sel_hi:[1,0,1]
	v_pk_fma_f32 v[76:77], v[252:253], v[116:117], v[190:191] op_sel:[0,1,0] op_sel_hi:[1,1,1]
	v_pk_mul_f32 v[192:193], v[70:71], v[122:123] op_sel_hi:[1,0]
	v_pk_fma_f32 v[192:193], v[72:73], v[122:123], v[192:193] op_sel:[0,1,0] op_sel_hi:[1,1,1]
	v_pk_fma_f32 v[192:193], v[74:75], v[124:125], v[192:193] op_sel_hi:[1,0,1]
	v_pk_fma_f32 v[192:193], v[76:77], v[124:125], v[192:193] op_sel:[0,1,0] op_sel_hi:[1,1,1]

	s_nop 0
	v_cndmask_b32_e64 v82, v92, v161, s[18:19]
	ds_write_b32 v78, v82 offset:2048
	s_waitcnt lgkmcnt(0)
	s_nop 0
	ds_read_b128 v[82:85], v79 offset:0x1a00
	ds_read_b128 v[86:89], v79 offset:0x3a00
	ds_read_b128 v[114:117], v79 offset:0x5a00
	ds_read_b128 v[118:121], v79 offset:0x7a00
	ds_read_b128 v[122:125], v79 offset:0x9a00
	ds_read_b32 v126, v80 offset:0xd00
	ds_read_b32 v127, v81 offset:0xd00
	v_pk_mul_f32 v[250:251], v[70:71], v[166:167] op_sel_hi:[1,0]
	v_pk_fma_f32 v[250:251], v[72:73], v[166:167], v[250:251] op_sel:[0,1,0] op_sel_hi:[1,1,1]
	v_pk_fma_f32 v[250:251], v[74:75], v[168:169], v[250:251] op_sel_hi:[1,0,1]
	v_pk_fma_f32 v[250:251], v[76:77], v[168:169], v[250:251] op_sel:[0,1,0] op_sel_hi:[1,1,1]
	v_pk_mul_f32 v[184:185], v[182:183], v[174:175] op_sel_hi:[1,0]
	v_pk_mul_f32 v[186:187], v[182:183], v[174:175] op_sel:[0,1] op_sel_hi:[1,1]
	v_add_f32_dpp v252, v251, v250 quad_perm:[1,0,3,2] row_mask:0xf bank_mask:0xf bound_ctrl:1
	v_add_f32_dpp v92, v193, v192 quad_perm:[1,0,3,2] row_mask:0xf bank_mask:0xf bound_ctrl:1
	v_pk_mul_f32 v[188:189], v[182:183], v[176:177] op_sel_hi:[1,0]
	v_add_f32_dpp v252, v252, v252 quad_perm:[2,3,0,1] row_mask:0xf bank_mask:0xf bound_ctrl:1
	v_add_f32_dpp v92, v92, v92 quad_perm:[2,3,0,1] row_mask:0xf bank_mask:0xf bound_ctrl:1
	v_pk_mul_f32 v[190:191], v[182:183], v[176:177] op_sel:[0,1] op_sel_hi:[1,1]
	v_add_f32_dpp v252, v252, v252 row_ror:4 row_mask:0xf bank_mask:0xf bound_ctrl:1
	v_add_f32_dpp v92, v92, v92 row_ror:4 row_mask:0xf bank_mask:0xf bound_ctrl:1
	v_pk_fma_f32 v[184:185], v[70:71], v[162:163], v[184:185] op_sel_hi:[1,0,1]
	v_add_f32_dpp v252, v252, v252 row_ror:8 row_mask:0xf bank_mask:0xf bound_ctrl:1
	v_add_f32_dpp v92, v92, v92 row_ror:8 row_mask:0xf bank_mask:0xf bound_ctrl:1
	v_pk_fma_f32 v[186:187], v[72:73], v[162:163], v[186:187] op_sel:[0,1,0] op_sel_hi:[1,1,1]
	v_mov_b32_dpp v253, v252 quad_perm:[1,0,3,2] row_mask:0xf bank_mask:0xf bound_ctrl:1
	v_pk_fma_f32 v[188:189], v[74:75], v[164:165], v[188:189] op_sel_hi:[1,0,1]
	v_pk_fma_f32 v[190:191], v[76:77], v[164:165], v[190:191] op_sel:[0,1,0] op_sel_hi:[1,1,1]
	v_pk_fma_f32 v[70:71], v[252:253], v[170:171], v[184:185] op_sel_hi:[1,0,1]
	v_pk_fma_f32 v[72:73], v[252:253], v[170:171], v[186:187] op_sel:[0,1,0] op_sel_hi:[1,1,1]
	v_pk_fma_f32 v[74:75], v[252:253], v[172:173], v[188:189] op_sel_hi:[1,0,1]
	v_pk_fma_f32 v[76:77], v[252:253], v[172:173], v[190:191] op_sel:[0,1,0] op_sel_hi:[1,1,1]
	v_pk_mul_f32 v[194:195], v[70:71], v[178:179] op_sel_hi:[1,0]
	v_pk_fma_f32 v[194:195], v[72:73], v[178:179], v[194:195] op_sel:[0,1,0] op_sel_hi:[1,1,1]
	v_pk_fma_f32 v[194:195], v[74:75], v[180:181], v[194:195] op_sel_hi:[1,0,1]
	v_pk_fma_f32 v[194:195], v[76:77], v[180:181], v[194:195] op_sel:[0,1,0] op_sel_hi:[1,1,1]

	s_waitcnt lgkmcnt(0)
	v_cndmask_b32_e64 v92, 0, v92, s[4:5]
	ds_read_b128 v[162:165], v79 offset:0x1b00
	ds_read_b128 v[166:169], v79 offset:0x3b00
	ds_read_b128 v[170:173], v79 offset:0x5b00
	ds_read_b128 v[174:177], v79 offset:0x7b00
	ds_read_b128 v[178:181], v79 offset:0x9b00
	ds_read_b32 v182, v80 offset:0xd80
	ds_read_b32 v183, v81 offset:0xd80
	v_pk_mul_f32 v[250:251], v[70:71], v[86:87] op_sel_hi:[1,0]
	v_pk_fma_f32 v[250:251], v[72:73], v[86:87], v[250:251] op_sel:[0,1,0] op_sel_hi:[1,1,1]
	v_pk_fma_f32 v[250:251], v[74:75], v[88:89], v[250:251] op_sel_hi:[1,0,1]
	v_pk_fma_f32 v[250:251], v[76:77], v[88:89], v[250:251] op_sel:[0,1,0] op_sel_hi:[1,1,1]
	v_pk_mul_f32 v[184:185], v[126:127], v[118:119] op_sel_hi:[1,0]
	v_pk_mul_f32 v[186:187], v[126:127], v[118:119] op_sel:[0,1] op_sel_hi:[1,1]
	v_add_f32_dpp v252, v251, v250 quad_perm:[1,0,3,2] row_mask:0xf bank_mask:0xf bound_ctrl:1
	v_add_f32_dpp v161, v195, v194 quad_perm:[1,0,3,2] row_mask:0xf bank_mask:0xf bound_ctrl:1
	v_pk_mul_f32 v[188:189], v[126:127], v[120:121] op_sel_hi:[1,0]
	v_add_f32_dpp v252, v252, v252 quad_perm:[2,3,0,1] row_mask:0xf bank_mask:0xf bound_ctrl:1
	v_add_f32_dpp v161, v161, v161 quad_perm:[2,3,0,1] row_mask:0xf bank_mask:0xf bound_ctrl:1
	v_pk_mul_f32 v[190:191], v[126:127], v[120:121] op_sel:[0,1] op_sel_hi:[1,1]
	v_add_f32_dpp v252, v252, v252 row_ror:4 row_mask:0xf bank_mask:0xf bound_ctrl:1
	v_add_f32_dpp v161, v161, v161 row_ror:4 row_mask:0xf bank_mask:0xf bound_ctrl:1
	v_pk_fma_f32 v[184:185], v[70:71], v[82:83], v[184:185] op_sel_hi:[1,0,1]
	v_add_f32_dpp v252, v252, v252 row_ror:8 row_mask:0xf bank_mask:0xf bound_ctrl:1
	v_add_f32_dpp v161, v161, v161 row_ror:8 row_mask:0xf bank_mask:0xf bound_ctrl:1
	v_pk_fma_f32 v[186:187], v[72:73], v[82:83], v[186:187] op_sel:[0,1,0] op_sel_hi:[1,1,1]
	v_mov_b32_dpp v253, v252 quad_perm:[1,0,3,2] row_mask:0xf bank_mask:0xf bound_ctrl:1
	v_pk_fma_f32 v[188:189], v[74:75], v[84:85], v[188:189] op_sel_hi:[1,0,1]
	v_pk_fma_f32 v[190:191], v[76:77], v[84:85], v[190:191] op_sel:[0,1,0] op_sel_hi:[1,1,1]
	v_pk_fma_f32 v[70:71], v[252:253], v[114:115], v[184:185] op_sel_hi:[1,0,1]
	v_pk_fma_f32 v[72:73], v[252:253], v[114:115], v[186:187] op_sel:[0,1,0] op_sel_hi:[1,1,1]
	v_pk_fma_f32 v[74:75], v[252:253], v[116:117], v[188:189] op_sel_hi:[1,0,1]
	v_pk_fma_f32 v[76:77], v[252:253], v[116:117], v[190:191] op_sel:[0,1,0] op_sel_hi:[1,1,1]
	v_pk_mul_f32 v[192:193], v[70:71], v[122:123] op_sel_hi:[1,0]
	v_pk_fma_f32 v[192:193], v[72:73], v[122:123], v[192:193] op_sel:[0,1,0] op_sel_hi:[1,1,1]
	v_pk_fma_f32 v[192:193], v[74:75], v[124:125], v[192:193] op_sel_hi:[1,0,1]
	v_pk_fma_f32 v[192:193], v[76:77], v[124:125], v[192:193] op_sel:[0,1,0] op_sel_hi:[1,1,1]

	s_waitcnt lgkmcnt(0)
	v_cndmask_b32_e64 v92, v92, v161, s[6:7]
	ds_read_b128 v[82:85], v79 offset:0x1c00
	ds_read_b128 v[86:89], v79 offset:0x3c00
	ds_read_b128 v[114:117], v79 offset:0x5c00
	ds_read_b128 v[118:121], v79 offset:0x7c00
	ds_read_b128 v[122:125], v79 offset:0x9c00
	ds_read_b32 v126, v80 offset:0xe00
	ds_read_b32 v127, v81 offset:0xe00
	v_pk_mul_f32 v[250:251], v[70:71], v[166:167] op_sel_hi:[1,0]
	v_pk_fma_f32 v[250:251], v[72:73], v[166:167], v[250:251] op_sel:[0,1,0] op_sel_hi:[1,1,1]
	v_pk_fma_f32 v[250:251], v[74:75], v[168:169], v[250:251] op_sel_hi:[1,0,1]
	v_pk_fma_f32 v[250:251], v[76:77], v[168:169], v[250:251] op_sel:[0,1,0] op_sel_hi:[1,1,1]
	v_pk_mul_f32 v[184:185], v[182:183], v[174:175] op_sel_hi:[1,0]
	v_pk_mul_f32 v[186:187], v[182:183], v[174:175] op_sel:[0,1] op_sel_hi:[1,1]
	v_add_f32_dpp v252, v251, v250 quad_perm:[1,0,3,2] row_mask:0xf bank_mask:0xf bound_ctrl:1
	v_add_f32_dpp v161, v193, v192 quad_perm:[1,0,3,2] row_mask:0xf bank_mask:0xf bound_ctrl:1
	v_pk_mul_f32 v[188:189], v[182:183], v[176:177] op_sel_hi:[1,0]
	v_add_f32_dpp v252, v252, v252 quad_perm:[2,3,0,1] row_mask:0xf bank_mask:0xf bound_ctrl:1
	v_add_f32_dpp v161, v161, v161 quad_perm:[2,3,0,1] row_mask:0xf bank_mask:0xf bound_ctrl:1
	v_pk_mul_f32 v[190:191], v[182:183], v[176:177] op_sel:[0,1] op_sel_hi:[1,1]
	v_add_f32_dpp v252, v252, v252 row_ror:4 row_mask:0xf bank_mask:0xf bound_ctrl:1
	v_add_f32_dpp v161, v161, v161 row_ror:4 row_mask:0xf bank_mask:0xf bound_ctrl:1
	v_pk_fma_f32 v[184:185], v[70:71], v[162:163], v[184:185] op_sel_hi:[1,0,1]
	v_add_f32_dpp v252, v252, v252 row_ror:8 row_mask:0xf bank_mask:0xf bound_ctrl:1
	v_add_f32_dpp v161, v161, v161 row_ror:8 row_mask:0xf bank_mask:0xf bound_ctrl:1
	v_pk_fma_f32 v[186:187], v[72:73], v[162:163], v[186:187] op_sel:[0,1,0] op_sel_hi:[1,1,1]
	v_mov_b32_dpp v253, v252 quad_perm:[1,0,3,2] row_mask:0xf bank_mask:0xf bound_ctrl:1
	v_pk_fma_f32 v[188:189], v[74:75], v[164:165], v[188:189] op_sel_hi:[1,0,1]
	v_pk_fma_f32 v[190:191], v[76:77], v[164:165], v[190:191] op_sel:[0,1,0] op_sel_hi:[1,1,1]
	v_pk_fma_f32 v[70:71], v[252:253], v[170:171], v[184:185] op_sel_hi:[1,0,1]
	v_pk_fma_f32 v[72:73], v[252:253], v[170:171], v[186:187] op_sel:[0,1,0] op_sel_hi:[1,1,1]
	v_pk_fma_f32 v[74:75], v[252:253], v[172:173], v[188:189] op_sel_hi:[1,0,1]
	v_pk_fma_f32 v[76:77], v[252:253], v[172:173], v[190:191] op_sel:[0,1,0] op_sel_hi:[1,1,1]
	v_pk_mul_f32 v[194:195], v[70:71], v[178:179] op_sel_hi:[1,0]
	v_pk_fma_f32 v[194:195], v[72:73], v[178:179], v[194:195] op_sel:[0,1,0] op_sel_hi:[1,1,1]
	v_pk_fma_f32 v[194:195], v[74:75], v[180:181], v[194:195] op_sel_hi:[1,0,1]
	v_pk_fma_f32 v[194:195], v[76:77], v[180:181], v[194:195] op_sel:[0,1,0] op_sel_hi:[1,1,1]

	s_waitcnt lgkmcnt(0)
	v_cndmask_b32_e64 v92, v92, v161, s[8:9]
	ds_read_b128 v[162:165], v79 offset:0x1d00
	ds_read_b128 v[166:169], v79 offset:0x3d00
	ds_read_b128 v[170:173], v79 offset:0x5d00
	ds_read_b128 v[174:177], v79 offset:0x7d00
	ds_read_b128 v[178:181], v79 offset:0x9d00
	ds_read_b32 v182, v80 offset:0xe80
	ds_read_b32 v183, v81 offset:0xe80
	v_pk_mul_f32 v[250:251], v[70:71], v[86:87] op_sel_hi:[1,0]
	v_pk_fma_f32 v[250:251], v[72:73], v[86:87], v[250:251] op_sel:[0,1,0] op_sel_hi:[1,1,1]
	v_pk_fma_f32 v[250:251], v[74:75], v[88:89], v[250:251] op_sel_hi:[1,0,1]
	v_pk_fma_f32 v[250:251], v[76:77], v[88:89], v[250:251] op_sel:[0,1,0] op_sel_hi:[1,1,1]
	v_pk_mul_f32 v[184:185], v[126:127], v[118:119] op_sel_hi:[1,0]
	v_pk_mul_f32 v[186:187], v[126:127], v[118:119] op_sel:[0,1] op_sel_hi:[1,1]
	v_add_f32_dpp v252, v251, v250 quad_perm:[1,0,3,2] row_mask:0xf bank_mask:0xf bound_ctrl:1
	v_add_f32_dpp v161, v195, v194 quad_perm:[1,0,3,2] row_mask:0xf bank_mask:0xf bound_ctrl:1
	v_pk_mul_f32 v[188:189], v[126:127], v[120:121] op_sel_hi:[1,0]
	v_add_f32_dpp v252, v252, v252 quad_perm:[2,3,0,1] row_mask:0xf bank_mask:0xf bound_ctrl:1
	v_add_f32_dpp v161, v161, v161 quad_perm:[2,3,0,1] row_mask:0xf bank_mask:0xf bound_ctrl:1
	v_pk_mul_f32 v[190:191], v[126:127], v[120:121] op_sel:[0,1] op_sel_hi:[1,1]
	v_add_f32_dpp v252, v252, v252 row_ror:4 row_mask:0xf bank_mask:0xf bound_ctrl:1
	v_add_f32_dpp v161, v161, v161 row_ror:4 row_mask:0xf bank_mask:0xf bound_ctrl:1
	v_pk_fma_f32 v[184:185], v[70:71], v[82:83], v[184:185] op_sel_hi:[1,0,1]
	v_add_f32_dpp v252, v252, v252 row_ror:8 row_mask:0xf bank_mask:0xf bound_ctrl:1
	v_add_f32_dpp v161, v161, v161 row_ror:8 row_mask:0xf bank_mask:0xf bound_ctrl:1
	v_pk_fma_f32 v[186:187], v[72:73], v[82:83], v[186:187] op_sel:[0,1,0] op_sel_hi:[1,1,1]
	v_mov_b32_dpp v253, v252 quad_perm:[1,0,3,2] row_mask:0xf bank_mask:0xf bound_ctrl:1
	v_pk_fma_f32 v[188:189], v[74:75], v[84:85], v[188:189] op_sel_hi:[1,0,1]
	v_pk_fma_f32 v[190:191], v[76:77], v[84:85], v[190:191] op_sel:[0,1,0] op_sel_hi:[1,1,1]
	v_pk_fma_f32 v[70:71], v[252:253], v[114:115], v[184:185] op_sel_hi:[1,0,1]
	v_pk_fma_f32 v[72:73], v[252:253], v[114:115], v[186:187] op_sel:[0,1,0] op_sel_hi:[1,1,1]
	v_pk_fma_f32 v[74:75], v[252:253], v[116:117], v[188:189] op_sel_hi:[1,0,1]
	v_pk_fma_f32 v[76:77], v[252:253], v[116:117], v[190:191] op_sel:[0,1,0] op_sel_hi:[1,1,1]
	v_pk_mul_f32 v[192:193], v[70:71], v[122:123] op_sel_hi:[1,0]
	v_pk_fma_f32 v[192:193], v[72:73], v[122:123], v[192:193] op_sel:[0,1,0] op_sel_hi:[1,1,1]
	v_pk_fma_f32 v[192:193], v[74:75], v[124:125], v[192:193] op_sel_hi:[1,0,1]
	v_pk_fma_f32 v[192:193], v[76:77], v[124:125], v[192:193] op_sel:[0,1,0] op_sel_hi:[1,1,1]

	s_waitcnt lgkmcnt(0)
	v_cndmask_b32_e64 v92, v92, v161, s[10:11]
	ds_read_b128 v[82:85], v79 offset:0x1e00
	ds_read_b128 v[86:89], v79 offset:0x3e00
	ds_read_b128 v[114:117], v79 offset:0x5e00
	ds_read_b128 v[118:121], v79 offset:0x7e00
	ds_read_b128 v[122:125], v79 offset:0x9e00
	ds_read_b32 v126, v80 offset:0xf00
	ds_read_b32 v127, v81 offset:0xf00
	v_pk_mul_f32 v[250:251], v[70:71], v[166:167] op_sel_hi:[1,0]
	v_pk_fma_f32 v[250:251], v[72:73], v[166:167], v[250:251] op_sel:[0,1,0] op_sel_hi:[1,1,1]
	v_pk_fma_f32 v[250:251], v[74:75], v[168:169], v[250:251] op_sel_hi:[1,0,1]
	v_pk_fma_f32 v[250:251], v[76:77], v[168:169], v[250:251] op_sel:[0,1,0] op_sel_hi:[1,1,1]
	v_pk_mul_f32 v[184:185], v[182:183], v[174:175] op_sel_hi:[1,0]
	v_pk_mul_f32 v[186:187], v[182:183], v[174:175] op_sel:[0,1] op_sel_hi:[1,1]
	v_add_f32_dpp v252, v251, v250 quad_perm:[1,0,3,2] row_mask:0xf bank_mask:0xf bound_ctrl:1
	v_add_f32_dpp v161, v193, v192 quad_perm:[1,0,3,2] row_mask:0xf bank_mask:0xf bound_ctrl:1
	v_pk_mul_f32 v[188:189], v[182:183], v[176:177] op_sel_hi:[1,0]
	v_add_f32_dpp v252, v252, v252 quad_perm:[2,3,0,1] row_mask:0xf bank_mask:0xf bound_ctrl:1
	v_add_f32_dpp v161, v161, v161 quad_perm:[2,3,0,1] row_mask:0xf bank_mask:0xf bound_ctrl:1
	v_pk_mul_f32 v[190:191], v[182:183], v[176:177] op_sel:[0,1] op_sel_hi:[1,1]
	v_add_f32_dpp v252, v252, v252 row_ror:4 row_mask:0xf bank_mask:0xf bound_ctrl:1
	v_add_f32_dpp v161, v161, v161 row_ror:4 row_mask:0xf bank_mask:0xf bound_ctrl:1
	v_pk_fma_f32 v[184:185], v[70:71], v[162:163], v[184:185] op_sel_hi:[1,0,1]
	v_add_f32_dpp v252, v252, v252 row_ror:8 row_mask:0xf bank_mask:0xf bound_ctrl:1
	v_add_f32_dpp v161, v161, v161 row_ror:8 row_mask:0xf bank_mask:0xf bound_ctrl:1
	v_pk_fma_f32 v[186:187], v[72:73], v[162:163], v[186:187] op_sel:[0,1,0] op_sel_hi:[1,1,1]
	v_mov_b32_dpp v253, v252 quad_perm:[1,0,3,2] row_mask:0xf bank_mask:0xf bound_ctrl:1
	v_pk_fma_f32 v[188:189], v[74:75], v[164:165], v[188:189] op_sel_hi:[1,0,1]
	v_pk_fma_f32 v[190:191], v[76:77], v[164:165], v[190:191] op_sel:[0,1,0] op_sel_hi:[1,1,1]
	v_pk_fma_f32 v[70:71], v[252:253], v[170:171], v[184:185] op_sel_hi:[1,0,1]
	v_pk_fma_f32 v[72:73], v[252:253], v[170:171], v[186:187] op_sel:[0,1,0] op_sel_hi:[1,1,1]
	v_pk_fma_f32 v[74:75], v[252:253], v[172:173], v[188:189] op_sel_hi:[1,0,1]
	v_pk_fma_f32 v[76:77], v[252:253], v[172:173], v[190:191] op_sel:[0,1,0] op_sel_hi:[1,1,1]
	v_pk_mul_f32 v[194:195], v[70:71], v[178:179] op_sel_hi:[1,0]
	v_pk_fma_f32 v[194:195], v[72:73], v[178:179], v[194:195] op_sel:[0,1,0] op_sel_hi:[1,1,1]
	v_pk_fma_f32 v[194:195], v[74:75], v[180:181], v[194:195] op_sel_hi:[1,0,1]
	v_pk_fma_f32 v[194:195], v[76:77], v[180:181], v[194:195] op_sel:[0,1,0] op_sel_hi:[1,1,1]

	s_waitcnt lgkmcnt(0)
	v_cndmask_b32_e64 v92, v92, v161, s[12:13]
	ds_read_b128 v[162:165], v79 offset:0x1f00
	ds_read_b128 v[166:169], v79 offset:0x3f00
	ds_read_b128 v[170:173], v79 offset:0x5f00
	ds_read_b128 v[174:177], v79 offset:0x7f00
	ds_read_b128 v[178:181], v79 offset:0x9f00
	ds_read_b32 v182, v80 offset:0xf80
	ds_read_b32 v183, v81 offset:0xf80
	v_pk_mul_f32 v[250:251], v[70:71], v[86:87] op_sel_hi:[1,0]
	v_pk_fma_f32 v[250:251], v[72:73], v[86:87], v[250:251] op_sel:[0,1,0] op_sel_hi:[1,1,1]
	v_pk_fma_f32 v[250:251], v[74:75], v[88:89], v[250:251] op_sel_hi:[1,0,1]
	v_pk_fma_f32 v[250:251], v[76:77], v[88:89], v[250:251] op_sel:[0,1,0] op_sel_hi:[1,1,1]
	v_pk_mul_f32 v[184:185], v[126:127], v[118:119] op_sel_hi:[1,0]
	v_pk_mul_f32 v[186:187], v[126:127], v[118:119] op_sel:[0,1] op_sel_hi:[1,1]
	v_add_f32_dpp v252, v251, v250 quad_perm:[1,0,3,2] row_mask:0xf bank_mask:0xf bound_ctrl:1
	v_add_f32_dpp v161, v195, v194 quad_perm:[1,0,3,2] row_mask:0xf bank_mask:0xf bound_ctrl:1
	v_pk_mul_f32 v[188:189], v[126:127], v[120:121] op_sel_hi:[1,0]
	v_add_f32_dpp v252, v252, v252 quad_perm:[2,3,0,1] row_mask:0xf bank_mask:0xf bound_ctrl:1
	v_add_f32_dpp v161, v161, v161 quad_perm:[2,3,0,1] row_mask:0xf bank_mask:0xf bound_ctrl:1
	v_pk_mul_f32 v[190:191], v[126:127], v[120:121] op_sel:[0,1] op_sel_hi:[1,1]
	v_add_f32_dpp v252, v252, v252 row_ror:4 row_mask:0xf bank_mask:0xf bound_ctrl:1
	v_add_f32_dpp v161, v161, v161 row_ror:4 row_mask:0xf bank_mask:0xf bound_ctrl:1
	v_pk_fma_f32 v[184:185], v[70:71], v[82:83], v[184:185] op_sel_hi:[1,0,1]
	v_add_f32_dpp v252, v252, v252 row_ror:8 row_mask:0xf bank_mask:0xf bound_ctrl:1
	v_add_f32_dpp v161, v161, v161 row_ror:8 row_mask:0xf bank_mask:0xf bound_ctrl:1
	v_pk_fma_f32 v[186:187], v[72:73], v[82:83], v[186:187] op_sel:[0,1,0] op_sel_hi:[1,1,1]
	v_mov_b32_dpp v253, v252 quad_perm:[1,0,3,2] row_mask:0xf bank_mask:0xf bound_ctrl:1
	v_pk_fma_f32 v[188:189], v[74:75], v[84:85], v[188:189] op_sel_hi:[1,0,1]
	v_pk_fma_f32 v[190:191], v[76:77], v[84:85], v[190:191] op_sel:[0,1,0] op_sel_hi:[1,1,1]
	v_pk_fma_f32 v[70:71], v[252:253], v[114:115], v[184:185] op_sel_hi:[1,0,1]
	v_pk_fma_f32 v[72:73], v[252:253], v[114:115], v[186:187] op_sel:[0,1,0] op_sel_hi:[1,1,1]
	v_pk_fma_f32 v[74:75], v[252:253], v[116:117], v[188:189] op_sel_hi:[1,0,1]
	v_pk_fma_f32 v[76:77], v[252:253], v[116:117], v[190:191] op_sel:[0,1,0] op_sel_hi:[1,1,1]
	v_pk_mul_f32 v[192:193], v[70:71], v[122:123] op_sel_hi:[1,0]
	v_pk_fma_f32 v[192:193], v[72:73], v[122:123], v[192:193] op_sel:[0,1,0] op_sel_hi:[1,1,1]
	v_pk_fma_f32 v[192:193], v[74:75], v[124:125], v[192:193] op_sel_hi:[1,0,1]
	v_pk_fma_f32 v[192:193], v[76:77], v[124:125], v[192:193] op_sel:[0,1,0] op_sel_hi:[1,1,1]

	s_waitcnt lgkmcnt(0)
	v_cndmask_b32_e64 v92, v92, v161, s[14:15]
	ds_read_b128 v[82:85], v79 offset:0x2000
	ds_read_b128 v[86:89], v79 offset:0x4000
	ds_read_b128 v[114:117], v79 offset:0x6000
	ds_read_b128 v[118:121], v79 offset:0x8000
	ds_read_b128 v[122:125], v79 offset:0xa000
	ds_read_b32 v79, v80 offset:0x1000
	ds_read_b32 v161, v81 offset:0x1000
	v_pk_mul_f32 v[250:251], v[70:71], v[166:167] op_sel_hi:[1,0]
	v_pk_fma_f32 v[250:251], v[72:73], v[166:167], v[250:251] op_sel:[0,1,0] op_sel_hi:[1,1,1]
	v_pk_fma_f32 v[250:251], v[74:75], v[168:169], v[250:251] op_sel_hi:[1,0,1]
	v_pk_fma_f32 v[250:251], v[76:77], v[168:169], v[250:251] op_sel:[0,1,0] op_sel_hi:[1,1,1]
	v_pk_mul_f32 v[80:81], v[182:183], v[174:175] op_sel_hi:[1,0]
	v_pk_mul_f32 v[126:127], v[182:183], v[174:175] op_sel:[0,1] op_sel_hi:[1,1]
	v_add_f32_dpp v252, v251, v250 quad_perm:[1,0,3,2] row_mask:0xf bank_mask:0xf bound_ctrl:1
	v_add_f32_dpp v190, v193, v192 quad_perm:[1,0,3,2] row_mask:0xf bank_mask:0xf bound_ctrl:1
	v_pk_mul_f32 v[184:185], v[182:183], v[176:177] op_sel_hi:[1,0]
	v_add_f32_dpp v252, v252, v252 quad_perm:[2,3,0,1] row_mask:0xf bank_mask:0xf bound_ctrl:1
	v_add_f32_dpp v190, v190, v190 quad_perm:[2,3,0,1] row_mask:0xf bank_mask:0xf bound_ctrl:1
	v_pk_mul_f32 v[186:187], v[182:183], v[176:177] op_sel:[0,1] op_sel_hi:[1,1]
	v_add_f32_dpp v252, v252, v252 row_ror:4 row_mask:0xf bank_mask:0xf bound_ctrl:1
	v_add_f32_dpp v190, v190, v190 row_ror:4 row_mask:0xf bank_mask:0xf bound_ctrl:1
	v_pk_fma_f32 v[80:81], v[70:71], v[162:163], v[80:81] op_sel_hi:[1,0,1]
	v_add_f32_dpp v252, v252, v252 row_ror:8 row_mask:0xf bank_mask:0xf bound_ctrl:1
	v_add_f32_dpp v190, v190, v190 row_ror:8 row_mask:0xf bank_mask:0xf bound_ctrl:1
	v_pk_fma_f32 v[126:127], v[72:73], v[162:163], v[126:127] op_sel:[0,1,0] op_sel_hi:[1,1,1]
	v_mov_b32_dpp v253, v252 quad_perm:[1,0,3,2] row_mask:0xf bank_mask:0xf bound_ctrl:1
	v_pk_fma_f32 v[184:185], v[74:75], v[164:165], v[184:185] op_sel_hi:[1,0,1]
	v_pk_fma_f32 v[186:187], v[76:77], v[164:165], v[186:187] op_sel:[0,1,0] op_sel_hi:[1,1,1]
	v_pk_fma_f32 v[70:71], v[252:253], v[170:171], v[80:81] op_sel_hi:[1,0,1]
	v_pk_fma_f32 v[72:73], v[252:253], v[170:171], v[126:127] op_sel:[0,1,0] op_sel_hi:[1,1,1]
	v_pk_fma_f32 v[74:75], v[252:253], v[172:173], v[184:185] op_sel_hi:[1,0,1]
	v_pk_fma_f32 v[76:77], v[252:253], v[172:173], v[186:187] op_sel:[0,1,0] op_sel_hi:[1,1,1]
	v_pk_mul_f32 v[188:189], v[70:71], v[178:179] op_sel_hi:[1,0]
	v_pk_fma_f32 v[188:189], v[72:73], v[178:179], v[188:189] op_sel:[0,1,0] op_sel_hi:[1,1,1]
	v_pk_fma_f32 v[188:189], v[74:75], v[180:181], v[188:189] op_sel_hi:[1,0,1]
	v_pk_fma_f32 v[188:189], v[76:77], v[180:181], v[188:189] op_sel:[0,1,0] op_sel_hi:[1,1,1]

; __device__ __forceinline__ float pair16_sum(f32x2 p) { float x = p.x + dpp_mov<0xB1>(p.y); x = dpp_add<0x4E>(x); x = dpp_add<0x124>(x); x = dpp_add<0x128>(x); return x; }
; __device__ __forceinline__ void p4_scan(Frame& F) {
;     ...
;                     { const float y7 = pair16_sum(qq); ykeep = ((kap >> 1) == 7) ? y7 : ykeep; }
;                     yb[(24 + (kap >> 1)) * 32 + rown] = ykeep;
;                 }
;     ...
;                 asm volatile("s_waitcnt lgkmcnt(0)" ::: "memory"); __builtin_amdgcn_s_barrier(); asm volatile("" ::: "memory");
	s_waitcnt lgkmcnt(0)
	v_cndmask_b32_e64 v80, v92, v190, s[16:17]
	s_nop 0
	v_add_f32_dpp v79, v189, v188 quad_perm:[1,0,3,2] row_mask:0xf bank_mask:0xf bound_ctrl:1
	s_nop 1
	v_add_f32_dpp v79, v79, v79 quad_perm:[2,3,0,1] row_mask:0xf bank_mask:0xf bound_ctrl:1
	s_nop 1
	v_add_f32_dpp v79, v79, v79 row_ror:4 row_mask:0xf bank_mask:0xf bound_ctrl:1
	s_nop 1
	v_add_f32_dpp v79, v79, v79 row_ror:8 row_mask:0xf bank_mask:0xf bound_ctrl:1
	v_cndmask_b32_e64 v79, v80, v79, s[18:19]
	ds_write_b32 v78, v79 offset:3072
	s_waitcnt lgkmcnt(0)
	s_barrier
	s_cbranch_scc1 .LBB0_489
	s_setprio 0
	s_mov_b64 s[2:3], 0

; #define LAS __attribute__((address_space(3)))
; __device__ __forceinline__ unsigned pk4_fp8(float a, float b, float c, float d) { int w = 0; w = __builtin_amdgcn_cvt_pk_fp8_f32(a, b, w, false); w = __builtin_amdgcn_cvt_pk_fp8_f32(c, d, w, true); return (unsigned)w; }
; __device__ __forceinline__ float swiglu1(float g, float l) {
;     g = fminf(g, 7.0f); l = fminf(fmaxf(l, -7.0f), 7.0f);
;     const float s = __builtin_amdgcn_rcpf(1.0f + __expf(-1.702f * g));
;     return g * s * (l + 1.0f);
; }
;     __device__ __forceinline__ void operator()(const f32x4 (&acc)[2][2][4][2], const Unit& u, int wr, int wc, int fr, int fq) const {
;         const int e = u.pn / npn, pnl = u.pn - e * npn; const int tid = threadIdx.x;
;         const int col0 = pnl * BM + wc * 32 + 8 * fq;
;         f32x4 bv[2][2];
; #pragma unroll
;         for (int bj = 0; bj < 2; ++bj)
; #pragma unroll
;             for (int n = 0; n < 2; ++n) bv[bj][n] = *(const f32x4*)(bias + (size_t)e * bias_ld + col0 + bj * HALF + 4 * n);
;         LAS unsigned char* wp = stg + (16 * wr + fr) * STG8_PITCH + 16 * wc + 4 * fq;
;         const int rr = (tid >> 3) & 31, cc = tid & 7, ms = tid >> 8;
;         const LAS unsigned char* rp = stg + rr * STG8_PITCH + cc * 16;
;         unsigned char* gp = O + (size_t)(u.pm * BM + 64 * (rr >> 4) + (rr & 15)) * ldc + pnl * (BM / 2) + cc * 16;
; #pragma unroll
;         for (int ai = 0; ai < 2; ++ai) {
; #pragma unroll
;             for (int m = 0; m < 4; ++m)
; #pragma unroll
;                 for (int bj = 0; bj < 2; ++bj) { const f32x4 v0 = acc[ai][bj][m][0] * scale + bv[bj][0], v1 = acc[ai][bj][m][1] * scale + bv[bj][1];
;                     *(LAS unsigned*)(wp + m * (32 * STG8_PITCH) + 64 * bj) = pk4_fp8(swiglu1(v0[0], v0[1]), swiglu1(v0[2], v0[3]), swiglu1(v1[0], v1[1]), swiglu1(v1[2], v1[3])); }
.LBB0_1010:
	s_ashr_i32 s2, s23, 31
	s_lshr_b32 s2, s2, 28
	s_add_i32 s3, s23, s2
	s_ashr_i32 s2, s3, 4
	s_and_b32 s3, s3, -16
	s_sub_i32 s23, s23, s3
	s_ashr_i32 s3, s2, 31
	s_lshl_b64 s[2:3], s[2:3], 14
	v_readlane_b32 s52, v254, 0
	v_lshl_or_b32 v2, s23, 8, v200
	v_readlane_b32 s53, v254, 1
	s_add_u32 s2, s52, s2
	s_addc_u32 s3, s53, s3
	v_ashrrev_i32_e32 v3, 31, v2
	s_nop 15
	s_nop 15
	v_lshl_add_u64 v[2:3], v[2:3], 2, s[2:3]
	global_load_dwordx4 v[14:17], v[2:3], off
	global_load_dwordx4 v[10:13], v[2:3], off offset:16
	global_load_dwordx4 v[6:9], v[2:3], off offset:512
	s_nop 0
	global_load_dwordx4 v[2:5], v[2:3], off offset:528
	v_mov_b32_e32 v176, 0
	v_lshl_or_b32 v18, s22, 8, v201
	v_ashrrev_i32_e32 v19, 31, v18
	v_lshlrev_b64 v[18:19], 11, v[18:19]
	s_lshl_b32 s22, s23, 7
	v_lshl_add_u64 v[18:19], s[8:9], 0, v[18:19]
	s_ashr_i32 s23, s22, 31
	v_lshl_add_u64 v[18:19], v[18:19], 0, s[22:23]
	v_lshl_add_u64 v[18:19], v[18:19], 0, v[170:171]
	s_cmp_eq_u32 s42, s46
	s_mov_b64 s[2:3], -1
	v_readlane_b32 s54, v254, 2
	v_readlane_b32 s55, v254, 3
	v_readlane_b32 s56, v254, 4
	v_readlane_b32 s57, v254, 5
	v_readlane_b32 s58, v254, 6
	v_readlane_b32 s59, v254, 7
	s_waitcnt vmcnt(0)
	v_pk_fma_f32 v[20:21], v[160:161], s[16:17], v[16:17] op_sel_hi:[1,0,1]
	v_pk_fma_f32 v[22:23], v[158:159], s[16:17], v[14:15] op_sel_hi:[1,0,1]
	v_min_f32_e32 v20, 0x40e00000, v20
	v_min_f32_e32 v22, 0x40e00000, v22
	v_pk_fma_f32 v[32:33], v[148:149], s[16:17], v[4:5] op_sel_hi:[1,0,1]
	v_mul_f32_e32 v148, 0xc01d265f, v22
	v_mul_f32_e32 v149, 0xc01d265f, v20
	v_pk_fma_f32 v[24:25], v[156:157], s[16:17], v[12:13] op_sel_hi:[1,0,1]
	v_pk_fma_f32 v[26:27], v[154:155], s[16:17], v[10:11] op_sel_hi:[1,0,1]
	v_exp_f32_e32 v148, v148
	v_exp_f32_e32 v149, v149
	v_min_f32_e32 v26, 0x40e00000, v26
	v_min_f32_e32 v24, 0x40e00000, v24
	v_pk_fma_f32 v[28:29], v[152:153], s[16:17], v[8:9] op_sel_hi:[1,0,1]
	v_pk_fma_f32 v[30:31], v[150:151], s[16:17], v[6:7] op_sel_hi:[1,0,1]
	v_mul_f32_e32 v150, 0xc01d265f, v26
	v_mul_f32_e32 v151, 0xc01d265f, v24
	v_min_f32_e32 v30, 0x40e00000, v30
	v_min_f32_e32 v28, 0x40e00000, v28
	v_mul_f32_e32 v152, 0xc01d265f, v30
	v_mul_f32_e32 v153, 0xc01d265f, v28
	v_exp_f32_e32 v150, v150
	v_exp_f32_e32 v151, v151
	v_add_f32_e32 v148, 1.0, v148
	v_add_f32_e32 v149, 1.0, v149
	v_rcp_f32_e32 v148, v148
	v_rcp_f32_e32 v149, v149
	v_pk_fma_f32 v[146:147], v[146:147], s[16:17], v[2:3] op_sel_hi:[1,0,1]
	v_exp_f32_e32 v152, v152
	v_exp_f32_e32 v153, v153
	v_min_f32_e32 v146, 0x40e00000, v146
	v_min_f32_e32 v32, 0x40e00000, v32
	v_med3_f32 v23, v23, s47, v204
	v_med3_f32 v21, v21, s47, v204
	v_mul_f32_e32 v154, 0xc01d265f, v146
	v_mul_f32_e32 v155, 0xc01d265f, v32
	v_add_f32_e32 v150, 1.0, v150
	v_add_f32_e32 v151, 1.0, v151
	v_add_f32_e32 v23, 1.0, v23
	v_add_f32_e32 v21, 1.0, v21
	v_rcp_f32_e32 v150, v150
	v_rcp_f32_e32 v151, v151
	v_mul_f32_e32 v22, v22, v148
	v_mul_f32_e32 v20, v20, v149
	v_exp_f32_e32 v154, v154
	v_exp_f32_e32 v155, v155
	v_add_f32_e32 v152, 1.0, v152
	v_add_f32_e32 v153, 1.0, v153
	v_mul_f32_e32 v22, v23, v22
	v_mul_f32_e32 v20, v21, v20
	v_rcp_f32_e32 v152, v152
	v_rcp_f32_e32 v153, v153
	v_cvt_pk_fp8_f32 v176, v22, v20
	v_med3_f32 v27, v27, s47, v204
	v_med3_f32 v25, v25, s47, v204
	v_add_f32_e32 v27, 1.0, v27
	v_add_f32_e32 v25, 1.0, v25
	v_mul_f32_e32 v26, v26, v150
	v_mul_f32_e32 v24, v24, v151
	v_med3_f32 v31, v31, s47, v204
	v_med3_f32 v29, v29, s47, v204
	v_add_f32_e32 v154, 1.0, v154
	v_add_f32_e32 v155, 1.0, v155
	v_mul_f32_e32 v21, v27, v26
	v_mul_f32_e32 v23, v25, v24
	v_add_f32_e32 v31, 1.0, v31
	v_add_f32_e32 v29, 1.0, v29
	v_rcp_f32_e32 v154, v154
	v_mul_f32_e32 v30, v30, v152
	v_mul_f32_e32 v28, v28, v153
	v_cvt_pk_fp8_f32 v176, v21, v23 op_sel:[0,0,1]
	v_rcp_f32_e32 v21, v155
	v_mul_f32_e32 v20, v31, v30
	v_mul_f32_e32 v22, v29, v28
	v_mov_b32_e32 v28, 0
	v_cvt_pk_fp8_f32 v28, v20, v22
	v_med3_f32 v147, v147, s47, v204
	v_med3_f32 v23, v33, s47, v204
	v_add_f32_e32 v147, 1.0, v147
	v_mul_f32_e32 v146, v146, v154
	v_mul_f32_e32 v20, v32, v21
	v_add_f32_e32 v21, 1.0, v23
	v_pk_fma_f32 v[22:23], v[142:143], s[16:17], v[14:15] op_sel_hi:[1,0,1]
	v_mul_f32_e32 v24, v147, v146
	v_mul_f32_e32 v20, v21, v20
	v_min_f32_e32 v22, 0x40e00000, v22
	v_cvt_pk_fp8_f32 v28, v24, v20 op_sel:[0,0,1]
	v_mul_f32_e32 v24, 0xc01d265f, v22
	v_exp_f32_e32 v29, v24
	v_pk_fma_f32 v[20:21], v[144:145], s[16:17], v[16:17] op_sel_hi:[1,0,1]
	v_pk_fma_f32 v[26:27], v[138:139], s[16:17], v[10:11] op_sel_hi:[1,0,1]
	v_min_f32_e32 v20, 0x40e00000, v20
	v_add_f32_e32 v29, 1.0, v29
	v_mul_f32_e32 v30, 0xc01d265f, v20
	v_rcp_f32_e32 v29, v29
	v_exp_f32_e32 v30, v30
	v_med3_f32 v23, v23, s47, v204
	v_min_f32_e32 v26, 0x40e00000, v26
	v_mul_f32_e32 v22, v22, v29
	v_add_f32_e32 v23, 1.0, v23
	v_mul_f32_e32 v29, 0xc01d265f, v26
	v_mul_f32_e32 v22, v23, v22
	v_add_f32_e32 v23, 1.0, v30
	v_rcp_f32_e32 v23, v23
	v_exp_f32_e32 v29, v29
	v_pk_fma_f32 v[24:25], v[140:141], s[16:17], v[12:13] op_sel_hi:[1,0,1]
	v_med3_f32 v21, v21, s47, v204
	v_min_f32_e32 v24, 0x40e00000, v24
	v_mul_f32_e32 v20, v20, v23
	v_add_f32_e32 v23, 1.0, v29
	v_mul_f32_e32 v29, 0xc01d265f, v24
	v_rcp_f32_e32 v23, v23
	v_exp_f32_e32 v29, v29
	v_add_f32_e32 v21, 1.0, v21
	v_mul_f32_e32 v20, v21, v20
	v_mul_f32_e32 v23, v26, v23
	v_add_f32_e32 v26, 1.0, v29
	v_rcp_f32_e32 v26, v26
	v_med3_f32 v21, v27, s47, v204
	v_add_f32_e32 v21, 1.0, v21
	v_mul_f32_e32 v23, v21, v23
	v_med3_f32 v21, v25, s47, v204
	v_mul_f32_e32 v24, v24, v26
	v_add_f32_e32 v21, 1.0, v21
	v_mov_b32_e32 v29, 0
	v_mul_f32_e32 v24, v21, v24
	v_cvt_pk_fp8_f32 v29, v22, v20
	v_pk_fma_f32 v[20:21], v[134:135], s[16:17], v[6:7] op_sel_hi:[1,0,1]
; #define LAS __attribute__((address_space(3)))
; __device__ __forceinline__ unsigned pk4_fp8(float a, float b, float c, float d) { int w = 0; w = __builtin_amdgcn_cvt_pk_fp8_f32(a, b, w, false); w = __builtin_amdgcn_cvt_pk_fp8_f32(c, d, w, true); return (unsigned)w; }
; __device__ __forceinline__ float swiglu1(float g, float l) {
;     g = fminf(g, 7.0f); l = fminf(fmaxf(l, -7.0f), 7.0f);
;     const float s = __builtin_amdgcn_rcpf(1.0f + __expf(-1.702f * g));
;     return g * s * (l + 1.0f);
; }
;     __device__ __forceinline__ void operator()(const f32x4 (&acc)[2][2][4][2], const Unit& u, int wr, int wc, int fr, int fq) const {
;     ...
;             for (int m = 0; m < 4; ++m)
; #pragma unroll
;                 for (int bj = 0; bj < 2; ++bj) { const f32x4 v0 = acc[ai][bj][m][0] * scale + bv[bj][0], v1 = acc[ai][bj][m][1] * scale + bv[bj][1];
;                     *(LAS unsigned*)(wp + m * (32 * STG8_PITCH) + 64 * bj) = pk4_fp8(swiglu1(v0[0], v0[1]), swiglu1(v0[2], v0[3]), swiglu1(v1[0], v1[1]), swiglu1(v1[2], v1[3])); }
	ds_write2_b32 v202, v176, v28 offset1:16
	v_min_f32_e32 v20, 0x40e00000, v20
	v_mul_f32_e32 v22, 0xc01d265f, v20
	v_exp_f32_e32 v26, v22
	v_cvt_pk_fp8_f32 v29, v23, v24 op_sel:[0,0,1]
	v_pk_fma_f32 v[22:23], v[136:137], s[16:17], v[8:9] op_sel_hi:[1,0,1]
	v_med3_f32 v21, v21, s47, v204
	v_add_f32_e32 v26, 1.0, v26
	v_min_f32_e32 v22, 0x40e00000, v22
	v_rcp_f32_e32 v30, v26
	v_mul_f32_e32 v26, 0xc01d265f, v22
	v_exp_f32_e32 v31, v26
	v_pk_fma_f32 v[26:27], v[130:131], s[16:17], v[2:3] op_sel_hi:[1,0,1]
	v_mul_f32_e32 v20, v20, v30
	v_add_f32_e32 v21, 1.0, v21
	v_mul_f32_e32 v20, v21, v20
	v_med3_f32 v21, v23, s47, v204
	v_min_f32_e32 v23, 0x40e00000, v26
	v_add_f32_e32 v30, 1.0, v31
	v_mul_f32_e32 v26, 0xc01d265f, v23
	v_rcp_f32_e32 v30, v30
	v_exp_f32_e32 v26, v26
	v_pk_fma_f32 v[24:25], v[132:133], s[16:17], v[4:5] op_sel_hi:[1,0,1]
	v_mul_f32_e32 v22, v22, v30
	v_add_f32_e32 v21, 1.0, v21
	v_min_f32_e32 v24, 0x40e00000, v24
	v_mul_f32_e32 v21, v21, v22
	v_med3_f32 v22, v27, s47, v204
	v_add_f32_e32 v26, 1.0, v26
	v_mul_f32_e32 v27, 0xc01d265f, v24
	v_rcp_f32_e32 v26, v26
	v_exp_f32_e32 v27, v27
	v_add_f32_e32 v22, 1.0, v22
	v_mul_f32_e32 v23, v23, v26
	v_mul_f32_e32 v22, v22, v23
	v_add_f32_e32 v23, 1.0, v27
	v_rcp_f32_e32 v23, v23
	v_med3_f32 v25, v25, s47, v204
	v_mov_b32_e32 v26, 0
	v_cvt_pk_fp8_f32 v26, v20, v21
	v_mul_f32_e32 v20, v24, v23
	v_add_f32_e32 v21, 1.0, v25
	v_pk_fma_f32 v[24:25], v[126:127], s[16:17], v[14:15] op_sel_hi:[1,0,1]
	v_mul_f32_e32 v20, v21, v20
	v_min_f32_e32 v23, 0x40e00000, v24
	v_mul_f32_e32 v24, 0xc01d265f, v23
	v_exp_f32_e32 v24, v24
	v_cvt_pk_fp8_f32 v26, v22, v20 op_sel:[0,0,1]
	v_pk_fma_f32 v[20:21], v[128:129], s[16:17], v[16:17] op_sel_hi:[1,0,1]
	v_add_u32_e32 v22, 0x1000, v202
	v_add_f32_e32 v24, 1.0, v24
	v_min_f32_e32 v20, 0x40e00000, v20
	v_rcp_f32_e32 v24, v24
	v_mul_f32_e32 v30, 0xc01d265f, v20
	v_exp_f32_e32 v30, v30
	ds_write2_b32 v22, v29, v26 offset0:128 offset1:144
	v_pk_fma_f32 v[28:29], v[122:123], s[16:17], v[10:11] op_sel_hi:[1,0,1]
	v_med3_f32 v25, v25, s47, v204
	v_mul_f32_e32 v23, v23, v24
	v_add_f32_e32 v24, 1.0, v25
	v_min_f32_e32 v25, 0x40e00000, v28
	v_mul_f32_e32 v28, 0xc01d265f, v25
	v_mul_f32_e32 v23, v24, v23
	v_add_f32_e32 v24, 1.0, v30
	v_rcp_f32_e32 v24, v24
	v_exp_f32_e32 v28, v28
	v_pk_fma_f32 v[26:27], v[124:125], s[16:17], v[12:13] op_sel_hi:[1,0,1]
	v_med3_f32 v21, v21, s47, v204
	v_min_f32_e32 v26, 0x40e00000, v26
	v_mul_f32_e32 v20, v20, v24
	v_add_f32_e32 v24, 1.0, v28
	v_mul_f32_e32 v28, 0xc01d265f, v26
	v_rcp_f32_e32 v24, v24
	v_exp_f32_e32 v28, v28
	v_add_f32_e32 v21, 1.0, v21
	v_mul_f32_e32 v20, v21, v20
	v_mul_f32_e32 v24, v25, v24
	v_add_f32_e32 v25, 1.0, v28
	v_rcp_f32_e32 v25, v25
	v_med3_f32 v21, v29, s47, v204
	v_add_f32_e32 v21, 1.0, v21
	v_mul_f32_e32 v24, v21, v24
	v_med3_f32 v21, v27, s47, v204
	v_mul_f32_e32 v25, v26, v25
	v_add_f32_e32 v21, 1.0, v21
	v_mov_b32_e32 v30, 0
	v_mul_f32_e32 v25, v21, v25
	v_cvt_pk_fp8_f32 v30, v23, v20
	v_pk_fma_f32 v[20:21], v[118:119], s[16:17], v[6:7] op_sel_hi:[1,0,1]
	v_pk_fma_f32 v[26:27], v[116:117], s[16:17], v[4:5] op_sel_hi:[1,0,1]
	v_min_f32_e32 v20, 0x40e00000, v20
	v_mul_f32_e32 v23, 0xc01d265f, v20
	v_exp_f32_e32 v23, v23
	v_cvt_pk_fp8_f32 v30, v24, v25 op_sel:[0,0,1]
	v_pk_fma_f32 v[24:25], v[120:121], s[16:17], v[8:9] op_sel_hi:[1,0,1]
	v_med3_f32 v21, v21, s47, v204
	v_min_f32_e32 v24, 0x40e00000, v24
	v_mul_f32_e32 v28, 0xc01d265f, v24
	v_add_f32_e32 v23, 1.0, v23
	v_rcp_f32_e32 v23, v23
	v_exp_f32_e32 v31, v28
	v_pk_fma_f32 v[28:29], v[114:115], s[16:17], v[2:3] op_sel_hi:[1,0,1]
	v_add_f32_e32 v21, 1.0, v21
	v_mul_f32_e32 v20, v20, v23
	v_add_f32_e32 v23, 1.0, v31
	v_rcp_f32_e32 v23, v23
	v_mul_f32_e32 v20, v21, v20
	v_med3_f32 v21, v25, s47, v204
	v_min_f32_e32 v26, 0x40e00000, v26
	v_mul_f32_e32 v23, v24, v23
	v_min_f32_e32 v24, 0x40e00000, v28
	v_mul_f32_e32 v25, 0xc01d265f, v24
	v_exp_f32_e32 v25, v25
	v_mul_f32_e32 v28, 0xc01d265f, v26
	v_exp_f32_e32 v28, v28
	v_add_f32_e32 v25, 1.0, v25
	v_rcp_f32_e32 v25, v25
	v_add_f32_e32 v21, 1.0, v21
	v_mul_f32_e32 v21, v21, v23
	v_med3_f32 v23, v29, s47, v204
	v_mul_f32_e32 v24, v24, v25
	v_add_f32_e32 v23, 1.0, v23
	v_mul_f32_e32 v23, v23, v24
	v_add_f32_e32 v24, 1.0, v28
	v_rcp_f32_e32 v24, v24
	v_mov_b32_e32 v31, 0
	v_cvt_pk_fp8_f32 v31, v20, v21
	v_med3_f32 v25, v27, s47, v204
	v_mul_f32_e32 v20, v26, v24
	v_add_f32_e32 v21, 1.0, v25
	v_mul_f32_e32 v20, v21, v20
	v_pk_fma_f32 v[24:25], v[110:111], s[16:17], v[14:15] op_sel_hi:[1,0,1]
	v_cvt_pk_fp8_f32 v31, v23, v20 op_sel:[0,0,1]
	v_min_f32_e32 v23, 0x40e00000, v24
	v_mul_f32_e32 v24, 0xc01d265f, v23
	v_exp_f32_e32 v24, v24
	v_pk_fma_f32 v[20:21], v[112:113], s[16:17], v[16:17] op_sel_hi:[1,0,1]
	v_pk_fma_f32 v[28:29], v[106:107], s[16:17], v[10:11] op_sel_hi:[1,0,1]
	v_min_f32_e32 v20, 0x40e00000, v20
	v_add_f32_e32 v24, 1.0, v24
	v_rcp_f32_e32 v24, v24
	v_mul_f32_e32 v32, 0xc01d265f, v20
	v_exp_f32_e32 v32, v32
	v_med3_f32 v25, v25, s47, v204
	v_mul_f32_e32 v23, v23, v24
	v_add_f32_e32 v24, 1.0, v25
	v_min_f32_e32 v25, 0x40e00000, v28
	v_mul_f32_e32 v28, 0xc01d265f, v25
	v_mul_f32_e32 v23, v24, v23
	v_add_f32_e32 v24, 1.0, v32
	v_rcp_f32_e32 v24, v24
	v_exp_f32_e32 v28, v28
	v_pk_fma_f32 v[26:27], v[108:109], s[16:17], v[12:13] op_sel_hi:[1,0,1]
	v_med3_f32 v21, v21, s47, v204
	v_min_f32_e32 v26, 0x40e00000, v26
	v_mul_f32_e32 v20, v20, v24
	v_add_f32_e32 v24, 1.0, v28
	v_mul_f32_e32 v28, 0xc01d265f, v26
	v_rcp_f32_e32 v24, v24
	v_exp_f32_e32 v28, v28
	v_add_f32_e32 v21, 1.0, v21
	v_mul_f32_e32 v20, v21, v20
	v_mul_f32_e32 v24, v25, v24
	v_add_f32_e32 v25, 1.0, v28
	v_rcp_f32_e32 v25, v25
; #define LAS __attribute__((address_space(3)))
; __device__ __forceinline__ unsigned pk4_fp8(float a, float b, float c, float d) { int w = 0; w = __builtin_amdgcn_cvt_pk_fp8_f32(a, b, w, false); w = __builtin_amdgcn_cvt_pk_fp8_f32(c, d, w, true); return (unsigned)w; }
; __device__ __forceinline__ float swiglu1(float g, float l) {
;     g = fminf(g, 7.0f); l = fminf(fmaxf(l, -7.0f), 7.0f);
;     const float s = __builtin_amdgcn_rcpf(1.0f + __expf(-1.702f * g));
;     return g * s * (l + 1.0f);
; }
;     __device__ __forceinline__ void operator()(const f32x4 (&acc)[2][2][4][2], const Unit& u, int wr, int wc, int fr, int fq) const {
;     ...
;             for (int m = 0; m < 4; ++m)
; #pragma unroll
;                 for (int bj = 0; bj < 2; ++bj) { const f32x4 v0 = acc[ai][bj][m][0] * scale + bv[bj][0], v1 = acc[ai][bj][m][1] * scale + bv[bj][1];
;                     *(LAS unsigned*)(wp + m * (32 * STG8_PITCH) + 64 * bj) = pk4_fp8(swiglu1(v0[0], v0[1]), swiglu1(v0[2], v0[3]), swiglu1(v1[0], v1[1]), swiglu1(v1[2], v1[3])); }
;             asm volatile("s_waitcnt lgkmcnt(0)" ::: "memory"); __builtin_amdgcn_s_barrier(); asm volatile("" ::: "memory");
; #pragma unroll
;             for (int k2 = 0; k2 < 2; ++k2) { const int m = ms + 2 * k2;
;                 *(u32x4*)(gp + (size_t)(ai * HALF + m * 16) * ldc) = *(const LAS u32x4*)(rp + m * (32 * STG8_PITCH)); }
	v_med3_f32 v21, v29, s47, v204
	v_add_f32_e32 v21, 1.0, v21
	v_mul_f32_e32 v24, v21, v24
	v_med3_f32 v21, v27, s47, v204
	v_mul_f32_e32 v25, v26, v25
	v_add_f32_e32 v21, 1.0, v21
	v_mov_b32_e32 v32, 0
	v_mul_f32_e32 v25, v21, v25
	v_cvt_pk_fp8_f32 v32, v23, v20
	v_pk_fma_f32 v[20:21], v[102:103], s[16:17], v[6:7] op_sel_hi:[1,0,1]
	v_pk_fma_f32 v[26:27], v[100:101], s[16:17], v[4:5] op_sel_hi:[1,0,1]
	v_min_f32_e32 v20, 0x40e00000, v20
	v_mul_f32_e32 v23, 0xc01d265f, v20
	v_exp_f32_e32 v23, v23
	v_cvt_pk_fp8_f32 v32, v24, v25 op_sel:[0,0,1]
	v_pk_fma_f32 v[24:25], v[104:105], s[16:17], v[8:9] op_sel_hi:[1,0,1]
	v_med3_f32 v21, v21, s47, v204
	v_min_f32_e32 v24, 0x40e00000, v24
	v_mul_f32_e32 v28, 0xc01d265f, v24
	v_add_f32_e32 v23, 1.0, v23
	v_rcp_f32_e32 v23, v23
	v_exp_f32_e32 v33, v28
	v_pk_fma_f32 v[28:29], v[98:99], s[16:17], v[2:3] op_sel_hi:[1,0,1]
	v_add_f32_e32 v21, 1.0, v21
	v_mul_f32_e32 v20, v20, v23
	v_add_f32_e32 v23, 1.0, v33
	v_rcp_f32_e32 v23, v23
	v_mul_f32_e32 v20, v21, v20
	v_med3_f32 v21, v25, s47, v204
	v_min_f32_e32 v26, 0x40e00000, v26
	v_mul_f32_e32 v23, v24, v23
	v_min_f32_e32 v24, 0x40e00000, v28
	v_mul_f32_e32 v25, 0xc01d265f, v24
	v_exp_f32_e32 v25, v25
	v_mul_f32_e32 v28, 0xc01d265f, v26
	v_exp_f32_e32 v28, v28
	v_add_f32_e32 v25, 1.0, v25
	v_rcp_f32_e32 v25, v25
	v_add_f32_e32 v21, 1.0, v21
	v_mul_f32_e32 v21, v21, v23
	v_med3_f32 v23, v29, s47, v204
	v_mul_f32_e32 v24, v24, v25
	v_add_f32_e32 v23, 1.0, v23
	v_mul_f32_e32 v23, v23, v24
	v_add_f32_e32 v24, 1.0, v28
	v_rcp_f32_e32 v24, v24
	v_med3_f32 v25, v27, s47, v204
	v_mov_b32_e32 v27, 0
	v_cvt_pk_fp8_f32 v27, v20, v21
	v_mul_f32_e32 v20, v26, v24
	v_add_f32_e32 v21, 1.0, v25
	v_mul_f32_e32 v20, v21, v20
	v_cvt_pk_fp8_f32 v27, v23, v20 op_sel:[0,0,1]
	v_add_u32_e32 v23, 0x2400, v202
	v_add_u32_e32 v24, 0x3400, v202
	ds_write2_b32 v23, v30, v31 offset1:16
	ds_write2_b32 v24, v32, v27 offset0:128 offset1:144
	s_waitcnt lgkmcnt(0)
	s_barrier
	ds_read_b128 v[26:29], v203
	ds_read_b128 v[30:33], v203 offset:9216
	v_lshl_add_u64 v[20:21], v[18:19], 0, v[172:173]
	v_lshl_add_u64 v[18:19], v[18:19], 0, v[174:175]
	s_waitcnt lgkmcnt(1)
	global_store_dwordx4 v[20:21], v[26:29], off
	s_waitcnt lgkmcnt(0)
	global_store_dwordx4 v[18:19], v[30:33], off
	v_pk_fma_f32 v[28:29], v[94:95], s[16:17], v[14:15] op_sel_hi:[1,0,1]
	v_pk_fma_f32 v[26:27], v[96:97], s[16:17], v[16:17] op_sel_hi:[1,0,1]
	v_min_f32_e32 v25, 0x40e00000, v28
	v_mul_f32_e32 v28, 0xc01d265f, v25
	v_exp_f32_e32 v28, v28
	v_min_f32_e32 v26, 0x40e00000, v26
	v_pk_fma_f32 v[32:33], v[90:91], s[16:17], v[10:11] op_sel_hi:[1,0,1]
	v_mul_f32_e32 v90, 0xc01d265f, v26
	v_add_f32_e32 v28, 1.0, v28
	v_rcp_f32_e32 v28, v28
	v_exp_f32_e32 v90, v90
	v_med3_f32 v29, v29, s47, v204
	v_mul_f32_e32 v25, v25, v28
	v_add_f32_e32 v28, 1.0, v29
	v_min_f32_e32 v29, 0x40e00000, v32
	v_mul_f32_e32 v32, 0xc01d265f, v29
	v_mul_f32_e32 v25, v28, v25
	v_add_f32_e32 v28, 1.0, v90
	v_rcp_f32_e32 v28, v28
	v_exp_f32_e32 v32, v32
	v_pk_fma_f32 v[30:31], v[92:93], s[16:17], v[12:13] op_sel_hi:[1,0,1]
	v_med3_f32 v27, v27, s47, v204
	v_min_f32_e32 v30, 0x40e00000, v30
	v_mul_f32_e32 v26, v26, v28
	v_add_f32_e32 v28, 1.0, v32
	v_mul_f32_e32 v32, 0xc01d265f, v30
	v_rcp_f32_e32 v28, v28
	v_exp_f32_e32 v32, v32
	v_add_f32_e32 v27, 1.0, v27
	v_mul_f32_e32 v26, v27, v26
	v_mul_f32_e32 v28, v29, v28
	v_add_f32_e32 v29, 1.0, v32
	v_rcp_f32_e32 v29, v29
	v_med3_f32 v27, v33, s47, v204
	v_add_f32_e32 v27, 1.0, v27
	v_mul_f32_e32 v28, v27, v28
	v_med3_f32 v27, v31, s47, v204
	v_mul_f32_e32 v29, v30, v29
	v_add_f32_e32 v27, 1.0, v27
	v_mov_b32_e32 v90, 0
	v_mul_f32_e32 v29, v27, v29
	v_cvt_pk_fp8_f32 v90, v25, v26
	v_pk_fma_f32 v[26:27], v[86:87], s[16:17], v[6:7] op_sel_hi:[1,0,1]
	v_pk_fma_f32 v[30:31], v[84:85], s[16:17], v[4:5] op_sel_hi:[1,0,1]
	v_min_f32_e32 v25, 0x40e00000, v26
	v_mul_f32_e32 v26, 0xc01d265f, v25
	v_exp_f32_e32 v26, v26
	v_cvt_pk_fp8_f32 v90, v28, v29 op_sel:[0,0,1]
	v_pk_fma_f32 v[28:29], v[88:89], s[16:17], v[8:9] op_sel_hi:[1,0,1]
	v_med3_f32 v27, v27, s47, v204
	v_min_f32_e32 v28, 0x40e00000, v28
	v_mul_f32_e32 v32, 0xc01d265f, v28
	v_add_f32_e32 v26, 1.0, v26
	v_rcp_f32_e32 v26, v26
	v_exp_f32_e32 v84, v32
	v_pk_fma_f32 v[32:33], v[82:83], s[16:17], v[2:3] op_sel_hi:[1,0,1]
	v_add_f32_e32 v27, 1.0, v27
	v_mul_f32_e32 v25, v25, v26
	v_add_f32_e32 v26, 1.0, v84
	v_rcp_f32_e32 v26, v26
	v_mul_f32_e32 v25, v27, v25
	v_med3_f32 v27, v29, s47, v204
	v_min_f32_e32 v30, 0x40e00000, v30
	v_mul_f32_e32 v26, v28, v26
	v_min_f32_e32 v28, 0x40e00000, v32
	v_mul_f32_e32 v29, 0xc01d265f, v28
	v_exp_f32_e32 v29, v29
	v_mul_f32_e32 v32, 0xc01d265f, v30
	v_exp_f32_e32 v32, v32
	v_add_f32_e32 v29, 1.0, v29
	v_rcp_f32_e32 v29, v29
	v_add_f32_e32 v27, 1.0, v27
	v_mul_f32_e32 v26, v27, v26
	v_med3_f32 v27, v33, s47, v204
	v_mul_f32_e32 v28, v28, v29
	v_add_f32_e32 v27, 1.0, v27
	v_mul_f32_e32 v27, v27, v28
	v_add_f32_e32 v28, 1.0, v32
	v_rcp_f32_e32 v28, v28
	v_mov_b32_e32 v82, 0
	v_cvt_pk_fp8_f32 v82, v25, v26
	v_med3_f32 v29, v31, s47, v204
	v_mul_f32_e32 v25, v30, v28
	v_add_f32_e32 v26, 1.0, v29
	v_mul_f32_e32 v25, v26, v25
	v_pk_fma_f32 v[28:29], v[78:79], s[16:17], v[14:15] op_sel_hi:[1,0,1]
	v_cvt_pk_fp8_f32 v82, v27, v25 op_sel:[0,0,1]
	v_min_f32_e32 v25, 0x40e00000, v28
	v_mul_f32_e32 v28, 0xc01d265f, v25
	v_exp_f32_e32 v28, v28
	v_pk_fma_f32 v[26:27], v[80:81], s[16:17], v[16:17] op_sel_hi:[1,0,1]
	v_pk_fma_f32 v[32:33], v[74:75], s[16:17], v[10:11] op_sel_hi:[1,0,1]
	v_min_f32_e32 v26, 0x40e00000, v26
	v_add_f32_e32 v28, 1.0, v28
	v_rcp_f32_e32 v28, v28
	v_mul_f32_e32 v74, 0xc01d265f, v26
	v_exp_f32_e32 v74, v74
; #define LAS __attribute__((address_space(3)))
; __device__ __forceinline__ unsigned pk4_fp8(float a, float b, float c, float d) { int w = 0; w = __builtin_amdgcn_cvt_pk_fp8_f32(a, b, w, false); w = __builtin_amdgcn_cvt_pk_fp8_f32(c, d, w, true); return (unsigned)w; }
; __device__ __forceinline__ float swiglu1(float g, float l) {
;     g = fminf(g, 7.0f); l = fminf(fmaxf(l, -7.0f), 7.0f);
;     const float s = __builtin_amdgcn_rcpf(1.0f + __expf(-1.702f * g));
;     return g * s * (l + 1.0f);
; }
;     __device__ __forceinline__ void operator()(const f32x4 (&acc)[2][2][4][2], const Unit& u, int wr, int wc, int fr, int fq) const {
;     ...
;             for (int m = 0; m < 4; ++m)
; #pragma unroll
;                 for (int bj = 0; bj < 2; ++bj) { const f32x4 v0 = acc[ai][bj][m][0] * scale + bv[bj][0], v1 = acc[ai][bj][m][1] * scale + bv[bj][1];
;                     *(LAS unsigned*)(wp + m * (32 * STG8_PITCH) + 64 * bj) = pk4_fp8(swiglu1(v0[0], v0[1]), swiglu1(v0[2], v0[3]), swiglu1(v1[0], v1[1]), swiglu1(v1[2], v1[3])); }
	v_med3_f32 v29, v29, s47, v204
	v_mul_f32_e32 v25, v25, v28
	v_add_f32_e32 v28, 1.0, v29
	v_min_f32_e32 v29, 0x40e00000, v32
	v_mul_f32_e32 v32, 0xc01d265f, v29
	v_mul_f32_e32 v25, v28, v25
	v_add_f32_e32 v28, 1.0, v74
	v_rcp_f32_e32 v28, v28
	v_exp_f32_e32 v32, v32
	v_pk_fma_f32 v[30:31], v[76:77], s[16:17], v[12:13] op_sel_hi:[1,0,1]
	v_med3_f32 v27, v27, s47, v204
	v_min_f32_e32 v30, 0x40e00000, v30
	v_mul_f32_e32 v26, v26, v28
	v_add_f32_e32 v28, 1.0, v32
	v_mul_f32_e32 v32, 0xc01d265f, v30
	v_rcp_f32_e32 v28, v28
	v_exp_f32_e32 v32, v32
	v_add_f32_e32 v27, 1.0, v27
	v_mul_f32_e32 v26, v27, v26
	v_mul_f32_e32 v28, v29, v28
	v_add_f32_e32 v29, 1.0, v32
	v_rcp_f32_e32 v29, v29
	v_med3_f32 v27, v33, s47, v204
	v_add_f32_e32 v27, 1.0, v27
	v_mul_f32_e32 v28, v27, v28
	v_med3_f32 v27, v31, s47, v204
	v_mul_f32_e32 v29, v30, v29
	v_add_f32_e32 v27, 1.0, v27
	v_mov_b32_e32 v74, 0
	v_mul_f32_e32 v29, v27, v29
	v_cvt_pk_fp8_f32 v74, v25, v26
	v_pk_fma_f32 v[26:27], v[70:71], s[16:17], v[6:7] op_sel_hi:[1,0,1]
	v_pk_fma_f32 v[30:31], v[68:69], s[16:17], v[4:5] op_sel_hi:[1,0,1]
	v_min_f32_e32 v25, 0x40e00000, v26
	v_mul_f32_e32 v26, 0xc01d265f, v25
	v_exp_f32_e32 v26, v26
	v_cvt_pk_fp8_f32 v74, v28, v29 op_sel:[0,0,1]
	v_pk_fma_f32 v[28:29], v[72:73], s[16:17], v[8:9] op_sel_hi:[1,0,1]
	v_med3_f32 v27, v27, s47, v204
	v_min_f32_e32 v28, 0x40e00000, v28
	v_mul_f32_e32 v32, 0xc01d265f, v28
	v_add_f32_e32 v26, 1.0, v26
	v_rcp_f32_e32 v26, v26
	v_exp_f32_e32 v68, v32
	v_pk_fma_f32 v[32:33], v[66:67], s[16:17], v[2:3] op_sel_hi:[1,0,1]
	v_add_f32_e32 v27, 1.0, v27
	v_mul_f32_e32 v25, v25, v26
	v_add_f32_e32 v26, 1.0, v68
	v_rcp_f32_e32 v26, v26
	v_mul_f32_e32 v25, v27, v25
	v_med3_f32 v27, v29, s47, v204
	v_min_f32_e32 v30, 0x40e00000, v30
	v_mul_f32_e32 v26, v28, v26
	v_min_f32_e32 v28, 0x40e00000, v32
	v_mul_f32_e32 v29, 0xc01d265f, v28
	v_exp_f32_e32 v29, v29
	v_mul_f32_e32 v32, 0xc01d265f, v30
	v_exp_f32_e32 v32, v32
	v_add_f32_e32 v29, 1.0, v29
	v_rcp_f32_e32 v29, v29
	v_add_f32_e32 v27, 1.0, v27
	v_mul_f32_e32 v26, v27, v26
	v_med3_f32 v27, v33, s47, v204
	v_mul_f32_e32 v28, v28, v29
	v_add_f32_e32 v27, 1.0, v27
	v_mul_f32_e32 v27, v27, v28
	v_add_f32_e32 v28, 1.0, v32
	v_rcp_f32_e32 v28, v28
	v_mov_b32_e32 v66, 0
	v_cvt_pk_fp8_f32 v66, v25, v26
	v_med3_f32 v29, v31, s47, v204
	v_mul_f32_e32 v25, v30, v28
	v_add_f32_e32 v26, 1.0, v29
	v_mul_f32_e32 v25, v26, v25
	v_pk_fma_f32 v[28:29], v[58:59], s[16:17], v[14:15] op_sel_hi:[1,0,1]
	v_cvt_pk_fp8_f32 v66, v27, v25 op_sel:[0,0,1]
	v_min_f32_e32 v25, 0x40e00000, v28
	v_mul_f32_e32 v28, 0xc01d265f, v25
	v_exp_f32_e32 v28, v28
	v_pk_fma_f32 v[26:27], v[60:61], s[16:17], v[16:17] op_sel_hi:[1,0,1]
	v_pk_fma_f32 v[32:33], v[50:51], s[16:17], v[10:11] op_sel_hi:[1,0,1]
	v_min_f32_e32 v26, 0x40e00000, v26
	v_add_f32_e32 v28, 1.0, v28
	v_rcp_f32_e32 v28, v28
	v_mul_f32_e32 v50, 0xc01d265f, v26
	v_exp_f32_e32 v50, v50
	v_med3_f32 v29, v29, s47, v204
	v_mul_f32_e32 v25, v25, v28
	v_add_f32_e32 v28, 1.0, v29
	v_min_f32_e32 v29, 0x40e00000, v32
	v_mul_f32_e32 v32, 0xc01d265f, v29
	v_mul_f32_e32 v25, v28, v25
	v_add_f32_e32 v28, 1.0, v50
	v_rcp_f32_e32 v28, v28
	v_exp_f32_e32 v32, v32
	v_pk_fma_f32 v[30:31], v[52:53], s[16:17], v[12:13] op_sel_hi:[1,0,1]
	v_med3_f32 v27, v27, s47, v204
	v_min_f32_e32 v30, 0x40e00000, v30
	v_mul_f32_e32 v26, v26, v28
	v_add_f32_e32 v28, 1.0, v32
	v_mul_f32_e32 v32, 0xc01d265f, v30
	v_rcp_f32_e32 v28, v28
	v_exp_f32_e32 v32, v32
	v_add_f32_e32 v27, 1.0, v27
	v_mul_f32_e32 v26, v27, v26
	v_mul_f32_e32 v28, v29, v28
	v_add_f32_e32 v29, 1.0, v32
	v_rcp_f32_e32 v29, v29
	v_med3_f32 v27, v33, s47, v204
	v_add_f32_e32 v27, 1.0, v27
	v_mul_f32_e32 v28, v27, v28
	v_med3_f32 v27, v31, s47, v204
	v_mul_f32_e32 v29, v30, v29
	v_add_f32_e32 v27, 1.0, v27
	v_mov_b32_e32 v50, 0
	v_mul_f32_e32 v29, v27, v29
	v_cvt_pk_fp8_f32 v50, v25, v26
	v_pk_fma_f32 v[26:27], v[62:63], s[16:17], v[6:7] op_sel_hi:[1,0,1]
	v_pk_fma_f32 v[30:31], v[56:57], s[16:17], v[4:5] op_sel_hi:[1,0,1]
	v_min_f32_e32 v25, 0x40e00000, v26
	v_mul_f32_e32 v26, 0xc01d265f, v25
	v_exp_f32_e32 v26, v26
	v_cvt_pk_fp8_f32 v50, v28, v29 op_sel:[0,0,1]
	v_pk_fma_f32 v[28:29], v[64:65], s[16:17], v[8:9] op_sel_hi:[1,0,1]
	v_med3_f32 v27, v27, s47, v204
	v_min_f32_e32 v28, 0x40e00000, v28
	v_mul_f32_e32 v32, 0xc01d265f, v28
	v_add_f32_e32 v26, 1.0, v26
	v_rcp_f32_e32 v26, v26
	v_exp_f32_e32 v51, v32
	v_pk_fma_f32 v[32:33], v[54:55], s[16:17], v[2:3] op_sel_hi:[1,0,1]
	v_add_f32_e32 v27, 1.0, v27
; #define LAS __attribute__((address_space(3)))
; __device__ __forceinline__ unsigned pk4_fp8(float a, float b, float c, float d) { int w = 0; w = __builtin_amdgcn_cvt_pk_fp8_f32(a, b, w, false); w = __builtin_amdgcn_cvt_pk_fp8_f32(c, d, w, true); return (unsigned)w; }
; __device__ __forceinline__ float swiglu1(float g, float l) {
;     g = fminf(g, 7.0f); l = fminf(fmaxf(l, -7.0f), 7.0f);
;     const float s = __builtin_amdgcn_rcpf(1.0f + __expf(-1.702f * g));
;     return g * s * (l + 1.0f);
; }
;     __device__ __forceinline__ void operator()(const f32x4 (&acc)[2][2][4][2], const Unit& u, int wr, int wc, int fr, int fq) const {
;     ...
;         for (int ai = 0; ai < 2; ++ai) {
; #pragma unroll
;             for (int m = 0; m < 4; ++m)
; #pragma unroll
;                 for (int bj = 0; bj < 2; ++bj) { const f32x4 v0 = acc[ai][bj][m][0] * scale + bv[bj][0], v1 = acc[ai][bj][m][1] * scale + bv[bj][1];
;                     *(LAS unsigned*)(wp + m * (32 * STG8_PITCH) + 64 * bj) = pk4_fp8(swiglu1(v0[0], v0[1]), swiglu1(v0[2], v0[3]), swiglu1(v1[0], v1[1]), swiglu1(v1[2], v1[3])); }
;             asm volatile("s_waitcnt lgkmcnt(0)" ::: "memory"); __builtin_amdgcn_s_barrier(); asm volatile("" ::: "memory");
; #pragma unroll
;             for (int k2 = 0; k2 < 2; ++k2) { const int m = ms + 2 * k2;
;                 *(u32x4*)(gp + (size_t)(ai * HALF + m * 16) * ldc) = *(const LAS u32x4*)(rp + m * (32 * STG8_PITCH)); }
;             asm volatile("s_waitcnt lgkmcnt(0)" ::: "memory"); __builtin_amdgcn_s_barrier(); asm volatile("" ::: "memory");
;         }
	v_mul_f32_e32 v25, v25, v26
	v_add_f32_e32 v26, 1.0, v51
	v_rcp_f32_e32 v26, v26
	v_mul_f32_e32 v25, v27, v25
	v_med3_f32 v27, v29, s47, v204
	v_min_f32_e32 v30, 0x40e00000, v30
	v_mul_f32_e32 v26, v28, v26
	v_min_f32_e32 v28, 0x40e00000, v32
	v_mul_f32_e32 v29, 0xc01d265f, v28
	v_exp_f32_e32 v29, v29
	v_mul_f32_e32 v32, 0xc01d265f, v30
	v_exp_f32_e32 v32, v32
	v_add_f32_e32 v29, 1.0, v29
	v_rcp_f32_e32 v29, v29
	v_add_f32_e32 v27, 1.0, v27
	v_mul_f32_e32 v26, v27, v26
	v_med3_f32 v27, v33, s47, v204
	v_mul_f32_e32 v28, v28, v29
	v_add_f32_e32 v27, 1.0, v27
	v_mul_f32_e32 v27, v27, v28
	v_add_f32_e32 v28, 1.0, v32
	v_rcp_f32_e32 v28, v28
	v_med3_f32 v29, v31, s47, v204
	v_mov_b32_e32 v31, 0
	v_cvt_pk_fp8_f32 v31, v25, v26
	v_mul_f32_e32 v25, v30, v28
	v_add_f32_e32 v26, 1.0, v29
	v_pk_fma_f32 v[14:15], v[38:39], s[16:17], v[14:15] op_sel_hi:[1,0,1]
	v_mul_f32_e32 v25, v26, v25
	v_min_f32_e32 v14, 0x40e00000, v14
	v_cvt_pk_fp8_f32 v31, v27, v25 op_sel:[0,0,1]
	v_mul_f32_e32 v25, 0xc01d265f, v14
	v_exp_f32_e32 v25, v25
	v_pk_fma_f32 v[16:17], v[40:41], s[16:17], v[16:17] op_sel_hi:[1,0,1]
	v_pk_fma_f32 v[10:11], v[34:35], s[16:17], v[10:11] op_sel_hi:[1,0,1]
	v_min_f32_e32 v16, 0x40e00000, v16
	v_add_f32_e32 v25, 1.0, v25
	v_mul_f32_e32 v26, 0xc01d265f, v16
	v_rcp_f32_e32 v25, v25
	v_exp_f32_e32 v26, v26
	v_med3_f32 v15, v15, s47, v204
	v_min_f32_e32 v10, 0x40e00000, v10
	v_mul_f32_e32 v14, v14, v25
	v_add_f32_e32 v15, 1.0, v15
	v_mul_f32_e32 v25, 0xc01d265f, v10
	v_mul_f32_e32 v14, v15, v14
	v_add_f32_e32 v15, 1.0, v26
	v_rcp_f32_e32 v15, v15
	v_exp_f32_e32 v25, v25
	v_pk_fma_f32 v[12:13], v[36:37], s[16:17], v[12:13] op_sel_hi:[1,0,1]
	v_med3_f32 v17, v17, s47, v204
	v_min_f32_e32 v12, 0x40e00000, v12
	v_mul_f32_e32 v15, v16, v15
	v_add_f32_e32 v16, 1.0, v17
	v_add_f32_e32 v17, 1.0, v25
	v_mul_f32_e32 v25, 0xc01d265f, v12
	v_exp_f32_e32 v25, v25
	v_rcp_f32_e32 v17, v17
	v_mul_f32_e32 v15, v16, v15
	v_med3_f32 v11, v11, s47, v204
	v_add_f32_e32 v16, 1.0, v25
	v_rcp_f32_e32 v16, v16
	v_mul_f32_e32 v10, v10, v17
	v_add_f32_e32 v11, 1.0, v11
	v_pk_fma_f32 v[6:7], v[46:47], s[16:17], v[6:7] op_sel_hi:[1,0,1]
	v_mul_f32_e32 v10, v11, v10
	v_med3_f32 v11, v13, s47, v204
	v_min_f32_e32 v6, 0x40e00000, v6
	v_mul_f32_e32 v12, v12, v16
	v_add_f32_e32 v11, 1.0, v11
	v_mul_f32_e32 v13, 0xc01d265f, v6
	v_mul_f32_e32 v11, v11, v12
	v_mov_b32_e32 v12, 0
	v_cvt_pk_fp8_f32 v12, v14, v15
	v_exp_f32_e32 v13, v13
	v_pk_fma_f32 v[8:9], v[48:49], s[16:17], v[8:9] op_sel_hi:[1,0,1]
	v_pk_fma_f32 v[2:3], v[42:43], s[16:17], v[2:3] op_sel_hi:[1,0,1]
	v_min_f32_e32 v8, 0x40e00000, v8
	v_cvt_pk_fp8_f32 v12, v10, v11 op_sel:[0,0,1]
	v_add_f32_e32 v10, 1.0, v13
	v_mul_f32_e32 v11, 0xc01d265f, v8
	v_rcp_f32_e32 v10, v10
	v_exp_f32_e32 v11, v11
	v_med3_f32 v7, v7, s47, v204
	v_mul_f32_e32 v6, v6, v10
	v_add_f32_e32 v7, 1.0, v7
	v_min_f32_e32 v2, 0x40e00000, v2
	v_add_f32_e32 v10, 1.0, v11
	v_mul_f32_e32 v6, v7, v6
	v_med3_f32 v7, v9, s47, v204
	v_mul_f32_e32 v9, 0xc01d265f, v2
	v_rcp_f32_e32 v10, v10
	v_exp_f32_e32 v9, v9
	v_pk_fma_f32 v[4:5], v[44:45], s[16:17], v[4:5] op_sel_hi:[1,0,1]
	v_mul_f32_e32 v8, v8, v10
	v_add_f32_e32 v7, 1.0, v7
	v_min_f32_e32 v4, 0x40e00000, v4
	v_mul_f32_e32 v7, v7, v8
	v_add_f32_e32 v8, 1.0, v9
	v_mul_f32_e32 v9, 0xc01d265f, v4
	v_rcp_f32_e32 v8, v8
	v_exp_f32_e32 v9, v9
	v_med3_f32 v3, v3, s47, v204
	v_mul_f32_e32 v2, v2, v8
	v_add_f32_e32 v3, 1.0, v3
	v_mul_f32_e32 v2, v3, v2
	v_add_f32_e32 v3, 1.0, v9
	v_rcp_f32_e32 v3, v3
	v_mov_b32_e32 v8, 0
	v_cvt_pk_fp8_f32 v8, v6, v7
	v_med3_f32 v5, v5, s47, v204
	v_mul_f32_e32 v3, v4, v3
	v_add_f32_e32 v4, 1.0, v5
	v_mul_f32_e32 v3, v4, v3
	v_cvt_pk_fp8_f32 v8, v2, v3 op_sel:[0,0,1]
	s_waitcnt lgkmcnt(0)
	s_barrier
	ds_write2_b32 v202, v90, v82 offset1:16
	ds_write2_b32 v22, v74, v66 offset0:128 offset1:144
	ds_write2_b32 v23, v50, v31 offset1:16
	ds_write2_b32 v24, v12, v8 offset0:128 offset1:144
	s_waitcnt lgkmcnt(0)
	s_barrier
	ds_read_b128 v[2:5], v203
	ds_read_b128 v[6:9], v203 offset:9216
	v_add_co_u32_e32 v10, vcc, s48, v20
	s_nop 1
	v_addc_co_u32_e32 v11, vcc, 0, v21, vcc
	s_waitcnt lgkmcnt(1)
	global_store_dwordx4 v[10:11], v[2:5], off
	s_nop 1
	v_add_co_u32_e32 v2, vcc, 0x40000, v18
	s_nop 1
	v_addc_co_u32_e32 v3, vcc, 0, v19, vcc
	s_waitcnt lgkmcnt(0)
	global_store_dwordx4 v[2:3], v[6:9], off
	s_waitcnt lgkmcnt(0)
	s_barrier
	s_cbranch_scc1 .LBB0_993
	s_andn2_b64 vcc, exec, s[6:7]
	s_cbranch_vccnz .LBB0_992
	s_barrier
	s_branch .LBB0_992

; #define LAS __attribute__((address_space(3)))
; __device__ __forceinline__ f32x4 ld_bf4(const bf16_t* p) { const u32x2 w = *(const u32x2*)p; return (f32x4){__builtin_bit_cast(float, w.x << 16), __builtin_bit_cast(float, w.x & 0xffff0000u), __builtin_bit_cast(float, w.y << 16), __builtin_bit_cast(float, w.y & 0xffff0000u)}; }
; __device__ __forceinline__ void p11_final(Frame& F) {
;     ...
;     const LAS int* tab = (const LAS int*)(F.lds + TAB_OFF); const LAS int* rp = (const LAS int*)(F.lds + RP_OFF);
;     const float* mod = WSP(float, WS_MOD); const bf16_t* X1 = WSP(bf16_t, WS_X1); const unsigned char* YM = WSP(unsigned char, WS_YM);
;     const int* tok_e = WSP(int, WS_ROUTE); const int* tok_rank = tok_e + M_LAT * TOPK; const float* tok_gate = (const float*)(tok_rank + M_LAT * TOPK);
;     const int gw = F.bx * NWAVES + F.wave, NGW = F.G * NWAVES;
;     for (int row = gw; row < M_LAT; row += NGW) {
;         const float* mr = mod + (row / T) * NMOD;
;         f32x4 v[8];
; #pragma unroll
;         for (int j = 0; j < 8; ++j) v[j] = (f32x4){0.f, 0.f, 0.f, 0.f};
; #pragma unroll
;         for (int k = 0; k < TOPK; ++k) {
;             const int e = tok_e[row * TOPK + k], rank = tok_rank[row * TOPK + k]; const float gt = tok_gate[row * TOPK + k];
;             const unsigned char* yr = YM + (size_t)(tab[e] + rp[e * RR + (row / (8 * ((M_LAT + NGW - 1) / NGW))) % RR] + rank) * D;
; #pragma unroll
;             for (int j = 0; j < 8; ++j) { const int w = *(const int*)(yr + 4 * F.lane + 256 * j);
;                 const f32x2 lo = __builtin_amdgcn_cvt_pk_f32_fp8(w, false), hi = __builtin_amdgcn_cvt_pk_f32_fp8(w, true);
;                 v[j].x += gt * lo.x; v[j].y += gt * lo.y; v[j].z += gt * hi.x; v[j].w += gt * hi.y; }
;         }
;         float ss = 0.f;
; #pragma unroll
;         for (int j = 0; j < 8; ++j) ss += (v[j].x * v[j].x + v[j].y * v[j].y) + (v[j].z * v[j].z + v[j].w * v[j].w);
;         const float rstd = __builtin_amdgcn_rsqf(wave_sum(ss) * (1.0f / D) + RMS_EPS);
; #pragma unroll
;         for (int j = 0; j < 8; ++j) { const int c = 4 * F.lane + 256 * j;
;             const f32x4 xv = ld_bf4(X1 + (size_t)row * D + c), g = *(const f32x4*)(IN_NORMG + 3 * D + c), gt = *(const f32x4*)(mr + 5 * D + c);
.LBB0_1213:
	s_or_b64 exec, exec, s[0:1]
	s_lshl_b32 s0, s91, 3
	v_readlane_b32 s1, v254, 35
	s_add_i32 s0, s0, s1
	s_cmpk_gt_i32 s0, 0x3fff
	s_waitcnt lgkmcnt(0)
	s_barrier
	s_cbranch_scc1 .LBB0_1216
	s_add_u32 s12, s96, 0x8ec00000
	s_addc_u32 s13, s97, 0
	s_add_u32 s14, s96, 0x8ec40000
	s_addc_u32 s15, s97, 0
	s_add_u32 s16, s96, 0x8ec80000
	s_addc_u32 s17, s97, 0
	s_lshl_b32 s4, s79, 3
	s_abs_i32 s1, s4
	v_cvt_f32_u32_e32 v0, s1
	s_sub_i32 s5, 0, s1
	s_add_i32 s2, s4, 0x3fff
	s_xor_b32 s3, s2, s4
	v_rcp_iflag_f32_e32 v0, v0
	s_abs_i32 s2, s2
	s_ashr_i32 s3, s3, 31
	v_lshlrev_b32_e32 v8, 2, v1
	v_mul_f32_e32 v0, 0x4f7ffffe, v0
	v_cvt_u32_f32_e32 v0, v0
	v_mov_b32_e32 v9, 0
	v_lshl_add_u64 v[2:3], s[96:97], 0, v[8:9]
	v_mov_b32_e32 v5, v9
	v_readfirstlane_b32 s6, v0
	s_mul_i32 s5, s5, s6
	s_mul_hi_u32 s5, s6, s5
	s_add_i32 s6, s6, s5
	s_mul_hi_u32 s5, s2, s6
	s_mul_i32 s6, s5, s1
	s_sub_i32 s2, s2, s6
	s_add_i32 s7, s5, 1
	s_sub_i32 s6, s2, s1
	s_cmp_ge_u32 s2, s1
	s_cselect_b32 s5, s7, s5
	s_cselect_b32 s2, s6, s2
	s_add_i32 s6, s5, 1
	s_cmp_ge_u32 s2, s1
	s_cselect_b32 s1, s6, s5
	s_xor_b32 s1, s1, s3
	s_sub_i32 s1, s1, s3
	s_lshl_b32 s1, s1, 3
	s_mov_b64 s[2:3], 0xb3400000
	v_lshl_add_u64 v[10:11], v[2:3], 0, s[2:3]
	s_add_u32 s2, s48, 0x6000
	v_or_b32_e32 v0, 0x100, v8
	s_addc_u32 s3, s49, 0
	v_lshlrev_b32_e32 v4, 2, v0
	s_abs_i32 s18, s1
	v_lshl_add_u64 v[14:15], s[2:3], 0, v[4:5]
	v_cvt_f32_u32_e32 v5, s18
	v_or_b32_e32 v4, 0x200, v8
	v_lshlrev_b32_e32 v6, 2, v4
	v_mov_b32_e32 v7, v9
	v_rcp_iflag_f32_e32 v5, v5
	v_lshl_add_u64 v[16:17], s[2:3], 0, v[6:7]
	v_or_b32_e32 v6, 0x300, v8
	v_or_b32_e32 v32, 0x400, v8
	v_mul_f32_e32 v5, 0x4f7ffffe, v5
	v_cvt_u32_f32_e32 v5, v5
	v_or_b32_e32 v34, 0x500, v8
	v_or_b32_e32 v36, 0x600, v8
	v_or_b32_e32 v38, 0x700, v8
	v_lshlrev_b32_e32 v2, 4, v1
	v_mov_b32_e32 v3, v9
	v_lshlrev_b32_e32 v18, 2, v6
	v_mov_b32_e32 v19, v9
	v_lshlrev_b32_e32 v20, 2, v32
	v_mov_b32_e32 v21, v9
	v_lshlrev_b32_e32 v22, 2, v34
	v_mov_b32_e32 v23, v9
	v_lshlrev_b32_e32 v24, 2, v36
	v_mov_b32_e32 v25, v9
	v_lshlrev_b32_e32 v26, 2, v38
	v_mov_b32_e32 v27, v9
	v_lshl_add_u64 v[12:13], s[2:3], 0, v[2:3]
	v_lshl_add_u64 v[18:19], s[2:3], 0, v[18:19]
	v_lshl_add_u64 v[20:21], s[2:3], 0, v[20:21]
	v_lshl_add_u64 v[22:23], s[2:3], 0, v[22:23]
	v_lshl_add_u64 v[24:25], s[2:3], 0, v[24:25]
	v_lshl_add_u64 v[26:27], s[2:3], 0, v[26:27]
	s_ashr_i32 s19, s1, 31
	s_sub_i32 s1, 0, s18
	v_readfirstlane_b32 s2, v5
	s_mul_i32 s1, s1, s2
	s_mul_hi_u32 s1, s2, s1
	s_add_i32 s20, s2, s1
	s_ashr_i32 s1, s0, 31
	s_lshl_b64 s[2:3], s[0:1], 12
	s_add_u32 s2, s96, s2
	v_lshlrev_b32_e32 v28, 3, v1
	v_mov_b32_e32 v29, v9
	s_addc_u32 s3, s97, s3
	v_lshl_add_u64 v[28:29], s[2:3], 0, v[28:29]
	s_mov_b64 s[2:3], 0x82c00000
	v_lshl_add_u64 v[28:29], v[28:29], 0, s[2:3]
	v_readlane_b32 s3, v254, 35
	s_lshl_b32 s2, s91, 5
	s_lshl_b32 s3, s3, 2
	v_readlane_b32 s24, v254, 0
	s_ashr_i32 s5, s4, 31
	s_add_i32 s2, s2, s3
	v_readlane_b32 s30, v254, 6
	v_readlane_b32 s31, v254, 7
	s_lshl_b64 s[6:7], s[4:5], 12
	s_or_b32 s2, s2, 3
	s_lshl_b32 s21, s79, 5
	s_lshl_b64 s[8:9], s[0:1], 13
	s_mov_b64 s[10:11], s[30:31]
	s_add_u32 s8, s10, s8
	s_addc_u32 s9, s11, s9
	v_lshl_add_u64 v[2:3], s[8:9], 0, v[2:3]
	s_mov_b64 s[8:9], 0x1000
	v_lshl_add_u64 v[30:31], v[2:3], 0, s[8:9]
	s_lshl_b64 s[8:9], s[4:5], 13
	s_add_i32 s1, 0, 0x20100
	v_mov_b32_e32 v56, 0x358637bd
	v_lshlrev_b32_e32 v57, 2, v8
	v_lshlrev_b32_e32 v58, 2, v0
	v_lshlrev_b32_e32 v59, 2, v4
	v_lshlrev_b32_e32 v60, 2, v6
	v_lshlrev_b32_e32 v61, 2, v32
	v_lshlrev_b32_e32 v62, 2, v34
	v_lshlrev_b32_e32 v63, 2, v36
	v_lshlrev_b32_e32 v64, 2, v38
	v_readlane_b32 s25, v254, 1
	v_readlane_b32 s26, v254, 2
	v_readlane_b32 s27, v254, 3
	v_readlane_b32 s28, v254, 4
	v_readlane_b32 s29, v254, 5
	global_load_dwordx4 v[152:155], v[14:15], off
	global_load_dwordx4 v[156:159], v[16:17], off
	global_load_dwordx4 v[160:163], v[18:19], off
	global_load_dwordx4 v[164:167], v[20:21], off
	global_load_dwordx4 v[168:171], v[22:23], off
	global_load_dwordx4 v[172:175], v[24:25], off
	global_load_dwordx4 v[176:179], v[26:27], off
	s_waitcnt vmcnt(0)
.LBB0_1215:
	s_ashr_i32 s3, s0, 31
	s_abs_i32 s5, s0
	s_lshr_b32 s11, s3, 20
	s_mul_hi_u32 s24, s5, s20
	s_add_i32 s11, s0, s11
	s_mul_i32 s22, s24, s18
	s_lshr_b32 s11, s11, 12
	s_sub_i32 s5, s5, s22
	s_mul_i32 s22, s11, 0x3000
	s_add_i32 s10, s2, -3
	s_xor_b32 s3, s3, s19
	s_add_i32 s25, s24, 1
	s_sub_i32 s11, s5, s18
	s_ashr_i32 s23, s22, 31
	s_cmp_ge_u32 s5, s18
	s_cselect_b32 s24, s25, s24
	s_cselect_b32 s5, s11, s5
	s_add_i32 s11, s24, 1
	s_cmp_ge_u32 s5, s18
	s_cselect_b32 s5, s11, s24
	s_xor_b32 s5, s5, s3
	s_sub_i32 s3, s5, s3
	s_ashr_i32 s5, s3, 31
	s_lshr_b32 s5, s5, 28
	s_add_i32 s5, s3, s5
	s_and_b32 s5, s5, 0x3ffffff0
	s_sub_i32 s3, s3, s5
	s_lshl_b32 s3, s3, 2
	s_ashr_i32 s11, s10, 31
	s_add_i32 s3, s3, 0
	s_lshl_b64 s[10:11], s[10:11], 2
	s_add_i32 s5, s3, 0x20300
	s_add_u32 s24, s12, s10
	s_addc_u32 s25, s13, s11
	s_lshl_b64 s[26:27], s[22:23], 2
	s_add_u32 s26, s96, s26
	s_addc_u32 s27, s97, s27
	s_add_u32 s26, s26, 0x10a000
	s_addc_u32 s27, s27, 0
	global_load_dwordx2 v[180:181], v[28:29], off offset:512
	global_load_dwordx4 v[196:199], v58, s[26:27]
	global_load_dwordx2 v[182:183], v[28:29], off offset:1024
	global_load_dwordx4 v[200:203], v59, s[26:27]
	global_load_dwordx2 v[184:185], v[28:29], off offset:1536
	global_load_dwordx4 v[204:207], v60, s[26:27]
	global_load_dwordx2 v[186:187], v[28:29], off offset:2048
	global_load_dwordx4 v[208:211], v61, s[26:27]
	global_load_dwordx2 v[188:189], v[28:29], off offset:2560
	global_load_dwordx4 v[212:215], v62, s[26:27]
; __device__ __forceinline__ f32x4 ld_bf4(const bf16_t* p) { const u32x2 w = *(const u32x2*)p; return (f32x4){__builtin_bit_cast(float, w.x << 16), __builtin_bit_cast(float, w.x & 0xffff0000u), __builtin_bit_cast(float, w.y << 16), __builtin_bit_cast(float, w.y & 0xffff0000u)}; }
; __device__ __forceinline__ void p11_final(Frame& F) {
;     ...
;         for (int k = 0; k < TOPK; ++k) {
;             const int e = tok_e[row * TOPK + k], rank = tok_rank[row * TOPK + k]; const float gt = tok_gate[row * TOPK + k];
;             const unsigned char* yr = YM + (size_t)(tab[e] + rp[e * RR + (row / (8 * ((M_LAT + NGW - 1) / NGW))) % RR] + rank) * D;
; #pragma unroll
;             for (int j = 0; j < 8; ++j) { const int w = *(const int*)(yr + 4 * F.lane + 256 * j);
;                 const f32x2 lo = __builtin_amdgcn_cvt_pk_f32_fp8(w, false), hi = __builtin_amdgcn_cvt_pk_f32_fp8(w, true);
;                 v[j].x += gt * lo.x; v[j].y += gt * lo.y; v[j].z += gt * hi.x; v[j].w += gt * hi.y; }
;         }
;         float ss = 0.f;
; #pragma unroll
;         for (int j = 0; j < 8; ++j) ss += (v[j].x * v[j].x + v[j].y * v[j].y) + (v[j].z * v[j].z + v[j].w * v[j].w);
;         const float rstd = __builtin_amdgcn_rsqf(wave_sum(ss) * (1.0f / D) + RMS_EPS);
; #pragma unroll
;         for (int j = 0; j < 8; ++j) { const int c = 4 * F.lane + 256 * j;
;             const f32x4 xv = ld_bf4(X1 + (size_t)row * D + c), g = *(const f32x4*)(IN_NORMG + 3 * D + c), gt = *(const f32x4*)(mr + 5 * D + c);
	global_load_dwordx2 v[190:191], v[28:29], off offset:3072
	global_load_dwordx4 v[216:219], v63, s[26:27]
	global_load_dwordx2 v[192:193], v[28:29], off offset:3584
	global_load_dwordx4 v[220:223], v64, s[26:27]
	global_load_dwordx2 v[34:35], v[28:29], off
	global_load_dwordx4 v[0:3], v[12:13], off
	global_load_dword v8, v9, s[24:25]
	s_add_u32 s24, s14, s10
	s_addc_u32 s25, s15, s11
	s_add_u32 s10, s16, s10
	s_addc_u32 s11, s17, s11
	global_load_dword v32, v9, s[24:25]
	global_load_dword v44, v9, s[10:11]
	s_add_i32 s24, s2, -2
	s_ashr_i32 s25, s24, 31
	s_lshl_b64 s[10:11], s[24:25], 2
	s_add_u32 s24, s12, s10
	s_addc_u32 s25, s13, s11
	global_load_dword v40, v9, s[24:25]
	s_add_u32 s24, s14, s10
	s_addc_u32 s25, s15, s11
	s_add_u32 s10, s16, s10
	s_addc_u32 s11, s17, s11
	global_load_dword v43, v9, s[24:25]
	global_load_dword v45, v9, s[10:11]
	s_add_i32 s24, s2, -1
	s_ashr_i32 s25, s24, 31
	s_lshl_b64 s[10:11], s[24:25], 2
	s_add_u32 s24, s12, s10
	s_addc_u32 s25, s13, s11
	global_load_dword v47, v9, s[24:25]
	s_add_u32 s24, s14, s10
	s_addc_u32 s25, s15, s11
	s_add_u32 s10, s16, s10
	s_addc_u32 s11, s17, s11
	s_ashr_i32 s3, s2, 31
	global_load_dword v48, v9, s[24:25]
	global_load_dword v42, v9, s[10:11]
	s_lshl_b64 s[10:11], s[2:3], 2
	s_add_u32 s24, s12, s10
	s_addc_u32 s25, s13, s11
	global_load_dword v49, v9, s[24:25]
	s_add_u32 s24, s14, s10
	s_addc_u32 s25, s15, s11
	global_load_dword v54, v9, s[24:25]
	s_add_u32 s10, s16, s10
	s_addc_u32 s11, s17, s11
	s_lshl_b64 s[22:23], s[22:23], 2
	s_add_u32 s3, s96, s22
	global_load_dword v46, v9, s[10:11]
	s_addc_u32 s11, s97, s23
	s_add_u32 s10, s3, 0x10a000
	s_addc_u32 s11, s11, 0
	global_load_dwordx4 v[4:7], v57, s[10:11]
	v_mov_b32_e32 v33, v9
	v_mov_b32_e32 v41, v9
	s_add_i32 s0, s0, s4
	s_add_i32 s2, s2, s21
	s_cmpk_lt_i32 s0, 0x4000
	s_waitcnt vmcnt(14)
	v_lshlrev_b32_e32 v36, 16, v34
	v_and_b32_e32 v37, 0xffff0000, v34
	s_waitcnt vmcnt(12)
	v_lshlrev_b32_e32 v34, 2, v8
	v_lshlrev_b32_e32 v8, 6, v8
	v_add_u32_e32 v34, s1, v34
	v_add_u32_e32 v8, s5, v8
	ds_read_b32 v34, v34
	ds_read_b32 v8, v8
	v_lshlrev_b32_e32 v38, 16, v35
	v_and_b32_e32 v39, 0xffff0000, v35
	s_waitcnt vmcnt(10)
	v_mov_b32_e32 v51, v44
	s_waitcnt lgkmcnt(1)
	v_add_u32_e32 v32, v34, v32
	s_waitcnt vmcnt(9)
	v_lshlrev_b32_e32 v34, 2, v40
	v_lshlrev_b32_e32 v35, 6, v40
	v_add_u32_e32 v34, s1, v34
	v_add_u32_e32 v35, s5, v35
	ds_read_b32 v40, v34
	s_waitcnt lgkmcnt(1)
	v_add_u32_e32 v34, v32, v8
	ds_read_b32 v8, v35
	v_ashrrev_i32_e32 v35, 31, v34
	v_lshlrev_b64 v[34:35], 11, v[34:35]
	v_lshl_add_u64 v[34:35], v[10:11], 0, v[34:35]
	global_load_dword v55, v[34:35], off
	global_load_dword v65, v[34:35], off offset:256
	global_load_dword v72, v[34:35], off offset:512
	global_load_dword v76, v[34:35], off offset:768
	global_load_dword v80, v[34:35], off offset:1024
	global_load_dword v84, v[34:35], off offset:1280
	global_load_dword v88, v[34:35], off offset:1536
	global_load_dword v92, v[34:35], off offset:1792
	s_waitcnt vmcnt(16) lgkmcnt(1)
	v_add_u32_e32 v34, v40, v43
	s_waitcnt vmcnt(14)
	v_lshlrev_b32_e32 v35, 2, v47
	v_lshlrev_b32_e32 v40, 6, v47
	v_add_u32_e32 v35, s1, v35
	v_add_u32_e32 v40, s5, v40
	s_waitcnt lgkmcnt(0)
	v_add_u32_e32 v34, v34, v8
	ds_read_b32 v43, v35
	ds_read_b32 v8, v40
	v_ashrrev_i32_e32 v35, 31, v34
	v_lshlrev_b64 v[34:35], 11, v[34:35]
	v_lshl_add_u64 v[34:35], v[10:11], 0, v[34:35]
	global_load_dword v47, v[34:35], off
	global_load_dword v100, v[34:35], off offset:256
	global_load_dword v104, v[34:35], off offset:512
	global_load_dword v108, v[34:35], off offset:768
	global_load_dword v112, v[34:35], off offset:1024
	global_load_dword v116, v[34:35], off offset:1280
	global_load_dword v120, v[34:35], off offset:1536
	global_load_dword v124, v[34:35], off offset:1792
	s_waitcnt vmcnt(19)
	v_lshlrev_b32_e32 v35, 2, v49
	v_lshlrev_b32_e32 v40, 6, v49
	v_add_u32_e32 v35, s1, v35
	s_waitcnt lgkmcnt(1)
	v_add_u32_e32 v34, v43, v48
	v_add_u32_e32 v40, s5, v40
	ds_read_b32 v43, v35
	s_waitcnt lgkmcnt(1)
	v_add_u32_e32 v34, v34, v8
	ds_read_b32 v8, v40
	v_ashrrev_i32_e32 v35, 31, v34
	v_lshlrev_b64 v[52:53], 11, v[34:35]
	v_lshl_add_u64 v[52:53], v[10:11], 0, v[52:53]
	s_waitcnt vmcnt(18) lgkmcnt(1)
	v_add_u32_e32 v40, v43, v54
	global_load_dword v34, v[52:53], off
	global_load_dword v48, v[52:53], off offset:256
	global_load_dword v126, v[52:53], off offset:512
	global_load_dword v127, v[52:53], off offset:768
	global_load_dword v128, v[52:53], off offset:1024
	global_load_dword v129, v[52:53], off offset:1280
	global_load_dword v130, v[52:53], off offset:1536
	global_load_dword v131, v[52:53], off offset:1792
	s_waitcnt lgkmcnt(0)
	v_add_u32_e32 v52, v40, v8
	v_ashrrev_i32_e32 v53, 31, v52
	v_lshlrev_b64 v[52:53], 11, v[52:53]
	v_lshl_add_u64 v[52:53], v[10:11], 0, v[52:53]
	global_load_dword v132, v[52:53], off
	global_load_dword v133, v[52:53], off offset:256
	global_load_dword v134, v[52:53], off offset:512
	global_load_dword v135, v[52:53], off offset:768
	global_load_dword v136, v[52:53], off offset:1024
	global_load_dword v137, v[52:53], off offset:1280
	global_load_dword v140, v[52:53], off offset:1536
	global_load_dword v144, v[52:53], off offset:1792
	v_mov_b32_e32 v32, v45
	v_mov_b32_e32 v50, v45
	s_waitcnt vmcnt(33)
	v_mov_b32_e32 v49, v46
	v_mov_b32_e32 v35, v46
	s_waitcnt vmcnt(31)
	v_cvt_pk_f32_fp8_e32 v[52:53], v55
	s_waitcnt vmcnt(30)
	v_cvt_pk_f32_fp8_e32 v[66:67], v65
	v_cvt_pk_f32_fp8_sdwa v[68:69], v65 src0_sel:WORD_1
	s_waitcnt vmcnt(29)
	v_cvt_pk_f32_fp8_e32 v[70:71], v72
	v_cvt_pk_f32_fp8_sdwa v[72:73], v72 src0_sel:WORD_1
	s_waitcnt vmcnt(28)
; __device__ __forceinline__ void p11_final(Frame& F) {
;     ...
;         for (int k = 0; k < TOPK; ++k) {
;             const int e = tok_e[row * TOPK + k], rank = tok_rank[row * TOPK + k]; const float gt = tok_gate[row * TOPK + k];
;             const unsigned char* yr = YM + (size_t)(tab[e] + rp[e * RR + (row / (8 * ((M_LAT + NGW - 1) / NGW))) % RR] + rank) * D;
; #pragma unroll
;             for (int j = 0; j < 8; ++j) { const int w = *(const int*)(yr + 4 * F.lane + 256 * j);
;                 const f32x2 lo = __builtin_amdgcn_cvt_pk_f32_fp8(w, false), hi = __builtin_amdgcn_cvt_pk_f32_fp8(w, true);
;                 v[j].x += gt * lo.x; v[j].y += gt * lo.y; v[j].z += gt * hi.x; v[j].w += gt * hi.y; }
;         }
;         float ss = 0.f;
; #pragma unroll
;         for (int j = 0; j < 8; ++j) ss += (v[j].x * v[j].x + v[j].y * v[j].y) + (v[j].z * v[j].z + v[j].w * v[j].w);
	v_cvt_pk_f32_fp8_e32 v[74:75], v76
	v_cvt_pk_f32_fp8_sdwa v[76:77], v76 src0_sel:WORD_1
	s_waitcnt vmcnt(27)
	v_cvt_pk_f32_fp8_e32 v[78:79], v80
	v_cvt_pk_f32_fp8_sdwa v[80:81], v80 src0_sel:WORD_1
	s_waitcnt vmcnt(26)
	v_cvt_pk_f32_fp8_e32 v[82:83], v84
	v_cvt_pk_f32_fp8_sdwa v[84:85], v84 src0_sel:WORD_1
	s_waitcnt vmcnt(25)
	v_cvt_pk_f32_fp8_e32 v[86:87], v88
	v_mov_b32_e32 v94, v66
	v_mov_b32_e32 v95, v68
	v_cvt_pk_f32_fp8_sdwa v[54:55], v55 src0_sel:WORD_1
	v_cvt_pk_f32_fp8_sdwa v[88:89], v88 src0_sel:WORD_1
	s_waitcnt vmcnt(19)
	v_cvt_pk_f32_fp8_e32 v[110:111], v112
	s_waitcnt vmcnt(18)
	v_cvt_pk_f32_fp8_e32 v[114:115], v116
	v_cvt_pk_f32_fp8_sdwa v[116:117], v116 src0_sel:WORD_1
	v_cvt_pk_f32_fp8_e32 v[90:91], v92
	v_cvt_pk_f32_fp8_sdwa v[92:93], v92 src0_sel:WORD_1
	v_mov_b32_e32 v68, v67
	v_mov_b32_e32 v66, v70
	v_mov_b32_e32 v67, v72
	v_mov_b32_e32 v72, v71
	v_mov_b32_e32 v70, v74
	v_mov_b32_e32 v71, v76
	v_mov_b32_e32 v76, v75
	v_pk_fma_f32 v[74:75], v[44:45], v[80:81], 0 op_sel_hi:[0,1,0]
	v_pk_fma_f32 v[80:81], v[44:45], v[94:95], 0 op_sel_hi:[0,1,0]
	v_cvt_pk_f32_fp8_e32 v[94:95], v47
	v_cvt_pk_f32_fp8_e32 v[98:99], v100
	v_cvt_pk_f32_fp8_sdwa v[100:101], v100 src0_sel:WORD_1
	v_cvt_pk_f32_fp8_e32 v[106:107], v108
	v_cvt_pk_f32_fp8_sdwa v[108:109], v108 src0_sel:WORD_1
	s_waitcnt vmcnt(17)
	v_cvt_pk_f32_fp8_e32 v[118:119], v120
	v_cvt_pk_f32_fp8_sdwa v[120:121], v120 src0_sel:WORD_1
	v_cvt_pk_f32_fp8_sdwa v[96:97], v47 src0_sel:WORD_1
	v_cvt_pk_f32_fp8_e32 v[102:103], v104
	v_cvt_pk_f32_fp8_sdwa v[104:105], v104 src0_sel:WORD_1
	v_cvt_pk_f32_fp8_sdwa v[112:113], v112 src0_sel:WORD_1
	v_fma_f32 v8, v44, v86, 0
	v_mov_b32_e32 v86, v78
	v_mov_b32_e32 v78, v82
	v_mov_b32_e32 v82, v84
	v_mov_b32_e32 v84, v87
	v_pk_fma_f32 v[52:53], v[44:45], v[52:53], 0 op_sel_hi:[0,1,0]
	v_mov_b32_e32 v87, v110
	v_mov_b32_e32 v110, v79
	v_mov_b32_e32 v79, v114
	v_mov_b32_e32 v114, v83
	v_mov_b32_e32 v83, v116
	v_mov_b32_e32 v116, v85
	v_fma_f32 v40, v44, v88, 0
	v_mov_b32_e32 v88, v89
	v_pk_fma_f32 v[54:55], v[44:45], v[54:55], 0 op_sel_hi:[0,1,0]
	v_mov_b32_e32 v85, v119
	v_mov_b32_e32 v89, v121
	v_pk_fma_f32 v[52:53], v[32:33], v[94:95], v[52:53] op_sel_hi:[0,1,1]
	v_mov_b32_e32 v94, v98
	v_mov_b32_e32 v95, v100
	v_mov_b32_e32 v100, v99
	v_mov_b32_e32 v98, v106
	v_mov_b32_e32 v99, v108
	v_mov_b32_e32 v108, v107
	v_mov_b32_e32 v119, v92
	v_pk_mul_f32 v[78:79], v[44:45], v[78:79]
	v_pk_mul_f32 v[106:107], v[44:45], v[116:117]
	v_pk_fma_f32 v[68:69], v[44:45], v[68:69], 0 op_sel_hi:[0,1,0]
	v_pk_fma_f32 v[66:67], v[44:45], v[66:67], 0 op_sel_hi:[0,1,0]
	v_pk_fma_f32 v[72:73], v[44:45], v[72:73], 0 op_sel_hi:[0,1,0]
	v_pk_fma_f32 v[70:71], v[44:45], v[70:71], 0 op_sel_hi:[0,1,0]
	v_pk_fma_f32 v[76:77], v[44:45], v[76:77], 0 op_sel_hi:[0,1,0]
	v_pk_fma_f32 v[54:55], v[32:33], v[96:97], v[54:55] op_sel_hi:[0,1,1]
	v_mov_b32_e32 v96, v102
	v_mov_b32_e32 v97, v104
	v_mov_b32_e32 v104, v103
	v_mov_b32_e32 v121, v93
	v_pk_mul_f32 v[86:87], v[44:45], v[86:87]
	v_pk_mul_f32 v[92:93], v[44:45], v[110:111]
	v_pk_mul_f32 v[102:103], v[44:45], v[114:115]
	v_pk_mul_f32 v[82:83], v[44:45], v[82:83]
	v_pk_mul_f32 v[84:85], v[44:45], v[84:85]
	v_pk_mul_f32 v[88:89], v[44:45], v[88:89]
	v_pk_fma_f32 v[80:81], v[32:33], v[94:95], v[80:81] op_sel_hi:[0,1,1]
	v_pk_fma_f32 v[94:95], v[50:51], v[118:119], v[8:9]
	v_add_f32_e32 v8, 0, v78
	v_add_f32_e32 v43, 0, v106
	v_pk_fma_f32 v[74:75], v[32:33], v[112:113], v[74:75] op_sel_hi:[0,1,1]
	v_pk_fma_f32 v[68:69], v[32:33], v[100:101], v[68:69] op_sel_hi:[0,1,1]
	v_pk_fma_f32 v[66:67], v[32:33], v[96:97], v[66:67] op_sel_hi:[0,1,1]
	v_pk_fma_f32 v[72:73], v[32:33], v[104:105], v[72:73] op_sel_hi:[0,1,1]
	v_pk_fma_f32 v[70:71], v[32:33], v[98:99], v[70:71] op_sel_hi:[0,1,1]
	v_pk_fma_f32 v[76:77], v[32:33], v[108:109], v[76:77] op_sel_hi:[0,1,1]
	v_pk_fma_f32 v[40:41], v[50:51], v[120:121], v[40:41]
	v_mov_b32_e32 v50, v86
	v_mov_b32_e32 v51, v92
	v_mov_b32_e32 v92, v87
	v_mov_b32_e32 v86, v102
	v_mov_b32_e32 v87, v82
	v_mov_b32_e32 v82, v103
	v_mov_b32_e32 v96, v84
	v_mov_b32_e32 v97, v88
	v_mov_b32_e32 v88, v85
	v_add_f32_e32 v32, v8, v79
	v_add_f32_e32 v147, v43, v107
	s_waitcnt vmcnt(15)
	v_cvt_pk_f32_fp8_e32 v[78:79], v34
	v_cvt_pk_f32_fp8_sdwa v[84:85], v34 src0_sel:WORD_1
	s_waitcnt vmcnt(14)
	v_cvt_pk_f32_fp8_e32 v[98:99], v48
	v_cvt_pk_f32_fp8_sdwa v[100:101], v48 src0_sel:WORD_1
	s_waitcnt vmcnt(13)
	v_cvt_pk_f32_fp8_e32 v[102:103], v126
	v_cvt_pk_f32_fp8_sdwa v[104:105], v126 src0_sel:WORD_1
	s_waitcnt vmcnt(12)
	v_cvt_pk_f32_fp8_e32 v[106:107], v127
	v_cvt_pk_f32_fp8_sdwa v[108:109], v127 src0_sel:WORD_1
	v_cvt_pk_f32_fp8_e32 v[122:123], v124
	v_cvt_pk_f32_fp8_sdwa v[124:125], v124 src0_sel:WORD_1
	s_waitcnt vmcnt(11)
	v_cvt_pk_f32_fp8_sdwa v[112:113], v128 src0_sel:WORD_1
	s_waitcnt vmcnt(9)
	v_cvt_pk_f32_fp8_e32 v[118:119], v130
	v_cvt_pk_f32_fp8_sdwa v[120:121], v130 src0_sel:WORD_1
	v_cvt_pk_f32_fp8_e32 v[110:111], v128
	v_cvt_pk_f32_fp8_e32 v[114:115], v129
	v_cvt_pk_f32_fp8_sdwa v[116:117], v129 src0_sel:WORD_1
	s_waitcnt vmcnt(8)
; __device__ __forceinline__ void p11_final(Frame& F) {
;     ...
;         for (int k = 0; k < TOPK; ++k) {
;             const int e = tok_e[row * TOPK + k], rank = tok_rank[row * TOPK + k]; const float gt = tok_gate[row * TOPK + k];
;             const unsigned char* yr = YM + (size_t)(tab[e] + rp[e * RR + (row / (8 * ((M_LAT + NGW - 1) / NGW))) % RR] + rank) * D;
; #pragma unroll
;             for (int j = 0; j < 8; ++j) { const int w = *(const int*)(yr + 4 * F.lane + 256 * j);
;                 const f32x2 lo = __builtin_amdgcn_cvt_pk_f32_fp8(w, false), hi = __builtin_amdgcn_cvt_pk_f32_fp8(w, true);
;                 v[j].x += gt * lo.x; v[j].y += gt * lo.y; v[j].z += gt * hi.x; v[j].w += gt * hi.y; }
;         }
;         float ss = 0.f;
; #pragma unroll
;         for (int j = 0; j < 8; ++j) ss += (v[j].x * v[j].x + v[j].y * v[j].y) + (v[j].z * v[j].z + v[j].w * v[j].w);
	v_cvt_pk_f32_fp8_e32 v[126:127], v131
	v_cvt_pk_f32_fp8_sdwa v[128:129], v131 src0_sel:WORD_1
	v_pk_add_f32 v[50:51], v[50:51], 0 op_sel_hi:[1,0]
	v_pk_add_f32 v[86:87], v[86:87], 0 op_sel_hi:[1,0]
	v_pk_add_f32 v[96:97], v[96:97], 0 op_sel_hi:[1,0]
	v_pk_fma_f32 v[52:53], v[42:43], v[78:79], v[52:53] op_sel_hi:[0,1,1]
	v_pk_fma_f32 v[54:55], v[42:43], v[84:85], v[54:55] op_sel_hi:[0,1,1]
	v_mov_b32_e32 v43, v46
	v_mov_b32_e32 v130, v98
	v_mov_b32_e32 v131, v100
	v_mov_b32_e32 v100, v99
	v_mov_b32_e32 v98, v102
	v_mov_b32_e32 v99, v104
	v_mov_b32_e32 v104, v103
	v_mov_b32_e32 v102, v106
	v_mov_b32_e32 v103, v108
	v_mov_b32_e32 v108, v107
	v_pk_add_f32 v[50:51], v[50:51], v[92:93]
	v_pk_add_f32 v[82:83], v[86:87], v[82:83]
	v_pk_add_f32 v[86:87], v[96:97], v[88:89]
	v_mov_b32_e32 v92, v119
	v_mov_b32_e32 v96, v121
	v_mov_b32_e32 v119, v124
	v_mov_b32_e32 v121, v125
	v_pk_fma_f32 v[80:81], v[42:43], v[130:131], v[80:81] op_sel_hi:[0,1,1]
	v_pk_fma_f32 v[68:69], v[42:43], v[100:101], v[68:69] op_sel_hi:[0,1,1]
	v_pk_fma_f32 v[66:67], v[42:43], v[98:99], v[66:67] op_sel_hi:[0,1,1]
	v_pk_fma_f32 v[72:73], v[42:43], v[104:105], v[72:73] op_sel_hi:[0,1,1]
	v_pk_fma_f32 v[70:71], v[42:43], v[102:103], v[70:71] op_sel_hi:[0,1,1]
	v_pk_fma_f32 v[76:77], v[42:43], v[108:109], v[76:77] op_sel_hi:[0,1,1]
	v_pk_fma_f32 v[74:75], v[42:43], v[112:113], v[74:75] op_sel_hi:[0,1,1]
	s_waitcnt vmcnt(7)
	v_cvt_pk_f32_fp8_e32 v[98:99], v132
	v_cvt_pk_f32_fp8_sdwa v[100:101], v132 src0_sel:WORD_1
	s_waitcnt vmcnt(6)
	v_cvt_pk_f32_fp8_e32 v[102:103], v133
	v_cvt_pk_f32_fp8_sdwa v[104:105], v133 src0_sel:WORD_1
	s_waitcnt vmcnt(5)
	v_cvt_pk_f32_fp8_e32 v[106:107], v134
	v_cvt_pk_f32_fp8_sdwa v[108:109], v134 src0_sel:WORD_1
	s_waitcnt vmcnt(4)
	v_cvt_pk_f32_fp8_e32 v[112:113], v135
	v_cvt_pk_f32_fp8_sdwa v[124:125], v135 src0_sel:WORD_1
	s_waitcnt vmcnt(3)
	v_cvt_pk_f32_fp8_e32 v[130:131], v136
	v_cvt_pk_f32_fp8_sdwa v[132:133], v136 src0_sel:WORD_1
	s_waitcnt vmcnt(2)
	v_cvt_pk_f32_fp8_e32 v[134:135], v137
	v_cvt_pk_f32_fp8_sdwa v[136:137], v137 src0_sel:WORD_1
	s_waitcnt vmcnt(1)
	v_cvt_pk_f32_fp8_e32 v[138:139], v140
	v_cvt_pk_f32_fp8_sdwa v[140:141], v140 src0_sel:WORD_1
	v_mul_f32_e32 v65, v44, v90
	v_mov_b32_e32 v78, v110
	v_mov_b32_e32 v84, v115
	v_mov_b32_e32 v90, v116
	v_mov_b32_e32 v115, v91
	s_waitcnt vmcnt(0)
	v_cvt_pk_f32_fp8_e32 v[142:143], v144
	v_cvt_pk_f32_fp8_sdwa v[144:145], v144 src0_sel:WORD_1
	v_pk_fma_f32 v[98:99], v[46:47], v[98:99], v[52:53] op_sel_hi:[0,1,1]
	v_mov_b32_e32 v79, v130
	v_mov_b32_e32 v130, v111
	v_mov_b32_e32 v85, v135
	v_mov_b32_e32 v91, v136
	v_mov_b32_e32 v136, v117
	v_mov_b32_e32 v93, v139
	v_mov_b32_e32 v97, v141
	v_mov_b32_e32 v53, v104
	v_mov_b32_e32 v104, v103
	v_mul_f32_e32 v146, v45, v122
	v_pk_fma_f32 v[100:101], v[46:47], v[100:101], v[54:55] op_sel_hi:[0,1,1]
	v_mov_b32_e32 v52, v102
	v_mov_b32_e32 v102, v106
	v_mov_b32_e32 v103, v108
	v_mov_b32_e32 v108, v107
	v_mov_b32_e32 v106, v112
	v_mov_b32_e32 v107, v124
	v_mov_b32_e32 v124, v113
	v_mov_b32_e32 v135, v123
	v_pk_mul_f32 v[78:79], v[42:43], v[78:79]
	v_pk_mul_f32 v[112:113], v[42:43], v[130:131]
	v_pk_mul_f32 v[84:85], v[42:43], v[84:85]
	v_pk_mul_f32 v[90:91], v[42:43], v[90:91]
	v_pk_mul_f32 v[122:123], v[42:43], v[136:137]
	v_pk_mul_f32 v[92:93], v[42:43], v[92:93]
	v_pk_mul_f32 v[96:97], v[42:43], v[96:97]
	v_pk_fma_f32 v[68:69], v[46:47], v[104:105], v[68:69] op_sel_hi:[0,1,1]
	v_mov_b32_e32 v43, v44
	v_pk_fma_f32 v[54:55], v[46:47], v[132:133], v[74:75] op_sel_hi:[0,1,1]
	v_mul_f32_e32 v8, v101, v101
	v_pk_fma_f32 v[80:81], v[46:47], v[52:53], v[80:81] op_sel_hi:[0,1,1]
	v_pk_fma_f32 v[66:67], v[46:47], v[102:103], v[66:67] op_sel_hi:[0,1,1]
	v_pk_fma_f32 v[72:73], v[46:47], v[108:109], v[72:73] op_sel_hi:[0,1,1]
	v_pk_fma_f32 v[70:71], v[46:47], v[106:107], v[70:71] op_sel_hi:[0,1,1]
	v_pk_fma_f32 v[76:77], v[46:47], v[124:125], v[76:77] op_sel_hi:[0,1,1]
	v_mov_b32_e32 v47, v45
	v_mul_f32_e32 v44, v99, v99
	v_mov_b32_e32 v52, v78
	v_mov_b32_e32 v53, v112
	v_mov_b32_e32 v112, v79
	v_mov_b32_e32 v78, v84
	v_mov_b32_e32 v79, v90
	v_pk_mul_f32 v[102:103], v[68:69], v[68:69]
	v_pk_fma_f32 v[32:33], v[42:43], v[114:115], v[32:33]
	v_mov_b32_e32 v43, v45
	v_mov_b32_e32 v139, v128
	v_mov_b32_e32 v141, v129
	v_mov_b32_e32 v90, v85
	v_mov_b32_e32 v84, v92
	v_mov_b32_e32 v85, v96
	v_mov_b32_e32 v96, v93
	v_pk_fma_f32 v[92:93], v[100:101], v[100:101], v[8:9] op_sel_hi:[1,1,0]
	v_pk_mul_f32 v[104:105], v[72:73], v[72:73]
	v_pk_fma_f32 v[44:45], v[98:99], v[98:99], v[44:45] op_sel_hi:[1,1,0]
	v_pk_add_f32 v[50:51], v[50:51], v[52:53]
	v_pk_add_f32 v[52:53], v[82:83], v[78:79]
	v_pk_fma_f32 v[82:83], v[80:81], v[80:81], v[102:103]
	v_pk_fma_f32 v[94:95], v[42:43], v[118:119], v[94:95]
	v_pk_fma_f32 v[40:41], v[42:43], v[120:121], v[40:41]
	v_pk_fma_f32 v[102:103], v[46:47], v[134:135], v[32:33]
	v_mov_b32_e32 v47, v42
	v_mul_f32_e32 v48, v46, v142
	v_mul_f32_e32 v111, v46, v144
	v_mul_f32_e32 v117, v46, v145
	v_pk_mul_f32 v[106:107], v[76:77], v[76:77]
	v_pk_add_f32 v[78:79], v[86:87], v[84:85]
	v_pk_fma_f32 v[84:85], v[66:67], v[66:67], v[104:105]
	v_mov_b32_e32 v45, v65
	v_mov_b32_e32 v93, v9
	v_pk_add_f32 v[104:105], v[50:51], v[112:113]
	v_pk_add_f32 v[90:91], v[52:53], v[90:91]
	v_pk_fma_f32 v[52:53], v[46:47], v[138:139], v[94:95]
	v_pk_fma_f32 v[46:47], v[46:47], v[140:141], v[40:41]
	v_pk_add_f32 v[40:41], v[82:83], v[82:83] op_sel:[0,1] op_sel_hi:[1,0]
	v_mul_f32_e32 v89, v42, v127
	v_mul_f32_e32 v34, v55, v55
	v_add_f32_e32 v74, v147, v122
	v_pk_fma_f32 v[86:87], v[70:71], v[70:71], v[106:107]
	v_pk_add_f32 v[50:51], v[78:79], v[96:97]
; __device__ __forceinline__ f32x4 ld_bf4(const bf16_t* p) { const u32x2 w = *(const u32x2*)p; return (f32x4){__builtin_bit_cast(float, w.x << 16), __builtin_bit_cast(float, w.x & 0xffff0000u), __builtin_bit_cast(float, w.y << 16), __builtin_bit_cast(float, w.y & 0xffff0000u)}; }
; __device__ __forceinline__ void p11_final(Frame& F) {
;     ...
;         float ss = 0.f;
; #pragma unroll
;         for (int j = 0; j < 8; ++j) ss += (v[j].x * v[j].x + v[j].y * v[j].y) + (v[j].z * v[j].z + v[j].w * v[j].w);
;         const float rstd = __builtin_amdgcn_rsqf(wave_sum(ss) * (1.0f / D) + RMS_EPS);
; #pragma unroll
;         for (int j = 0; j < 8; ++j) { const int c = 4 * F.lane + 256 * j;
;             const f32x4 xv = ld_bf4(X1 + (size_t)row * D + c), g = *(const f32x4*)(IN_NORMG + 3 * D + c), gt = *(const f32x4*)(mr + 5 * D + c);
;             *(f32x4*)(F.out + (size_t)row * D + c) = xv + gt * (v[j] * rstd * g); }
	v_pk_add_f32 v[32:33], v[44:45], v[92:93]
	v_mov_b32_e32 v88, v102
	v_mov_b32_e32 v41, v146
	v_pk_mov_b32 v[94:95], v[104:105], v[42:43] op_sel:[1,0]
	v_pk_mov_b32 v[96:97], v[104:105], v[126:127] op_sel:[1,0]
	v_pk_fma_f32 v[108:109], v[54:55], v[54:55], v[34:35] op_sel_hi:[1,1,0]
	v_add_f32_e32 v34, v74, v123
	v_pk_add_f32 v[78:79], v[84:85], v[84:85] op_sel:[0,1] op_sel_hi:[1,0]
	v_pk_add_f32 v[44:45], v[86:87], v[86:87] op_sel:[0,1] op_sel_hi:[1,0]
	v_pk_mul_f32 v[82:83], v[102:103], v[102:103]
	v_pk_mul_f32 v[84:85], v[104:105], v[104:105]
	v_pk_mul_f32 v[86:87], v[90:91], v[90:91]
	v_pk_add_f32 v[88:89], v[102:103], v[88:89]
	v_mov_b32_e32 v110, v52
	v_pk_add_f32 v[106:107], v[32:33], v[40:41]
	v_pk_mul_f32 v[42:43], v[94:95], v[96:97]
	v_mov_b32_e32 v75, v143
	v_mov_b32_e32 v109, v48
	v_mov_b32_e32 v74, v34
	v_pk_mul_f32 v[92:93], v[50:51], v[50:51]
	v_mov_b32_e32 v45, v48
	v_mov_b32_e32 v48, v90
	v_mov_b32_e32 v142, v90
	v_mov_b32_e32 v83, v89
	v_mov_b32_e32 v88, v87
	v_pk_add_f32 v[40:41], v[52:53], v[110:111]
	v_mov_b32_e32 v79, v43
	v_mov_b32_e32 v85, v107
	v_mov_b32_e32 v116, v46
	v_pk_fma_f32 v[86:87], v[52:53], v[52:53], v[92:93]
	v_pk_fma_f32 v[42:43], v[48:49], v[142:143], v[82:83]
	v_pk_fma_f32 v[48:49], v[34:35], v[74:75], v[88:89]
	v_pk_mul_f32 v[74:75], v[40:41], v[40:41]
	v_pk_add_f32 v[78:79], v[106:107], v[78:79]
	v_pk_fma_f32 v[84:85], v[94:95], v[96:97], v[84:85]
	v_pk_add_f32 v[32:33], v[46:47], v[116:117]
	v_mov_b32_e32 v87, v75
	v_pk_add_f32 v[44:45], v[78:79], v[44:45]
	v_pk_add_f32 v[74:75], v[84:85], v[108:109]
	v_pk_fma_f32 v[92:93], v[46:47], v[46:47], v[92:93] op_sel:[0,0,1] op_sel_hi:[1,1,0]
	v_pk_mul_f32 v[82:83], v[32:33], v[32:33]
	v_pk_add_f32 v[88:89], v[42:43], v[48:49]
	v_pk_mul_f32 v[48:49], v[42:43], v[48:49]
	v_pk_add_f32 v[78:79], v[44:45], v[74:75]
	v_pk_mul_f32 v[74:75], v[44:45], v[74:75]
	v_mov_b32_e32 v93, v83
	v_mov_b32_e32 v89, v49
	v_mov_b32_e32 v79, v75
	v_pk_add_f32 v[48:49], v[86:87], v[92:93]
	v_pk_add_f32 v[74:75], v[78:79], v[88:89]
	v_mov_b32_e32 v35, v34
	v_pk_add_f32 v[48:49], v[74:75], v[48:49]
	v_mov_b32_e32 v34, v91
	v_add_f32_e32 v8, v48, v49
	v_mov_b32_e32 v103, v90
	v_mov_b32_e32 v47, v51
	v_add_f32_dpp v8, v8, v8 quad_perm:[1,0,3,2] row_mask:0xf bank_mask:0xf bound_ctrl:1
	v_mov_b32_e32 v53, v50
	v_mov_b32_e32 v32, v41
	v_add_f32_dpp v8, v8, v8 quad_perm:[2,3,0,1] row_mask:0xf bank_mask:0xf bound_ctrl:1
	v_mov_b32_e32 v42, v45
	s_nop 0
	v_add_f32_dpp v8, v8, v8 row_ror:4 row_mask:0xf bank_mask:0xf bound_ctrl:1
	s_nop 1
	v_add_f32_dpp v8, v8, v8 row_ror:8 row_mask:0xf bank_mask:0xf bound_ctrl:1
	s_nop 0
	v_readlane_b32 s3, v8, 16
	v_readlane_b32 s5, v8, 48
	v_readlane_b32 s22, v8, 0
	v_readlane_b32 s23, v8, 32
	v_mov_b32_e32 v48, s3
	v_mov_b32_e32 v49, s5
	v_pk_add_f32 v[48:49], s[22:23], v[48:49]
	s_nop 0
	v_add_f32_e32 v8, v48, v49
	v_fmamk_f32 v8, v8, 0x3a000000, v56
	v_rsq_f32_e32 v8, v8
	s_nop 0
	v_pk_mul_f32 v[48:49], v[100:101], v[8:9] op_sel_hi:[1,0]
	v_pk_mul_f32 v[74:75], v[98:99], v[8:9] op_sel_hi:[1,0]
	v_pk_mul_f32 v[2:3], v[2:3], v[48:49]
	v_pk_mul_f32 v[0:1], v[0:1], v[74:75]
	v_pk_fma_f32 v[2:3], v[6:7], v[2:3], v[38:39]
	v_pk_fma_f32 v[0:1], v[4:5], v[0:1], v[36:37]
	global_store_dwordx4 v[30:31], v[0:3], off offset:-4096
	v_mov_b32_e32 v38, v81
	v_mov_b32_e32 v39, v69
	v_mov_b32_e32 v81, v68
	v_pk_mul_f32 v[38:39], v[38:39], v[8:9] op_sel_hi:[1,0]
	v_pk_mul_f32 v[48:49], v[80:81], v[8:9] op_sel_hi:[1,0]
	v_pk_mul_f32 v[34:35], v[34:35], v[8:9] op_sel_hi:[1,0]
	v_pk_mul_f32 v[32:33], v[32:33], v[8:9] op_sel_hi:[1,0]
; __device__ __forceinline__ f32x4 ld_bf4(const bf16_t* p) { const u32x2 w = *(const u32x2*)p; return (f32x4){__builtin_bit_cast(float, w.x << 16), __builtin_bit_cast(float, w.x & 0xffff0000u), __builtin_bit_cast(float, w.y << 16), __builtin_bit_cast(float, w.y & 0xffff0000u)}; }
; __device__ __forceinline__ void p11_final(Frame& F) {
;     ...
; #pragma unroll
;         for (int j = 0; j < 8; ++j) { const int c = 4 * F.lane + 256 * j;
;             const f32x4 xv = ld_bf4(X1 + (size_t)row * D + c), g = *(const f32x4*)(IN_NORMG + 3 * D + c), gt = *(const f32x4*)(mr + 5 * D + c);
;             *(f32x4*)(F.out + (size_t)row * D + c) = xv + gt * (v[j] * rstd * g); }
	v_lshlrev_b32_e32 v68, 16, v180
	v_and_b32_e32 v69, 0xffff0000, v180
	v_lshlrev_b32_e32 v36, 16, v181
	v_and_b32_e32 v37, 0xffff0000, v181
	v_pk_mul_f32 v[0:1], v[48:49], v[152:153]
	v_pk_mul_f32 v[2:3], v[38:39], v[154:155]
	v_pk_fma_f32 v[0:1], v[196:197], v[0:1], v[68:69]
	v_pk_fma_f32 v[2:3], v[198:199], v[2:3], v[36:37]
	global_store_dwordx4 v[30:31], v[0:3], off offset:-3072
	v_mov_b32_e32 v38, v67
	v_mov_b32_e32 v39, v73
	v_mov_b32_e32 v67, v72
	v_pk_mul_f32 v[38:39], v[38:39], v[8:9] op_sel_hi:[1,0]
	v_pk_mul_f32 v[48:49], v[66:67], v[8:9] op_sel_hi:[1,0]
	v_lshlrev_b32_e32 v66, 16, v182
	v_and_b32_e32 v67, 0xffff0000, v182
	v_lshlrev_b32_e32 v36, 16, v183
	v_and_b32_e32 v37, 0xffff0000, v183
	v_pk_mul_f32 v[0:1], v[48:49], v[156:157]
	v_pk_mul_f32 v[2:3], v[38:39], v[158:159]
	v_pk_fma_f32 v[0:1], v[200:201], v[0:1], v[66:67]
	v_pk_fma_f32 v[2:3], v[202:203], v[2:3], v[36:37]
	global_store_dwordx4 v[30:31], v[0:3], off offset:-2048
	v_mov_b32_e32 v38, v71
	v_mov_b32_e32 v39, v77
	v_mov_b32_e32 v71, v76
	v_pk_mul_f32 v[38:39], v[38:39], v[8:9] op_sel_hi:[1,0]
	v_pk_mul_f32 v[48:49], v[70:71], v[8:9] op_sel_hi:[1,0]
	v_lshlrev_b32_e32 v66, 16, v184
	v_and_b32_e32 v67, 0xffff0000, v184
	v_lshlrev_b32_e32 v36, 16, v185
	v_and_b32_e32 v37, 0xffff0000, v185
	v_pk_mul_f32 v[0:1], v[48:49], v[160:161]
	v_pk_mul_f32 v[2:3], v[38:39], v[162:163]
	v_pk_fma_f32 v[0:1], v[204:205], v[0:1], v[66:67]
	v_pk_fma_f32 v[2:3], v[206:207], v[2:3], v[36:37]
	global_store_dwordx4 v[30:31], v[0:3], off offset:-1024
	v_pk_mul_f32 v[38:39], v[54:55], v[8:9] op_sel_hi:[1,0]
	v_pk_mul_f32 v[48:49], v[104:105], v[8:9] op_sel_hi:[1,0]
	v_lshlrev_b32_e32 v54, 16, v186
	v_and_b32_e32 v55, 0xffff0000, v186
	v_lshlrev_b32_e32 v36, 16, v187
	v_and_b32_e32 v37, 0xffff0000, v187
	v_pk_mul_f32 v[0:1], v[48:49], v[164:165]
	v_pk_mul_f32 v[2:3], v[38:39], v[166:167]
	v_pk_fma_f32 v[0:1], v[208:209], v[0:1], v[54:55]
	v_pk_fma_f32 v[2:3], v[210:211], v[2:3], v[36:37]
	global_store_dwordx4 v[30:31], v[0:3], off
	v_pk_mul_f32 v[38:39], v[102:103], v[8:9] op_sel_hi:[1,0]
	v_lshlrev_b32_e32 v48, 16, v188
	v_and_b32_e32 v49, 0xffff0000, v188
	v_lshlrev_b32_e32 v36, 16, v189
	v_and_b32_e32 v37, 0xffff0000, v189
	v_pk_mul_f32 v[0:1], v[38:39], v[168:169]
	v_pk_mul_f32 v[2:3], v[34:35], v[170:171]
	v_pk_fma_f32 v[0:1], v[212:213], v[0:1], v[48:49]
	v_pk_fma_f32 v[2:3], v[214:215], v[2:3], v[36:37]
	global_store_dwordx4 v[30:31], v[0:3], off offset:1024
	v_pk_mul_f32 v[36:37], v[46:47], v[8:9] op_sel_hi:[1,0]
	v_pk_mul_f32 v[38:39], v[52:53], v[8:9] op_sel_hi:[1,0]
	v_lshlrev_b32_e32 v46, 16, v190
	v_and_b32_e32 v47, 0xffff0000, v190
	v_lshlrev_b32_e32 v34, 16, v191
	v_and_b32_e32 v35, 0xffff0000, v191
	v_pk_mul_f32 v[0:1], v[38:39], v[172:173]
	v_pk_mul_f32 v[2:3], v[36:37], v[174:175]
	v_pk_fma_f32 v[0:1], v[216:217], v[0:1], v[46:47]
	v_pk_fma_f32 v[2:3], v[218:219], v[2:3], v[34:35]
	global_store_dwordx4 v[30:31], v[0:3], off offset:2048
	v_pk_mul_f32 v[36:37], v[42:43], v[8:9] op_sel_hi:[1,0]
	v_lshl_add_u64 v[28:29], v[28:29], 0, s[6:7]
	v_lshlrev_b32_e32 v38, 16, v192
	v_and_b32_e32 v39, 0xffff0000, v192
	v_lshlrev_b32_e32 v34, 16, v193
	v_and_b32_e32 v35, 0xffff0000, v193
	v_pk_mul_f32 v[0:1], v[36:37], v[176:177]
	v_pk_mul_f32 v[2:3], v[32:33], v[178:179]
	v_pk_fma_f32 v[0:1], v[220:221], v[0:1], v[38:39]
	v_pk_fma_f32 v[2:3], v[222:223], v[2:3], v[34:35]
	global_store_dwordx4 v[30:31], v[0:3], off offset:3072
	v_lshl_add_u64 v[30:31], v[30:31], 0, s[8:9]
	s_cbranch_scc1 .LBB0_1215

; #define LAS __attribute__((address_space(3)))
; __global__ void __launch_bounds__(NTHR, 2) fwd_kernel(Args args) {
;     extern __shared__ __attribute__((aligned(16))) unsigned char lds_raw[];
;     Frame F;
;     F.lds = (LAS unsigned char*)lds_raw;
;     F.tid = threadIdx.x; F.lane = F.tid & 63; F.wave = __builtin_amdgcn_readfirstlane(F.tid >> 6);
;     F.G = gridDim.x; F.bx = blockIdx.x;
; #pragma unroll
;     for (int i = 0; i < 27; ++i) F.in[i] = args.in[i];
;     F.out = args.out; F.ws = args.ws;
	.amdhsa_kernel _Z10fwd_kernel4Args
		.amdhsa_group_segment_fixed_size 0
		.amdhsa_private_segment_fixed_size 0
		.amdhsa_kernarg_size 496
		.amdhsa_user_sgpr_count 2
		.amdhsa_user_sgpr_dispatch_ptr 0
		.amdhsa_user_sgpr_queue_ptr 0
		.amdhsa_user_sgpr_kernarg_segment_ptr 1
		.amdhsa_user_sgpr_dispatch_id 0
		.amdhsa_user_sgpr_kernarg_preload_length 0
		.amdhsa_user_sgpr_kernarg_preload_offset 0
		.amdhsa_user_sgpr_private_segment_size 0
		.amdhsa_uses_dynamic_stack 0
		.amdhsa_enable_private_segment 0
		.amdhsa_system_sgpr_workgroup_id_x 1
		.amdhsa_system_sgpr_workgroup_id_y 0
		.amdhsa_system_sgpr_workgroup_id_z 0
		.amdhsa_system_sgpr_workgroup_info 0
		.amdhsa_system_vgpr_workitem_id 0
		.amdhsa_next_free_vgpr 255
		.amdhsa_next_free_sgpr 102
		.amdhsa_accum_offset 256
		.amdhsa_reserve_vcc 1
		.amdhsa_float_round_mode_32 0
		.amdhsa_float_round_mode_16_64 0
		.amdhsa_float_denorm_mode_32 3
		.amdhsa_float_denorm_mode_16_64 3
		.amdhsa_dx10_clamp 1
		.amdhsa_ieee_mode 1
		.amdhsa_fp16_overflow 0
		.amdhsa_tg_split 0
		.amdhsa_exception_fp_ieee_invalid_op 0
		.amdhsa_exception_fp_denorm_src 0
		.amdhsa_exception_fp_ieee_div_zero 0
		.amdhsa_exception_fp_ieee_overflow 0
		.amdhsa_exception_fp_ieee_underflow 0
		.amdhsa_exception_fp_ieee_inexact 0
		.amdhsa_exception_int_div_zero 0
	.end_amdhsa_kernel

; #define LAS __attribute__((address_space(3)))
; __global__ void __launch_bounds__(NTHR, 2) fwd_kernel(Args args) {
;     extern __shared__ __attribute__((aligned(16))) unsigned char lds_raw[];
;     Frame F;
;     F.lds = (LAS unsigned char*)lds_raw;
;     F.tid = threadIdx.x; F.lane = F.tid & 63; F.wave = __builtin_amdgcn_readfirstlane(F.tid >> 6);
;     F.G = gridDim.x; F.bx = blockIdx.x;
; #pragma unroll
;     for (int i = 0; i < 27; ++i) F.in[i] = args.in[i];
;     F.out = args.out; F.ws = args.ws;
amdhsa.kernels:
  - .agpr_count:     0
    .args:
      - .offset:         0
        .size:           240
        .value_kind:     by_value
      - .offset:         240
        .size:           4
        .value_kind:     hidden_block_count_x
      - .offset:         244
        .size:           4
        .value_kind:     hidden_block_count_y
      - .offset:         248
        .size:           4
        .value_kind:     hidden_block_count_z
      - .offset:         252
        .size:           2
        .value_kind:     hidden_group_size_x
      - .offset:         254
        .size:           2
        .value_kind:     hidden_group_size_y
      - .offset:         256
        .size:           2
        .value_kind:     hidden_group_size_z
      - .offset:         258
        .size:           2
        .value_kind:     hidden_remainder_x
      - .offset:         260
        .size:           2
        .value_kind:     hidden_remainder_y
      - .offset:         262
        .size:           2
        .value_kind:     hidden_remainder_z
      - .offset:         280
        .size:           8
        .value_kind:     hidden_global_offset_x
      - .offset:         288
        .size:           8
        .value_kind:     hidden_global_offset_y
      - .offset:         296
        .size:           8
        .value_kind:     hidden_global_offset_z
      - .offset:         304
        .size:           2
        .value_kind:     hidden_grid_dims
      - .offset:         360
        .size:           4
        .value_kind:     hidden_dynamic_lds_size
    .group_segment_fixed_size: 0
    .kernarg_segment_align: 8
    .kernarg_segment_size: 496
    .language:       OpenCL C
    .language_version:
      - 2
      - 0
    .max_flat_workgroup_size: 512
    .name:           _Z10fwd_kernel4Args
    .private_segment_fixed_size: 0
    .sgpr_count:     108
    .sgpr_spill_count: 44
    .symbol:         _Z10fwd_kernel4Args.kd
    .uniform_work_group_size: 1
    .uses_dynamic_stack: false
    .vgpr_count:     255
    .vgpr_spill_count: 0
    .wavefront_size: 64
